# GEMM loops: redundant post-barrier lgkmcnt(0) removed (66 sites)
# speedup vs baseline: 1.0033x; 1.0033x over previous
.LBB0_236:
	ds_read_b128 v[154:157], v151
	ds_read_b128 v[158:161], v151 offset:1024
	ds_read_b128 v[162:165], v151 offset:2048
	ds_read_b128 v[166:169], v151 offset:3072
	ds_read_b128 v[172:175], v152
	ds_read_b128 v[176:179], v152 offset:1024
	ds_read_b128 v[180:183], v152 offset:2048
	ds_read_b128 v[184:187], v152 offset:3072
	s_add_u32 s29, s22, 0xfffc0080
	s_addc_u32 s40, s23, -1
	s_cmp_eq_u32 s28, 12
	s_cselect_b32 s43, s15, s40
	s_cselect_b32 s42, s56, s29
	s_cselect_b32 s41, s13, s59
	s_cselect_b32 s40, s57, s58
	v_lshl_add_u64 v[148:149], s[22:23], 0, v[140:141]
	s_add_i32 m0, s21, 0xc000
	ds_read_b128 v[188:191], v153
	ds_read_b128 v[192:195], v153 offset:1024
	ds_read_b128 v[196:199], v153 offset:2048
	ds_read_b128 v[200:203], v153 offset:3072
	ds_read_b128 v[204:207], v153 offset:4096
	ds_read_b128 v[208:211], v153 offset:5120
	ds_read_b128 v[212:215], v153 offset:6144
	ds_read_b128 v[216:219], v153 offset:7168
	global_load_lds_dwordx4 v[148:149], off
	v_lshl_add_u64 v[148:149], s[22:23], 0, v[142:143]
	s_add_i32 m0, s21, 0xe000
	s_nop 0
	global_load_lds_dwordx4 v[148:149], off
	s_waitcnt vmcnt(8)
	s_waitcnt lgkmcnt(0)
	s_barrier
	s_setprio 1
	v_mfma_f32_16x16x32_bf16 v[126:129], v[154:157], v[188:191], v[126:129]
	v_mfma_f32_16x16x32_bf16 v[122:125], v[162:165], v[188:191], v[122:125]
	v_mfma_f32_16x16x32_bf16 v[118:121], v[154:157], v[196:199], v[118:121]
	v_mfma_f32_16x16x32_bf16 v[110:113], v[162:165], v[196:199], v[110:113]
	v_mfma_f32_16x16x32_bf16 v[102:105], v[154:157], v[204:207], v[102:105]
	v_mfma_f32_16x16x32_bf16 v[94:97], v[162:165], v[204:207], v[94:97]
	v_mfma_f32_16x16x32_bf16 v[86:89], v[154:157], v[212:215], v[86:89]
	v_mfma_f32_16x16x32_bf16 v[78:81], v[162:165], v[212:215], v[78:81]
	v_mfma_f32_16x16x32_bf16 v[126:129], v[158:161], v[192:195], v[126:129]
	v_mfma_f32_16x16x32_bf16 v[122:125], v[166:169], v[192:195], v[122:125]
	v_mfma_f32_16x16x32_bf16 v[118:121], v[158:161], v[200:203], v[118:121]
	v_mfma_f32_16x16x32_bf16 v[110:113], v[166:169], v[200:203], v[110:113]
	v_mfma_f32_16x16x32_bf16 v[102:105], v[158:161], v[208:211], v[102:105]
	v_mfma_f32_16x16x32_bf16 v[94:97], v[166:169], v[208:211], v[94:97]
	v_mfma_f32_16x16x32_bf16 v[86:89], v[158:161], v[216:219], v[86:89]
	v_mfma_f32_16x16x32_bf16 v[78:81], v[166:169], v[216:219], v[78:81]
	s_setprio 0
	s_setprio 1
	v_mfma_f32_16x16x32_bf16 v[114:117], v[172:175], v[188:191], v[114:117]
	v_mfma_f32_16x16x32_bf16 v[106:109], v[180:183], v[188:191], v[106:109]
	v_mfma_f32_16x16x32_bf16 v[98:101], v[172:175], v[196:199], v[98:101]
	v_mfma_f32_16x16x32_bf16 v[90:93], v[180:183], v[196:199], v[90:93]
	v_mfma_f32_16x16x32_bf16 v[82:85], v[172:175], v[204:207], v[82:85]
	v_mfma_f32_16x16x32_bf16 v[74:77], v[180:183], v[204:207], v[74:77]
	v_mfma_f32_16x16x32_bf16 v[70:73], v[172:175], v[212:215], v[70:73]
	v_mfma_f32_16x16x32_bf16 v[66:69], v[180:183], v[212:215], v[66:69]
	v_mfma_f32_16x16x32_bf16 v[114:117], v[176:179], v[192:195], v[114:117]
	v_mfma_f32_16x16x32_bf16 v[106:109], v[184:187], v[192:195], v[106:109]
	v_mfma_f32_16x16x32_bf16 v[98:101], v[176:179], v[200:203], v[98:101]
	v_mfma_f32_16x16x32_bf16 v[90:93], v[184:187], v[200:203], v[90:93]
	v_mfma_f32_16x16x32_bf16 v[82:85], v[176:179], v[208:211], v[82:85]
	v_mfma_f32_16x16x32_bf16 v[74:77], v[184:187], v[208:211], v[74:77]
	v_mfma_f32_16x16x32_bf16 v[70:73], v[176:179], v[216:219], v[70:73]
	v_mfma_f32_16x16x32_bf16 v[66:69], v[184:187], v[216:219], v[66:69]
	s_setprio 0
	s_barrier
	s_add_i32 s29, s53, s31
	v_lshl_add_u64 v[148:149], s[40:41], 0, v[134:135]
	s_mov_b32 m0, s29
	ds_read_b128 v[188:191], v153 offset:16384
	ds_read_b128 v[192:195], v153 offset:17408
	ds_read_b128 v[196:199], v153 offset:18432
	ds_read_b128 v[200:203], v153 offset:19456
	ds_read_b128 v[204:207], v153 offset:20480
	ds_read_b128 v[208:211], v153 offset:21504
	ds_read_b128 v[212:215], v153 offset:22528
	ds_read_b128 v[216:219], v153 offset:23552
	global_load_lds_dwordx4 v[148:149], off
	s_add_i32 m0, s29, 0x2000
	s_add_u32 s60, s40, 0x4000
	v_lshl_add_u64 v[148:149], s[40:41], 0, v[130:131]
	s_addc_u32 s61, s41, 0
	s_add_i32 s29, s54, s31
	global_load_lds_dwordx4 v[148:149], off
	v_lshl_add_u64 v[148:149], s[60:61], 0, v[134:135]
	s_mov_b32 m0, s29
	v_lshl_add_u64 v[220:221], s[42:43], 0, v[132:133]
	global_load_lds_dwordx4 v[148:149], off
	v_lshl_add_u64 v[148:149], s[60:61], 0, v[130:131]
	s_add_i32 m0, s29, 0x2000
	s_nop 0
	global_load_lds_dwordx4 v[148:149], off
	v_lshl_add_u64 v[148:149], s[42:43], 0, v[136:137]
	s_mov_b32 m0, s21
	s_nop 0
	global_load_lds_dwordx4 v[148:149], off
	s_mov_b32 m0, s36
	s_nop 0
	global_load_lds_dwordx4 v[220:221], off
	s_waitcnt vmcnt(8)
	s_waitcnt lgkmcnt(0)
	s_barrier
	s_setprio 1
	v_mfma_f32_16x16x32_bf16 v[62:65], v[154:157], v[188:191], v[62:65]
	v_mfma_f32_16x16x32_bf16 v[58:61], v[162:165], v[188:191], v[58:61]
	v_mfma_f32_16x16x32_bf16 v[50:53], v[154:157], v[196:199], v[50:53]
	v_mfma_f32_16x16x32_bf16 v[42:45], v[162:165], v[196:199], v[42:45]
	v_mfma_f32_16x16x32_bf16 v[34:37], v[154:157], v[204:207], v[34:37]
	v_mfma_f32_16x16x32_bf16 v[26:29], v[162:165], v[204:207], v[26:29]
	v_mfma_f32_16x16x32_bf16 v[18:21], v[154:157], v[212:215], v[18:21]
	v_mfma_f32_16x16x32_bf16 v[10:13], v[162:165], v[212:215], v[10:13]
	v_mfma_f32_16x16x32_bf16 v[62:65], v[158:161], v[192:195], v[62:65]
	v_mfma_f32_16x16x32_bf16 v[58:61], v[166:169], v[192:195], v[58:61]
	v_mfma_f32_16x16x32_bf16 v[50:53], v[158:161], v[200:203], v[50:53]
	v_mfma_f32_16x16x32_bf16 v[42:45], v[166:169], v[200:203], v[42:45]
	v_mfma_f32_16x16x32_bf16 v[34:37], v[158:161], v[208:211], v[34:37]
	v_mfma_f32_16x16x32_bf16 v[26:29], v[166:169], v[208:211], v[26:29]
	v_mfma_f32_16x16x32_bf16 v[18:21], v[158:161], v[216:219], v[18:21]
	v_mfma_f32_16x16x32_bf16 v[10:13], v[166:169], v[216:219], v[10:13]
	s_setprio 0
	s_setprio 1
	v_mfma_f32_16x16x32_bf16 v[54:57], v[172:175], v[188:191], v[54:57]
	v_mfma_f32_16x16x32_bf16 v[46:49], v[180:183], v[188:191], v[46:49]
	v_mfma_f32_16x16x32_bf16 v[38:41], v[172:175], v[196:199], v[38:41]
	v_mfma_f32_16x16x32_bf16 v[30:33], v[180:183], v[196:199], v[30:33]
	v_mfma_f32_16x16x32_bf16 v[22:25], v[172:175], v[204:207], v[22:25]
	v_mfma_f32_16x16x32_bf16 v[14:17], v[180:183], v[204:207], v[14:17]
	v_mfma_f32_16x16x32_bf16 v[6:9], v[172:175], v[212:215], v[6:9]
	v_mfma_f32_16x16x32_bf16 v[2:5], v[180:183], v[212:215], v[2:5]
	v_mfma_f32_16x16x32_bf16 v[54:57], v[176:179], v[192:195], v[54:57]
	v_mfma_f32_16x16x32_bf16 v[46:49], v[184:187], v[192:195], v[46:49]
	v_mfma_f32_16x16x32_bf16 v[38:41], v[176:179], v[200:203], v[38:41]
	v_mfma_f32_16x16x32_bf16 v[30:33], v[184:187], v[200:203], v[30:33]
	v_mfma_f32_16x16x32_bf16 v[22:25], v[176:179], v[208:211], v[22:25]
	v_mfma_f32_16x16x32_bf16 v[14:17], v[184:187], v[208:211], v[14:17]
	v_mfma_f32_16x16x32_bf16 v[6:9], v[176:179], v[216:219], v[6:9]
	v_mfma_f32_16x16x32_bf16 v[2:5], v[184:187], v[216:219], v[2:5]
	s_setprio 0
	s_barrier
	s_add_i32 s29, 0, 0x18000
	s_add_i32 s60, 0, 0x1c000
	v_add_u32_e32 v166, s29, v150
	v_add_u32_e32 v171, s60, v150
	ds_read_b128 v[154:157], v166
	ds_read_b128 v[158:161], v166 offset:1024
	ds_read_b128 v[162:165], v166 offset:2048
	ds_read_b128 v[166:169], v166 offset:3072
	ds_read_b128 v[172:175], v171
	ds_read_b128 v[176:179], v171 offset:1024
	ds_read_b128 v[180:183], v171 offset:2048
	ds_read_b128 v[184:187], v171 offset:3072
	s_add_u32 s42, s42, 0x40000
	s_addc_u32 s43, s43, 0
	s_mov_b32 m0, s37
	v_lshl_add_u64 v[222:223], s[42:43], 0, v[136:137]
	ds_read_b128 v[188:191], v153 offset:32768
	ds_read_b128 v[192:195], v153 offset:33792
	ds_read_b128 v[196:199], v153 offset:34816
	ds_read_b128 v[200:203], v153 offset:35840
	ds_read_b128 v[204:207], v153 offset:36864
	ds_read_b128 v[208:211], v153 offset:37888
	ds_read_b128 v[212:215], v153 offset:38912
	ds_read_b128 v[216:219], v153 offset:39936
	global_load_lds_dwordx4 v[222:223], off
	v_lshl_add_u64 v[222:223], s[42:43], 0, v[132:133]
	s_mov_b32 m0, s44
	s_nop 0
	global_load_lds_dwordx4 v[222:223], off
	s_waitcnt vmcnt(8)
	s_waitcnt lgkmcnt(0)
	s_barrier
	s_setprio 1
	v_mfma_f32_16x16x32_bf16 v[126:129], v[154:157], v[188:191], v[126:129]
	v_mfma_f32_16x16x32_bf16 v[122:125], v[162:165], v[188:191], v[122:125]
	v_mfma_f32_16x16x32_bf16 v[118:121], v[154:157], v[196:199], v[118:121]
	v_mfma_f32_16x16x32_bf16 v[110:113], v[162:165], v[196:199], v[110:113]
	v_mfma_f32_16x16x32_bf16 v[102:105], v[154:157], v[204:207], v[102:105]
	v_mfma_f32_16x16x32_bf16 v[94:97], v[162:165], v[204:207], v[94:97]
	v_mfma_f32_16x16x32_bf16 v[86:89], v[154:157], v[212:215], v[86:89]
	v_mfma_f32_16x16x32_bf16 v[78:81], v[162:165], v[212:215], v[78:81]
	v_mfma_f32_16x16x32_bf16 v[126:129], v[158:161], v[192:195], v[126:129]
	v_mfma_f32_16x16x32_bf16 v[122:125], v[166:169], v[192:195], v[122:125]
	v_mfma_f32_16x16x32_bf16 v[118:121], v[158:161], v[200:203], v[118:121]
	v_mfma_f32_16x16x32_bf16 v[110:113], v[166:169], v[200:203], v[110:113]
	v_mfma_f32_16x16x32_bf16 v[102:105], v[158:161], v[208:211], v[102:105]
	v_mfma_f32_16x16x32_bf16 v[94:97], v[166:169], v[208:211], v[94:97]
	v_mfma_f32_16x16x32_bf16 v[86:89], v[158:161], v[216:219], v[86:89]
	v_mfma_f32_16x16x32_bf16 v[78:81], v[166:169], v[216:219], v[78:81]
	s_setprio 0
	s_setprio 1
	v_mfma_f32_16x16x32_bf16 v[114:117], v[172:175], v[188:191], v[114:117]
	v_mfma_f32_16x16x32_bf16 v[106:109], v[180:183], v[188:191], v[106:109]
	v_mfma_f32_16x16x32_bf16 v[98:101], v[172:175], v[196:199], v[98:101]
	v_mfma_f32_16x16x32_bf16 v[90:93], v[180:183], v[196:199], v[90:93]
	v_mfma_f32_16x16x32_bf16 v[82:85], v[172:175], v[204:207], v[82:85]
	v_mfma_f32_16x16x32_bf16 v[74:77], v[180:183], v[204:207], v[74:77]
	v_mfma_f32_16x16x32_bf16 v[70:73], v[172:175], v[212:215], v[70:73]
	v_mfma_f32_16x16x32_bf16 v[66:69], v[180:183], v[212:215], v[66:69]
	v_mfma_f32_16x16x32_bf16 v[114:117], v[176:179], v[192:195], v[114:117]
	v_mfma_f32_16x16x32_bf16 v[106:109], v[184:187], v[192:195], v[106:109]
	v_mfma_f32_16x16x32_bf16 v[98:101], v[176:179], v[200:203], v[98:101]
	v_mfma_f32_16x16x32_bf16 v[90:93], v[184:187], v[200:203], v[90:93]
	v_mfma_f32_16x16x32_bf16 v[82:85], v[176:179], v[208:211], v[82:85]
	v_mfma_f32_16x16x32_bf16 v[74:77], v[184:187], v[208:211], v[74:77]
	v_mfma_f32_16x16x32_bf16 v[70:73], v[176:179], v[216:219], v[70:73]
	v_mfma_f32_16x16x32_bf16 v[66:69], v[184:187], v[216:219], v[66:69]
	s_setprio 0
	s_barrier
	s_add_u32 s42, s40, 0x8000
	s_addc_u32 s43, s41, 0
	s_add_i32 s29, s29, s31
	v_lshl_add_u64 v[222:223], s[42:43], 0, v[134:135]
	s_mov_b32 m0, s29
	ds_read_b128 v[188:191], v153 offset:49152
	ds_read_b128 v[192:195], v153 offset:50176
	ds_read_b128 v[196:199], v153 offset:51200
	ds_read_b128 v[200:203], v153 offset:52224
	ds_read_b128 v[204:207], v153 offset:53248
	ds_read_b128 v[208:211], v153 offset:54272
	ds_read_b128 v[212:215], v153 offset:55296
	ds_read_b128 v[216:219], v153 offset:56320
	global_load_lds_dwordx4 v[222:223], off
	s_add_i32 m0, s29, 0x2000
	s_add_u32 s40, s40, 0xc000
	v_lshl_add_u64 v[222:223], s[42:43], 0, v[130:131]
	s_addc_u32 s41, s41, 0
	s_add_i32 s29, s60, s31
	global_load_lds_dwordx4 v[222:223], off
	v_lshl_add_u64 v[222:223], s[40:41], 0, v[134:135]
	s_mov_b32 m0, s29
	v_lshl_add_u64 v[148:149], v[148:149], 0, s[8:9]
	global_load_lds_dwordx4 v[222:223], off
	v_lshl_add_u64 v[222:223], s[40:41], 0, v[130:131]
	s_add_i32 m0, s29, 0x2000
	s_nop 0
	global_load_lds_dwordx4 v[222:223], off
	s_mov_b32 m0, s51
	s_nop 0
	global_load_lds_dwordx4 v[148:149], off
	v_lshl_add_u64 v[148:149], v[220:221], 0, s[8:9]
	s_mov_b32 m0, s52
	s_nop 0
	global_load_lds_dwordx4 v[148:149], off
	s_waitcnt vmcnt(8)
	s_waitcnt lgkmcnt(0)
	s_barrier
	s_setprio 1
	v_mfma_f32_16x16x32_bf16 v[62:65], v[154:157], v[188:191], v[62:65]
	v_mfma_f32_16x16x32_bf16 v[58:61], v[162:165], v[188:191], v[58:61]
	v_mfma_f32_16x16x32_bf16 v[50:53], v[154:157], v[196:199], v[50:53]
	v_mfma_f32_16x16x32_bf16 v[42:45], v[162:165], v[196:199], v[42:45]
	v_mfma_f32_16x16x32_bf16 v[34:37], v[154:157], v[204:207], v[34:37]
	v_mfma_f32_16x16x32_bf16 v[26:29], v[162:165], v[204:207], v[26:29]
	v_mfma_f32_16x16x32_bf16 v[18:21], v[154:157], v[212:215], v[18:21]
	v_mfma_f32_16x16x32_bf16 v[10:13], v[162:165], v[212:215], v[10:13]
	v_mfma_f32_16x16x32_bf16 v[62:65], v[158:161], v[192:195], v[62:65]
	v_mfma_f32_16x16x32_bf16 v[58:61], v[166:169], v[192:195], v[58:61]
	v_mfma_f32_16x16x32_bf16 v[50:53], v[158:161], v[200:203], v[50:53]
	v_mfma_f32_16x16x32_bf16 v[42:45], v[166:169], v[200:203], v[42:45]
	v_mfma_f32_16x16x32_bf16 v[34:37], v[158:161], v[208:211], v[34:37]
	v_mfma_f32_16x16x32_bf16 v[26:29], v[166:169], v[208:211], v[26:29]
	v_mfma_f32_16x16x32_bf16 v[18:21], v[158:161], v[216:219], v[18:21]
	v_mfma_f32_16x16x32_bf16 v[10:13], v[166:169], v[216:219], v[10:13]
	s_setprio 0
	s_setprio 1
	v_mfma_f32_16x16x32_bf16 v[54:57], v[172:175], v[188:191], v[54:57]
	v_mfma_f32_16x16x32_bf16 v[46:49], v[180:183], v[188:191], v[46:49]
	v_mfma_f32_16x16x32_bf16 v[38:41], v[172:175], v[196:199], v[38:41]
	v_mfma_f32_16x16x32_bf16 v[30:33], v[180:183], v[196:199], v[30:33]
	v_mfma_f32_16x16x32_bf16 v[22:25], v[172:175], v[204:207], v[22:25]
	v_mfma_f32_16x16x32_bf16 v[14:17], v[180:183], v[204:207], v[14:17]
	v_mfma_f32_16x16x32_bf16 v[6:9], v[172:175], v[212:215], v[6:9]
	v_mfma_f32_16x16x32_bf16 v[2:5], v[180:183], v[212:215], v[2:5]
	v_mfma_f32_16x16x32_bf16 v[54:57], v[176:179], v[192:195], v[54:57]
	v_mfma_f32_16x16x32_bf16 v[46:49], v[184:187], v[192:195], v[46:49]
	v_mfma_f32_16x16x32_bf16 v[38:41], v[176:179], v[200:203], v[38:41]
	v_mfma_f32_16x16x32_bf16 v[30:33], v[184:187], v[200:203], v[30:33]
	v_mfma_f32_16x16x32_bf16 v[22:25], v[176:179], v[208:211], v[22:25]
	v_mfma_f32_16x16x32_bf16 v[14:17], v[184:187], v[208:211], v[14:17]
	v_mfma_f32_16x16x32_bf16 v[6:9], v[176:179], v[216:219], v[6:9]
	v_mfma_f32_16x16x32_bf16 v[2:5], v[184:187], v[216:219], v[2:5]
	s_setprio 0
	s_barrier
	s_add_i32 s28, s28, 2
	s_add_u32 s58, s58, 0x10000
	s_addc_u32 s59, s59, 0
	s_add_u32 s22, s22, 0x100
	s_addc_u32 s23, s23, 0
	s_cmp_gt_u32 s28, 13
	s_cbranch_scc0 .LBB0_236
	s_and_b64 vcc, exec, s[10:11]
	s_cbranch_vccz .LBB0_239
	s_barrier

.LBB0_609:
	ds_read_b128 v[130:133], v177
	ds_read_b128 v[134:137], v177 offset:1024
	ds_read_b128 v[138:141], v177 offset:2048
	ds_read_b128 v[142:145], v177 offset:3072
	ds_read_b128 v[160:163], v178
	ds_read_b128 v[164:167], v178 offset:1024
	ds_read_b128 v[172:175], v178 offset:2048
	ds_read_b128 v[180:183], v178 offset:3072
	s_add_i32 s29, s28, 2
	s_add_u32 s40, s56, 0xfff80080
	s_addc_u32 s41, s57, -1
	s_cmp_eq_u32 s43, s28
	s_cselect_b32 s61, s49, s41
	s_cselect_b32 s60, s48, s40
	s_cselect_b32 s59, s51, s47
	s_cselect_b32 s58, s50, s45
	v_lshl_add_u64 v[168:169], s[56:57], 0, v[154:155]
	s_add_i32 m0, s63, 0xc000
	ds_read_b128 v[184:187], v179
	ds_read_b128 v[188:191], v179 offset:1024
	ds_read_b128 v[192:195], v179 offset:2048
	ds_read_b128 v[196:199], v179 offset:3072
	ds_read_b128 v[200:203], v179 offset:4096
	ds_read_b128 v[204:207], v179 offset:5120
	ds_read_b128 v[208:211], v179 offset:6144
	ds_read_b128 v[212:215], v179 offset:7168
	global_load_lds_dwordx4 v[168:169], off
	v_lshl_add_u64 v[168:169], s[56:57], 0, v[156:157]
	s_add_i32 m0, s63, 0xe000
	s_nop 0
	global_load_lds_dwordx4 v[168:169], off
	s_waitcnt vmcnt(8)
	s_waitcnt lgkmcnt(0)
	s_barrier
	s_setprio 1
	v_mfma_f32_16x16x32_bf16 v[126:129], v[130:133], v[184:187], v[126:129]
	v_mfma_f32_16x16x32_bf16 v[122:125], v[138:141], v[184:187], v[122:125]
	v_mfma_f32_16x16x32_bf16 v[118:121], v[130:133], v[192:195], v[118:121]
	v_mfma_f32_16x16x32_bf16 v[110:113], v[138:141], v[192:195], v[110:113]
	v_mfma_f32_16x16x32_bf16 v[102:105], v[130:133], v[200:203], v[102:105]
	v_mfma_f32_16x16x32_bf16 v[94:97], v[138:141], v[200:203], v[94:97]
	v_mfma_f32_16x16x32_bf16 v[86:89], v[130:133], v[208:211], v[86:89]
	v_mfma_f32_16x16x32_bf16 v[78:81], v[138:141], v[208:211], v[78:81]
	v_mfma_f32_16x16x32_bf16 v[126:129], v[134:137], v[188:191], v[126:129]
	v_mfma_f32_16x16x32_bf16 v[122:125], v[142:145], v[188:191], v[122:125]
	v_mfma_f32_16x16x32_bf16 v[118:121], v[134:137], v[196:199], v[118:121]
	v_mfma_f32_16x16x32_bf16 v[110:113], v[142:145], v[196:199], v[110:113]
	v_mfma_f32_16x16x32_bf16 v[102:105], v[134:137], v[204:207], v[102:105]
	v_mfma_f32_16x16x32_bf16 v[94:97], v[142:145], v[204:207], v[94:97]
	v_mfma_f32_16x16x32_bf16 v[86:89], v[134:137], v[212:215], v[86:89]
	v_mfma_f32_16x16x32_bf16 v[78:81], v[142:145], v[212:215], v[78:81]
	s_setprio 0
	s_setprio 1
	v_mfma_f32_16x16x32_bf16 v[114:117], v[160:163], v[184:187], v[114:117]
	v_mfma_f32_16x16x32_bf16 v[106:109], v[172:175], v[184:187], v[106:109]
	v_mfma_f32_16x16x32_bf16 v[98:101], v[160:163], v[192:195], v[98:101]
	v_mfma_f32_16x16x32_bf16 v[90:93], v[172:175], v[192:195], v[90:93]
	v_mfma_f32_16x16x32_bf16 v[82:85], v[160:163], v[200:203], v[82:85]
	v_mfma_f32_16x16x32_bf16 v[74:77], v[172:175], v[200:203], v[74:77]
	v_mfma_f32_16x16x32_bf16 v[70:73], v[160:163], v[208:211], v[70:73]
	v_mfma_f32_16x16x32_bf16 v[66:69], v[172:175], v[208:211], v[66:69]
	v_mfma_f32_16x16x32_bf16 v[114:117], v[164:167], v[188:191], v[114:117]
	v_mfma_f32_16x16x32_bf16 v[106:109], v[180:183], v[188:191], v[106:109]
	v_mfma_f32_16x16x32_bf16 v[98:101], v[164:167], v[196:199], v[98:101]
	v_mfma_f32_16x16x32_bf16 v[90:93], v[180:183], v[196:199], v[90:93]
	v_mfma_f32_16x16x32_bf16 v[82:85], v[164:167], v[204:207], v[82:85]
	v_mfma_f32_16x16x32_bf16 v[74:77], v[180:183], v[204:207], v[74:77]
	v_mfma_f32_16x16x32_bf16 v[70:73], v[164:167], v[212:215], v[70:73]
	v_mfma_f32_16x16x32_bf16 v[66:69], v[180:183], v[212:215], v[66:69]
	s_setprio 0
	s_barrier
	s_add_i32 s28, s71, s62
	v_lshl_add_u64 v[168:169], s[58:59], 0, v[148:149]
	s_mov_b32 m0, s28
	ds_read_b128 v[184:187], v179 offset:16384
	ds_read_b128 v[188:191], v179 offset:17408
	ds_read_b128 v[192:195], v179 offset:18432
	ds_read_b128 v[196:199], v179 offset:19456
	ds_read_b128 v[200:203], v179 offset:20480
	ds_read_b128 v[204:207], v179 offset:21504
	ds_read_b128 v[208:211], v179 offset:22528
	ds_read_b128 v[212:215], v179 offset:23552
	global_load_lds_dwordx4 v[168:169], off
	s_add_i32 m0, s28, 0x2000
	s_add_u32 s40, s58, 0x4000
	v_lshl_add_u64 v[168:169], s[58:59], 0, v[152:153]
	s_addc_u32 s41, s59, 0
	s_add_i32 s28, s72, s62
	global_load_lds_dwordx4 v[168:169], off
	v_lshl_add_u64 v[168:169], s[40:41], 0, v[148:149]
	s_mov_b32 m0, s28
	v_lshl_add_u64 v[216:217], s[60:61], 0, v[150:151]
	global_load_lds_dwordx4 v[168:169], off
	v_lshl_add_u64 v[168:169], s[40:41], 0, v[152:153]
	s_add_i32 m0, s28, 0x2000
	s_nop 0
	global_load_lds_dwordx4 v[168:169], off
	v_lshl_add_u64 v[168:169], s[60:61], 0, v[146:147]
	s_mov_b32 m0, s63
	s_nop 0
	global_load_lds_dwordx4 v[168:169], off
	s_mov_b32 m0, s53
	s_nop 0
	global_load_lds_dwordx4 v[216:217], off
	s_waitcnt vmcnt(8)
	s_waitcnt lgkmcnt(0)
	s_barrier
	s_setprio 1
	v_mfma_f32_16x16x32_bf16 v[62:65], v[130:133], v[184:187], v[62:65]
	v_mfma_f32_16x16x32_bf16 v[58:61], v[138:141], v[184:187], v[58:61]
	v_mfma_f32_16x16x32_bf16 v[54:57], v[130:133], v[192:195], v[54:57]
	v_mfma_f32_16x16x32_bf16 v[46:49], v[138:141], v[192:195], v[46:49]
	v_mfma_f32_16x16x32_bf16 v[38:41], v[130:133], v[200:203], v[38:41]
	v_mfma_f32_16x16x32_bf16 v[30:33], v[138:141], v[200:203], v[30:33]
	v_mfma_f32_16x16x32_bf16 v[22:25], v[130:133], v[208:211], v[22:25]
	v_mfma_f32_16x16x32_bf16 v[14:17], v[138:141], v[208:211], v[14:17]
	v_mfma_f32_16x16x32_bf16 v[62:65], v[134:137], v[188:191], v[62:65]
	v_mfma_f32_16x16x32_bf16 v[58:61], v[142:145], v[188:191], v[58:61]
	v_mfma_f32_16x16x32_bf16 v[54:57], v[134:137], v[196:199], v[54:57]
	v_mfma_f32_16x16x32_bf16 v[46:49], v[142:145], v[196:199], v[46:49]
	v_mfma_f32_16x16x32_bf16 v[38:41], v[134:137], v[204:207], v[38:41]
	v_mfma_f32_16x16x32_bf16 v[30:33], v[142:145], v[204:207], v[30:33]
	v_mfma_f32_16x16x32_bf16 v[22:25], v[134:137], v[212:215], v[22:25]
	v_mfma_f32_16x16x32_bf16 v[14:17], v[142:145], v[212:215], v[14:17]
	s_setprio 0
	s_setprio 1
	v_mfma_f32_16x16x32_bf16 v[50:53], v[160:163], v[184:187], v[50:53]
	v_mfma_f32_16x16x32_bf16 v[42:45], v[172:175], v[184:187], v[42:45]
	v_mfma_f32_16x16x32_bf16 v[34:37], v[160:163], v[192:195], v[34:37]
	v_mfma_f32_16x16x32_bf16 v[26:29], v[172:175], v[192:195], v[26:29]
	v_mfma_f32_16x16x32_bf16 v[18:21], v[160:163], v[200:203], v[18:21]
	v_mfma_f32_16x16x32_bf16 v[10:13], v[172:175], v[200:203], v[10:13]
	v_mfma_f32_16x16x32_bf16 v[6:9], v[160:163], v[208:211], v[6:9]
	v_mfma_f32_16x16x32_bf16 v[2:5], v[172:175], v[208:211], v[2:5]
	v_mfma_f32_16x16x32_bf16 v[50:53], v[164:167], v[188:191], v[50:53]
	v_mfma_f32_16x16x32_bf16 v[42:45], v[180:183], v[188:191], v[42:45]
	v_mfma_f32_16x16x32_bf16 v[34:37], v[164:167], v[196:199], v[34:37]
	v_mfma_f32_16x16x32_bf16 v[26:29], v[180:183], v[196:199], v[26:29]
	v_mfma_f32_16x16x32_bf16 v[18:21], v[164:167], v[204:207], v[18:21]
	v_mfma_f32_16x16x32_bf16 v[10:13], v[180:183], v[204:207], v[10:13]
	v_mfma_f32_16x16x32_bf16 v[6:9], v[164:167], v[212:215], v[6:9]
	v_mfma_f32_16x16x32_bf16 v[2:5], v[180:183], v[212:215], v[2:5]
	s_setprio 0
	s_barrier
	s_add_i32 s28, 0, 0x18000
	s_add_i32 s55, 0, 0x1c000
	v_add_u32_e32 v142, s28, v171
	v_add_u32_e32 v180, s55, v171
	ds_read_b128 v[130:133], v142
	ds_read_b128 v[134:137], v142 offset:1024
	ds_read_b128 v[138:141], v142 offset:2048
	ds_read_b128 v[142:145], v142 offset:3072
	ds_read_b128 v[160:163], v180
	ds_read_b128 v[164:167], v180 offset:1024
	ds_read_b128 v[172:175], v180 offset:2048
	ds_read_b128 v[180:183], v180 offset:3072
	s_add_u32 s40, s60, 0x80000
	s_addc_u32 s41, s61, 0
	s_mov_b32 m0, s64
	v_lshl_add_u64 v[218:219], s[40:41], 0, v[146:147]
	ds_read_b128 v[184:187], v179 offset:32768
	ds_read_b128 v[188:191], v179 offset:33792
	ds_read_b128 v[192:195], v179 offset:34816
	ds_read_b128 v[196:199], v179 offset:35840
	ds_read_b128 v[200:203], v179 offset:36864
	ds_read_b128 v[204:207], v179 offset:37888
	ds_read_b128 v[208:211], v179 offset:38912
	ds_read_b128 v[212:215], v179 offset:39936
	global_load_lds_dwordx4 v[218:219], off
	v_lshl_add_u64 v[218:219], s[40:41], 0, v[150:151]
	s_mov_b32 m0, s65
	s_nop 0
	global_load_lds_dwordx4 v[218:219], off
	s_waitcnt vmcnt(8)
	s_waitcnt lgkmcnt(0)
	s_barrier
	s_setprio 1
	v_mfma_f32_16x16x32_bf16 v[126:129], v[130:133], v[184:187], v[126:129]
	v_mfma_f32_16x16x32_bf16 v[122:125], v[138:141], v[184:187], v[122:125]
	v_mfma_f32_16x16x32_bf16 v[118:121], v[130:133], v[192:195], v[118:121]
	v_mfma_f32_16x16x32_bf16 v[110:113], v[138:141], v[192:195], v[110:113]
	v_mfma_f32_16x16x32_bf16 v[102:105], v[130:133], v[200:203], v[102:105]
	v_mfma_f32_16x16x32_bf16 v[94:97], v[138:141], v[200:203], v[94:97]
	v_mfma_f32_16x16x32_bf16 v[86:89], v[130:133], v[208:211], v[86:89]
	v_mfma_f32_16x16x32_bf16 v[78:81], v[138:141], v[208:211], v[78:81]
	v_mfma_f32_16x16x32_bf16 v[126:129], v[134:137], v[188:191], v[126:129]
	v_mfma_f32_16x16x32_bf16 v[122:125], v[142:145], v[188:191], v[122:125]
	v_mfma_f32_16x16x32_bf16 v[118:121], v[134:137], v[196:199], v[118:121]
	v_mfma_f32_16x16x32_bf16 v[110:113], v[142:145], v[196:199], v[110:113]
	v_mfma_f32_16x16x32_bf16 v[102:105], v[134:137], v[204:207], v[102:105]
	v_mfma_f32_16x16x32_bf16 v[94:97], v[142:145], v[204:207], v[94:97]
	v_mfma_f32_16x16x32_bf16 v[86:89], v[134:137], v[212:215], v[86:89]
	v_mfma_f32_16x16x32_bf16 v[78:81], v[142:145], v[212:215], v[78:81]
	s_setprio 0
	s_setprio 1
	v_mfma_f32_16x16x32_bf16 v[114:117], v[160:163], v[184:187], v[114:117]
	v_mfma_f32_16x16x32_bf16 v[106:109], v[172:175], v[184:187], v[106:109]
	v_mfma_f32_16x16x32_bf16 v[98:101], v[160:163], v[192:195], v[98:101]
	v_mfma_f32_16x16x32_bf16 v[90:93], v[172:175], v[192:195], v[90:93]
	v_mfma_f32_16x16x32_bf16 v[82:85], v[160:163], v[200:203], v[82:85]
	v_mfma_f32_16x16x32_bf16 v[74:77], v[172:175], v[200:203], v[74:77]
	v_mfma_f32_16x16x32_bf16 v[70:73], v[160:163], v[208:211], v[70:73]
	v_mfma_f32_16x16x32_bf16 v[66:69], v[172:175], v[208:211], v[66:69]
	v_mfma_f32_16x16x32_bf16 v[114:117], v[164:167], v[188:191], v[114:117]
	v_mfma_f32_16x16x32_bf16 v[106:109], v[180:183], v[188:191], v[106:109]
	v_mfma_f32_16x16x32_bf16 v[98:101], v[164:167], v[196:199], v[98:101]
	v_mfma_f32_16x16x32_bf16 v[90:93], v[180:183], v[196:199], v[90:93]
	v_mfma_f32_16x16x32_bf16 v[82:85], v[164:167], v[204:207], v[82:85]
	v_mfma_f32_16x16x32_bf16 v[74:77], v[180:183], v[204:207], v[74:77]
	v_mfma_f32_16x16x32_bf16 v[70:73], v[164:167], v[212:215], v[70:73]
	v_mfma_f32_16x16x32_bf16 v[66:69], v[180:183], v[212:215], v[66:69]
	s_setprio 0
	s_barrier
	s_add_u32 s40, s58, 0x8000
	s_addc_u32 s41, s59, 0
	s_add_i32 s28, s28, s62
	v_lshl_add_u64 v[218:219], s[40:41], 0, v[148:149]
	s_mov_b32 m0, s28
	ds_read_b128 v[184:187], v179 offset:49152
	ds_read_b128 v[188:191], v179 offset:50176
	ds_read_b128 v[192:195], v179 offset:51200
	ds_read_b128 v[196:199], v179 offset:52224
	ds_read_b128 v[200:203], v179 offset:53248
	ds_read_b128 v[204:207], v179 offset:54272
	ds_read_b128 v[208:211], v179 offset:55296
	ds_read_b128 v[212:215], v179 offset:56320
	global_load_lds_dwordx4 v[218:219], off
	s_add_i32 m0, s28, 0x2000
	v_lshl_add_u64 v[218:219], s[40:41], 0, v[152:153]
	s_add_u32 s40, s58, 0xc000
	s_addc_u32 s41, s59, 0
	s_add_i32 s28, s55, s62
	global_load_lds_dwordx4 v[218:219], off
	v_lshl_add_u64 v[218:219], s[40:41], 0, v[148:149]
	s_mov_b32 m0, s28
	v_lshl_add_u64 v[168:169], v[168:169], 0, s[12:13]
	global_load_lds_dwordx4 v[218:219], off
	v_lshl_add_u64 v[218:219], s[40:41], 0, v[152:153]
	s_add_i32 m0, s28, 0x2000
	s_nop 0
	global_load_lds_dwordx4 v[218:219], off
	s_mov_b32 m0, s30
	s_nop 0
	global_load_lds_dwordx4 v[168:169], off
	v_lshl_add_u64 v[168:169], v[216:217], 0, s[12:13]
	s_mov_b32 m0, s31
	s_nop 0
	global_load_lds_dwordx4 v[168:169], off
	s_waitcnt vmcnt(8)
	s_waitcnt lgkmcnt(0)
	s_barrier
	s_setprio 1
	v_mfma_f32_16x16x32_bf16 v[62:65], v[130:133], v[184:187], v[62:65]
	v_mfma_f32_16x16x32_bf16 v[58:61], v[138:141], v[184:187], v[58:61]
	v_mfma_f32_16x16x32_bf16 v[54:57], v[130:133], v[192:195], v[54:57]
	v_mfma_f32_16x16x32_bf16 v[46:49], v[138:141], v[192:195], v[46:49]
	v_mfma_f32_16x16x32_bf16 v[38:41], v[130:133], v[200:203], v[38:41]
	v_mfma_f32_16x16x32_bf16 v[30:33], v[138:141], v[200:203], v[30:33]
	v_mfma_f32_16x16x32_bf16 v[22:25], v[130:133], v[208:211], v[22:25]
	v_mfma_f32_16x16x32_bf16 v[14:17], v[138:141], v[208:211], v[14:17]
	v_mfma_f32_16x16x32_bf16 v[62:65], v[134:137], v[188:191], v[62:65]
	v_mfma_f32_16x16x32_bf16 v[58:61], v[142:145], v[188:191], v[58:61]
	v_mfma_f32_16x16x32_bf16 v[54:57], v[134:137], v[196:199], v[54:57]
	v_mfma_f32_16x16x32_bf16 v[46:49], v[142:145], v[196:199], v[46:49]
	v_mfma_f32_16x16x32_bf16 v[38:41], v[134:137], v[204:207], v[38:41]
	v_mfma_f32_16x16x32_bf16 v[30:33], v[142:145], v[204:207], v[30:33]
	v_mfma_f32_16x16x32_bf16 v[22:25], v[134:137], v[212:215], v[22:25]
	v_mfma_f32_16x16x32_bf16 v[14:17], v[142:145], v[212:215], v[14:17]
	s_setprio 0
	s_setprio 1
	v_mfma_f32_16x16x32_bf16 v[50:53], v[160:163], v[184:187], v[50:53]
	v_mfma_f32_16x16x32_bf16 v[42:45], v[172:175], v[184:187], v[42:45]
	v_mfma_f32_16x16x32_bf16 v[34:37], v[160:163], v[192:195], v[34:37]
	v_mfma_f32_16x16x32_bf16 v[26:29], v[172:175], v[192:195], v[26:29]
	v_mfma_f32_16x16x32_bf16 v[18:21], v[160:163], v[200:203], v[18:21]
	v_mfma_f32_16x16x32_bf16 v[10:13], v[172:175], v[200:203], v[10:13]
	v_mfma_f32_16x16x32_bf16 v[6:9], v[160:163], v[208:211], v[6:9]
	v_mfma_f32_16x16x32_bf16 v[2:5], v[172:175], v[208:211], v[2:5]
	v_mfma_f32_16x16x32_bf16 v[50:53], v[164:167], v[188:191], v[50:53]
	v_mfma_f32_16x16x32_bf16 v[42:45], v[180:183], v[188:191], v[42:45]
	v_mfma_f32_16x16x32_bf16 v[34:37], v[164:167], v[196:199], v[34:37]
	v_mfma_f32_16x16x32_bf16 v[26:29], v[180:183], v[196:199], v[26:29]
	v_mfma_f32_16x16x32_bf16 v[18:21], v[164:167], v[204:207], v[18:21]
	v_mfma_f32_16x16x32_bf16 v[10:13], v[180:183], v[204:207], v[10:13]
	v_mfma_f32_16x16x32_bf16 v[6:9], v[164:167], v[212:215], v[6:9]
	v_mfma_f32_16x16x32_bf16 v[2:5], v[180:183], v[212:215], v[2:5]
	s_setprio 0
	s_barrier
	s_add_u32 s45, s45, 0x10000
	s_addc_u32 s47, s47, 0
	s_add_u32 s56, s56, 0x100
	s_addc_u32 s57, s57, 0
	s_cmp_ge_u32 s29, s33
	s_mov_b32 s28, s29
	s_cbranch_scc0 .LBB0_609
	s_and_b64 vcc, exec, s[14:15]
	s_cbranch_vccz .LBB0_612
	s_barrier

.LBB0_739:
	ds_read_b128 v[156:159], v152
	ds_read_b128 v[160:163], v152 offset:1024
	ds_read_b128 v[164:167], v152 offset:2048
	ds_read_b128 v[172:175], v152 offset:3072
	ds_read_b128 v[176:179], v153
	ds_read_b128 v[180:183], v153 offset:1024
	ds_read_b128 v[184:187], v153 offset:2048
	ds_read_b128 v[188:191], v153 offset:3072
	s_add_u32 s29, s44, 0xfffc0080
	s_addc_u32 s40, s45, -1
	s_cmp_eq_u32 s28, 12
	s_cselect_b32 s49, s17, s40
	s_cselect_b32 s48, s43, s29
	s_cselect_b32 s47, s15, s65
	s_cselect_b32 s46, s63, s64
	v_lshl_add_u64 v[150:151], s[44:45], 0, v[142:143]
	s_add_i32 m0, s23, 0xc000
	ds_read_b128 v[192:195], v154
	ds_read_b128 v[196:199], v154 offset:1024
	ds_read_b128 v[200:203], v154 offset:2048
	ds_read_b128 v[204:207], v154 offset:3072
	ds_read_b128 v[208:211], v154 offset:4096
	ds_read_b128 v[212:215], v154 offset:5120
	ds_read_b128 v[216:219], v154 offset:6144
	ds_read_b128 v[220:223], v154 offset:7168
	global_load_lds_dwordx4 v[150:151], off
	v_lshl_add_u64 v[150:151], s[44:45], 0, v[144:145]
	s_add_i32 m0, s23, 0xe000
	s_nop 0
	global_load_lds_dwordx4 v[150:151], off
	s_waitcnt vmcnt(8)
	s_waitcnt lgkmcnt(0)
	s_barrier
	s_setprio 1
	v_mfma_f32_16x16x32_bf16 v[126:129], v[156:159], v[192:195], v[126:129]
	v_mfma_f32_16x16x32_bf16 v[122:125], v[164:167], v[192:195], v[122:125]
	v_mfma_f32_16x16x32_bf16 v[118:121], v[156:159], v[200:203], v[118:121]
	v_mfma_f32_16x16x32_bf16 v[114:117], v[164:167], v[200:203], v[114:117]
	v_mfma_f32_16x16x32_bf16 v[94:97], v[156:159], v[208:211], v[94:97]
	v_mfma_f32_16x16x32_bf16 v[90:93], v[164:167], v[208:211], v[90:93]
	v_mfma_f32_16x16x32_bf16 v[86:89], v[156:159], v[216:219], v[86:89]
	v_mfma_f32_16x16x32_bf16 v[82:85], v[164:167], v[216:219], v[82:85]
	v_mfma_f32_16x16x32_bf16 v[126:129], v[160:163], v[196:199], v[126:129]
	v_mfma_f32_16x16x32_bf16 v[122:125], v[172:175], v[196:199], v[122:125]
	v_mfma_f32_16x16x32_bf16 v[118:121], v[160:163], v[204:207], v[118:121]
	v_mfma_f32_16x16x32_bf16 v[114:117], v[172:175], v[204:207], v[114:117]
	v_mfma_f32_16x16x32_bf16 v[94:97], v[160:163], v[212:215], v[94:97]
	v_mfma_f32_16x16x32_bf16 v[90:93], v[172:175], v[212:215], v[90:93]
	v_mfma_f32_16x16x32_bf16 v[86:89], v[160:163], v[220:223], v[86:89]
	v_mfma_f32_16x16x32_bf16 v[82:85], v[172:175], v[220:223], v[82:85]
	s_setprio 0
	s_setprio 1
	v_mfma_f32_16x16x32_bf16 v[110:113], v[176:179], v[192:195], v[110:113]
	v_mfma_f32_16x16x32_bf16 v[106:109], v[184:187], v[192:195], v[106:109]
	v_mfma_f32_16x16x32_bf16 v[102:105], v[176:179], v[200:203], v[102:105]
	v_mfma_f32_16x16x32_bf16 v[98:101], v[184:187], v[200:203], v[98:101]
	v_mfma_f32_16x16x32_bf16 v[78:81], v[176:179], v[208:211], v[78:81]
	v_mfma_f32_16x16x32_bf16 v[74:77], v[184:187], v[208:211], v[74:77]
	v_mfma_f32_16x16x32_bf16 v[70:73], v[176:179], v[216:219], v[70:73]
	v_mfma_f32_16x16x32_bf16 v[66:69], v[184:187], v[216:219], v[66:69]
	v_mfma_f32_16x16x32_bf16 v[110:113], v[180:183], v[196:199], v[110:113]
	v_mfma_f32_16x16x32_bf16 v[106:109], v[188:191], v[196:199], v[106:109]
	v_mfma_f32_16x16x32_bf16 v[102:105], v[180:183], v[204:207], v[102:105]
	v_mfma_f32_16x16x32_bf16 v[98:101], v[188:191], v[204:207], v[98:101]
	v_mfma_f32_16x16x32_bf16 v[78:81], v[180:183], v[212:215], v[78:81]
	v_mfma_f32_16x16x32_bf16 v[74:77], v[188:191], v[212:215], v[74:77]
	v_mfma_f32_16x16x32_bf16 v[70:73], v[180:183], v[220:223], v[70:73]
	v_mfma_f32_16x16x32_bf16 v[66:69], v[188:191], v[220:223], v[66:69]
	s_setprio 0
	s_barrier
	s_add_i32 s29, s56, s31
	v_lshl_add_u64 v[150:151], s[46:47], 0, v[134:135]
	s_mov_b32 m0, s29
	ds_read_b128 v[192:195], v154 offset:16384
	ds_read_b128 v[196:199], v154 offset:17408
	ds_read_b128 v[200:203], v154 offset:18432
	ds_read_b128 v[204:207], v154 offset:19456
	ds_read_b128 v[208:211], v154 offset:20480
	ds_read_b128 v[212:215], v154 offset:21504
	ds_read_b128 v[216:219], v154 offset:22528
	ds_read_b128 v[220:223], v154 offset:23552
	global_load_lds_dwordx4 v[150:151], off
	s_add_i32 m0, s29, 0x2000
	s_add_u32 s40, s46, 0x4000
	v_lshl_add_u64 v[150:151], s[46:47], 0, v[130:131]
	s_addc_u32 s41, s47, 0
	s_add_i32 s29, s57, s31
	global_load_lds_dwordx4 v[150:151], off
	v_lshl_add_u64 v[150:151], s[40:41], 0, v[134:135]
	s_mov_b32 m0, s29
	v_lshl_add_u64 v[168:169], s[48:49], 0, v[132:133]
	global_load_lds_dwordx4 v[150:151], off
	v_lshl_add_u64 v[150:151], s[40:41], 0, v[130:131]
	s_add_i32 m0, s29, 0x2000
	s_nop 0
	global_load_lds_dwordx4 v[150:151], off
	v_lshl_add_u64 v[150:151], s[48:49], 0, v[136:137]
	s_mov_b32 m0, s23
	s_nop 0
	global_load_lds_dwordx4 v[150:151], off
	s_mov_b32 m0, s33
	s_nop 0
	global_load_lds_dwordx4 v[168:169], off
	s_waitcnt vmcnt(8)
	s_waitcnt lgkmcnt(0)
	s_barrier
	s_setprio 1
	v_mfma_f32_16x16x32_bf16 v[62:65], v[156:159], v[192:195], v[62:65]
	v_mfma_f32_16x16x32_bf16 v[58:61], v[164:167], v[192:195], v[58:61]
	v_mfma_f32_16x16x32_bf16 v[54:57], v[156:159], v[200:203], v[54:57]
	v_mfma_f32_16x16x32_bf16 v[50:53], v[164:167], v[200:203], v[50:53]
	v_mfma_f32_16x16x32_bf16 v[30:33], v[156:159], v[208:211], v[30:33]
	v_mfma_f32_16x16x32_bf16 v[26:29], v[164:167], v[208:211], v[26:29]
	v_mfma_f32_16x16x32_bf16 v[22:25], v[156:159], v[216:219], v[22:25]
	v_mfma_f32_16x16x32_bf16 v[18:21], v[164:167], v[216:219], v[18:21]
	v_mfma_f32_16x16x32_bf16 v[62:65], v[160:163], v[196:199], v[62:65]
	v_mfma_f32_16x16x32_bf16 v[58:61], v[172:175], v[196:199], v[58:61]
	v_mfma_f32_16x16x32_bf16 v[54:57], v[160:163], v[204:207], v[54:57]
	v_mfma_f32_16x16x32_bf16 v[50:53], v[172:175], v[204:207], v[50:53]
	v_mfma_f32_16x16x32_bf16 v[30:33], v[160:163], v[212:215], v[30:33]
	v_mfma_f32_16x16x32_bf16 v[26:29], v[172:175], v[212:215], v[26:29]
	v_mfma_f32_16x16x32_bf16 v[22:25], v[160:163], v[220:223], v[22:25]
	v_mfma_f32_16x16x32_bf16 v[18:21], v[172:175], v[220:223], v[18:21]
	s_setprio 0
	s_setprio 1
	v_mfma_f32_16x16x32_bf16 v[46:49], v[176:179], v[192:195], v[46:49]
	v_mfma_f32_16x16x32_bf16 v[42:45], v[184:187], v[192:195], v[42:45]
	v_mfma_f32_16x16x32_bf16 v[38:41], v[176:179], v[200:203], v[38:41]
	v_mfma_f32_16x16x32_bf16 v[34:37], v[184:187], v[200:203], v[34:37]
	v_mfma_f32_16x16x32_bf16 v[14:17], v[176:179], v[208:211], v[14:17]
	v_mfma_f32_16x16x32_bf16 v[10:13], v[184:187], v[208:211], v[10:13]
	v_mfma_f32_16x16x32_bf16 v[6:9], v[176:179], v[216:219], v[6:9]
	v_mfma_f32_16x16x32_bf16 v[2:5], v[184:187], v[216:219], v[2:5]
	v_mfma_f32_16x16x32_bf16 v[46:49], v[180:183], v[196:199], v[46:49]
	v_mfma_f32_16x16x32_bf16 v[42:45], v[188:191], v[196:199], v[42:45]
	v_mfma_f32_16x16x32_bf16 v[38:41], v[180:183], v[204:207], v[38:41]
	v_mfma_f32_16x16x32_bf16 v[34:37], v[188:191], v[204:207], v[34:37]
	v_mfma_f32_16x16x32_bf16 v[14:17], v[180:183], v[212:215], v[14:17]
	v_mfma_f32_16x16x32_bf16 v[10:13], v[188:191], v[212:215], v[10:13]
	v_mfma_f32_16x16x32_bf16 v[6:9], v[180:183], v[220:223], v[6:9]
	v_mfma_f32_16x16x32_bf16 v[2:5], v[188:191], v[220:223], v[2:5]
	s_setprio 0
	s_barrier
	s_add_i32 s29, 0, 0x18000
	v_add_u32_e32 v155, s29, v1
	s_add_i32 s66, 0, 0x1c000
	ds_read_b128 v[156:159], v155
	ds_read_b128 v[160:163], v155 offset:1024
	ds_read_b128 v[164:167], v155 offset:2048
	ds_read_b128 v[172:175], v155 offset:3072
	v_add_u32_e32 v155, s66, v1
	ds_read_b128 v[176:179], v155
	ds_read_b128 v[180:183], v155 offset:1024
	ds_read_b128 v[184:187], v155 offset:2048
	ds_read_b128 v[188:191], v155 offset:3072
	s_add_u32 s40, s48, 0x40000
	s_addc_u32 s41, s49, 0
	s_mov_b32 m0, s37
	v_lshl_add_u64 v[224:225], s[40:41], 0, v[136:137]
	ds_read_b128 v[192:195], v154 offset:32768
	ds_read_b128 v[196:199], v154 offset:33792
	ds_read_b128 v[200:203], v154 offset:34816
	ds_read_b128 v[204:207], v154 offset:35840
	ds_read_b128 v[208:211], v154 offset:36864
	ds_read_b128 v[212:215], v154 offset:37888
	ds_read_b128 v[216:219], v154 offset:38912
	ds_read_b128 v[220:223], v154 offset:39936
	global_load_lds_dwordx4 v[224:225], off
	v_lshl_add_u64 v[224:225], s[40:41], 0, v[132:133]
	s_mov_b32 m0, s50
	s_nop 0
	global_load_lds_dwordx4 v[224:225], off
	s_waitcnt vmcnt(8)
	s_waitcnt lgkmcnt(0)
	s_barrier
	s_setprio 1
	v_mfma_f32_16x16x32_bf16 v[126:129], v[156:159], v[192:195], v[126:129]
	v_mfma_f32_16x16x32_bf16 v[122:125], v[164:167], v[192:195], v[122:125]
	v_mfma_f32_16x16x32_bf16 v[118:121], v[156:159], v[200:203], v[118:121]
	v_mfma_f32_16x16x32_bf16 v[114:117], v[164:167], v[200:203], v[114:117]
	v_mfma_f32_16x16x32_bf16 v[94:97], v[156:159], v[208:211], v[94:97]
	v_mfma_f32_16x16x32_bf16 v[90:93], v[164:167], v[208:211], v[90:93]
	v_mfma_f32_16x16x32_bf16 v[86:89], v[156:159], v[216:219], v[86:89]
	v_mfma_f32_16x16x32_bf16 v[82:85], v[164:167], v[216:219], v[82:85]
	v_mfma_f32_16x16x32_bf16 v[126:129], v[160:163], v[196:199], v[126:129]
	v_mfma_f32_16x16x32_bf16 v[122:125], v[172:175], v[196:199], v[122:125]
	v_mfma_f32_16x16x32_bf16 v[118:121], v[160:163], v[204:207], v[118:121]
	v_mfma_f32_16x16x32_bf16 v[114:117], v[172:175], v[204:207], v[114:117]
	v_mfma_f32_16x16x32_bf16 v[94:97], v[160:163], v[212:215], v[94:97]
	v_mfma_f32_16x16x32_bf16 v[90:93], v[172:175], v[212:215], v[90:93]
	v_mfma_f32_16x16x32_bf16 v[86:89], v[160:163], v[220:223], v[86:89]
	v_mfma_f32_16x16x32_bf16 v[82:85], v[172:175], v[220:223], v[82:85]
	s_setprio 0
	s_setprio 1
	v_mfma_f32_16x16x32_bf16 v[110:113], v[176:179], v[192:195], v[110:113]
	v_mfma_f32_16x16x32_bf16 v[106:109], v[184:187], v[192:195], v[106:109]
	v_mfma_f32_16x16x32_bf16 v[102:105], v[176:179], v[200:203], v[102:105]
	v_mfma_f32_16x16x32_bf16 v[98:101], v[184:187], v[200:203], v[98:101]
	v_mfma_f32_16x16x32_bf16 v[78:81], v[176:179], v[208:211], v[78:81]
	v_mfma_f32_16x16x32_bf16 v[74:77], v[184:187], v[208:211], v[74:77]
	v_mfma_f32_16x16x32_bf16 v[70:73], v[176:179], v[216:219], v[70:73]
	v_mfma_f32_16x16x32_bf16 v[66:69], v[184:187], v[216:219], v[66:69]
	v_mfma_f32_16x16x32_bf16 v[110:113], v[180:183], v[196:199], v[110:113]
	v_mfma_f32_16x16x32_bf16 v[106:109], v[188:191], v[196:199], v[106:109]
	v_mfma_f32_16x16x32_bf16 v[102:105], v[180:183], v[204:207], v[102:105]
	v_mfma_f32_16x16x32_bf16 v[98:101], v[188:191], v[204:207], v[98:101]
	v_mfma_f32_16x16x32_bf16 v[78:81], v[180:183], v[212:215], v[78:81]
	v_mfma_f32_16x16x32_bf16 v[74:77], v[188:191], v[212:215], v[74:77]
	v_mfma_f32_16x16x32_bf16 v[70:73], v[180:183], v[220:223], v[70:73]
	v_mfma_f32_16x16x32_bf16 v[66:69], v[188:191], v[220:223], v[66:69]
	s_setprio 0
	s_barrier
	s_add_u32 s40, s46, 0x8000
	s_addc_u32 s41, s47, 0
	s_add_i32 s29, s29, s31
	v_lshl_add_u64 v[224:225], s[40:41], 0, v[134:135]
	s_mov_b32 m0, s29
	ds_read_b128 v[192:195], v154 offset:49152
	ds_read_b128 v[196:199], v154 offset:50176
	ds_read_b128 v[200:203], v154 offset:51200
	ds_read_b128 v[204:207], v154 offset:52224
	ds_read_b128 v[208:211], v154 offset:53248
	ds_read_b128 v[212:215], v154 offset:54272
	ds_read_b128 v[216:219], v154 offset:55296
	ds_read_b128 v[220:223], v154 offset:56320
	global_load_lds_dwordx4 v[224:225], off
	s_add_i32 m0, s29, 0x2000
	v_lshl_add_u64 v[224:225], s[40:41], 0, v[130:131]
	s_add_u32 s40, s46, 0xc000
	s_addc_u32 s41, s47, 0
	s_add_i32 s29, s66, s31
	global_load_lds_dwordx4 v[224:225], off
	v_lshl_add_u64 v[224:225], s[40:41], 0, v[134:135]
	s_mov_b32 m0, s29
	v_lshl_add_u64 v[150:151], v[150:151], 0, s[10:11]
	global_load_lds_dwordx4 v[224:225], off
	v_lshl_add_u64 v[224:225], s[40:41], 0, v[130:131]
	s_add_i32 m0, s29, 0x2000
	s_nop 0
	global_load_lds_dwordx4 v[224:225], off
	s_mov_b32 m0, s54
	s_nop 0
	global_load_lds_dwordx4 v[150:151], off
	v_lshl_add_u64 v[150:151], v[168:169], 0, s[10:11]
	s_mov_b32 m0, s55
	s_nop 0
	global_load_lds_dwordx4 v[150:151], off
	s_waitcnt vmcnt(8)
	s_waitcnt lgkmcnt(0)
	s_barrier
	s_setprio 1
	v_mfma_f32_16x16x32_bf16 v[62:65], v[156:159], v[192:195], v[62:65]
	v_mfma_f32_16x16x32_bf16 v[58:61], v[164:167], v[192:195], v[58:61]
	v_mfma_f32_16x16x32_bf16 v[54:57], v[156:159], v[200:203], v[54:57]
	v_mfma_f32_16x16x32_bf16 v[50:53], v[164:167], v[200:203], v[50:53]
	v_mfma_f32_16x16x32_bf16 v[30:33], v[156:159], v[208:211], v[30:33]
	v_mfma_f32_16x16x32_bf16 v[26:29], v[164:167], v[208:211], v[26:29]
	v_mfma_f32_16x16x32_bf16 v[22:25], v[156:159], v[216:219], v[22:25]
	v_mfma_f32_16x16x32_bf16 v[18:21], v[164:167], v[216:219], v[18:21]
	v_mfma_f32_16x16x32_bf16 v[62:65], v[160:163], v[196:199], v[62:65]
	v_mfma_f32_16x16x32_bf16 v[58:61], v[172:175], v[196:199], v[58:61]
	v_mfma_f32_16x16x32_bf16 v[54:57], v[160:163], v[204:207], v[54:57]
	v_mfma_f32_16x16x32_bf16 v[50:53], v[172:175], v[204:207], v[50:53]
	v_mfma_f32_16x16x32_bf16 v[30:33], v[160:163], v[212:215], v[30:33]
	v_mfma_f32_16x16x32_bf16 v[26:29], v[172:175], v[212:215], v[26:29]
	v_mfma_f32_16x16x32_bf16 v[22:25], v[160:163], v[220:223], v[22:25]
	v_mfma_f32_16x16x32_bf16 v[18:21], v[172:175], v[220:223], v[18:21]
	s_setprio 0
	s_setprio 1
	v_mfma_f32_16x16x32_bf16 v[46:49], v[176:179], v[192:195], v[46:49]
	v_mfma_f32_16x16x32_bf16 v[42:45], v[184:187], v[192:195], v[42:45]
	v_mfma_f32_16x16x32_bf16 v[38:41], v[176:179], v[200:203], v[38:41]
	v_mfma_f32_16x16x32_bf16 v[34:37], v[184:187], v[200:203], v[34:37]
	v_mfma_f32_16x16x32_bf16 v[14:17], v[176:179], v[208:211], v[14:17]
	v_mfma_f32_16x16x32_bf16 v[10:13], v[184:187], v[208:211], v[10:13]
	v_mfma_f32_16x16x32_bf16 v[6:9], v[176:179], v[216:219], v[6:9]
	v_mfma_f32_16x16x32_bf16 v[2:5], v[184:187], v[216:219], v[2:5]
	v_mfma_f32_16x16x32_bf16 v[46:49], v[180:183], v[196:199], v[46:49]
	v_mfma_f32_16x16x32_bf16 v[42:45], v[188:191], v[196:199], v[42:45]
	v_mfma_f32_16x16x32_bf16 v[38:41], v[180:183], v[204:207], v[38:41]
	v_mfma_f32_16x16x32_bf16 v[34:37], v[188:191], v[204:207], v[34:37]
	v_mfma_f32_16x16x32_bf16 v[14:17], v[180:183], v[212:215], v[14:17]
	v_mfma_f32_16x16x32_bf16 v[10:13], v[188:191], v[212:215], v[10:13]
	v_mfma_f32_16x16x32_bf16 v[6:9], v[180:183], v[220:223], v[6:9]
	v_mfma_f32_16x16x32_bf16 v[2:5], v[188:191], v[220:223], v[2:5]
	s_setprio 0
	s_barrier
	s_add_i32 s28, s28, 2
	s_add_u32 s64, s64, 0x10000
	s_addc_u32 s65, s65, 0
	s_add_u32 s44, s44, 0x100
	s_addc_u32 s45, s45, 0
	s_cmp_gt_u32 s28, 13
	s_cbranch_scc0 .LBB0_739
	s_and_b64 vcc, exec, s[12:13]
	s_cbranch_vccz .LBB0_742
	s_barrier

.LBB0_824:
	ds_read_b128 v[130:133], v179
	ds_read_b128 v[134:137], v179 offset:1024
	ds_read_b128 v[138:141], v179 offset:2048
	ds_read_b128 v[142:145], v179 offset:3072
	ds_read_b128 v[162:165], v180
	ds_read_b128 v[166:169], v180 offset:1024
	ds_read_b128 v[172:175], v180 offset:2048
	ds_read_b128 v[182:185], v180 offset:3072
	s_add_i32 s29, s28, 2
	s_add_u32 s40, s46, 0x4000
	s_addc_u32 s41, s47, 0
	s_cmp_eq_u32 s73, s28
	s_cselect_b32 s52, s42, s40
	s_cselect_b32 s53, s43, s41
	s_cselect_b32 s50, s44, s76
	s_cselect_b32 s51, s45, s77
	s_add_u32 s48, s52, 0x8000
	s_addc_u32 s49, s53, 0
	v_lshl_add_u64 v[176:177], s[46:47], 0, v[154:155]
	s_add_i32 m0, s57, 0xc000
	ds_read_b128 v[186:189], v181
	ds_read_b128 v[190:193], v181 offset:1024
	ds_read_b128 v[194:197], v181 offset:2048
	ds_read_b128 v[198:201], v181 offset:3072
	ds_read_b128 v[202:205], v181 offset:4096
	ds_read_b128 v[206:209], v181 offset:5120
	ds_read_b128 v[210:213], v181 offset:6144
	ds_read_b128 v[214:217], v181 offset:7168
	global_load_lds_dwordx4 v[176:177], off
	v_lshl_add_u64 v[176:177], s[46:47], 0, v[156:157]
	s_add_i32 m0, s57, 0xe000
	s_nop 0
	global_load_lds_dwordx4 v[176:177], off
	s_waitcnt vmcnt(8)
	s_waitcnt lgkmcnt(0)
	s_barrier
	s_setprio 1
	v_mfma_f32_16x16x32_bf16 v[126:129], v[130:133], v[186:189], v[126:129]
	v_mfma_f32_16x16x32_bf16 v[122:125], v[138:141], v[186:189], v[122:125]
	v_mfma_f32_16x16x32_bf16 v[118:121], v[130:133], v[194:197], v[118:121]
	v_mfma_f32_16x16x32_bf16 v[110:113], v[138:141], v[194:197], v[110:113]
	v_mfma_f32_16x16x32_bf16 v[102:105], v[130:133], v[202:205], v[102:105]
	v_mfma_f32_16x16x32_bf16 v[94:97], v[138:141], v[202:205], v[94:97]
	v_mfma_f32_16x16x32_bf16 v[86:89], v[130:133], v[210:213], v[86:89]
	v_mfma_f32_16x16x32_bf16 v[78:81], v[138:141], v[210:213], v[78:81]
	v_mfma_f32_16x16x32_bf16 v[126:129], v[134:137], v[190:193], v[126:129]
	v_mfma_f32_16x16x32_bf16 v[122:125], v[142:145], v[190:193], v[122:125]
	v_mfma_f32_16x16x32_bf16 v[118:121], v[134:137], v[198:201], v[118:121]
	v_mfma_f32_16x16x32_bf16 v[110:113], v[142:145], v[198:201], v[110:113]
	v_mfma_f32_16x16x32_bf16 v[102:105], v[134:137], v[206:209], v[102:105]
	v_mfma_f32_16x16x32_bf16 v[94:97], v[142:145], v[206:209], v[94:97]
	v_mfma_f32_16x16x32_bf16 v[86:89], v[134:137], v[214:217], v[86:89]
	v_mfma_f32_16x16x32_bf16 v[78:81], v[142:145], v[214:217], v[78:81]
	s_setprio 0
	s_setprio 1
	v_mfma_f32_16x16x32_bf16 v[114:117], v[162:165], v[186:189], v[114:117]
	v_mfma_f32_16x16x32_bf16 v[106:109], v[172:175], v[186:189], v[106:109]
	v_mfma_f32_16x16x32_bf16 v[98:101], v[162:165], v[194:197], v[98:101]
	v_mfma_f32_16x16x32_bf16 v[90:93], v[172:175], v[194:197], v[90:93]
	v_mfma_f32_16x16x32_bf16 v[82:85], v[162:165], v[202:205], v[82:85]
	v_mfma_f32_16x16x32_bf16 v[74:77], v[172:175], v[202:205], v[74:77]
	v_mfma_f32_16x16x32_bf16 v[70:73], v[162:165], v[210:213], v[70:73]
	v_mfma_f32_16x16x32_bf16 v[66:69], v[172:175], v[210:213], v[66:69]
	v_mfma_f32_16x16x32_bf16 v[114:117], v[166:169], v[190:193], v[114:117]
	v_mfma_f32_16x16x32_bf16 v[106:109], v[182:185], v[190:193], v[106:109]
	v_mfma_f32_16x16x32_bf16 v[98:101], v[166:169], v[198:201], v[98:101]
	v_mfma_f32_16x16x32_bf16 v[90:93], v[182:185], v[198:201], v[90:93]
	v_mfma_f32_16x16x32_bf16 v[82:85], v[166:169], v[206:209], v[82:85]
	v_mfma_f32_16x16x32_bf16 v[74:77], v[182:185], v[206:209], v[74:77]
	v_mfma_f32_16x16x32_bf16 v[70:73], v[166:169], v[214:217], v[70:73]
	v_mfma_f32_16x16x32_bf16 v[66:69], v[182:185], v[214:217], v[66:69]
	s_setprio 0
	s_barrier
	s_add_i32 s28, s65, s56
	v_lshl_add_u64 v[176:177], s[50:51], 0, v[148:149]
	s_mov_b32 m0, s28
	ds_read_b128 v[186:189], v181 offset:16384
	ds_read_b128 v[190:193], v181 offset:17408
	ds_read_b128 v[194:197], v181 offset:18432
	ds_read_b128 v[198:201], v181 offset:19456
	ds_read_b128 v[202:205], v181 offset:20480
	ds_read_b128 v[206:209], v181 offset:21504
	ds_read_b128 v[210:213], v181 offset:22528
	ds_read_b128 v[214:217], v181 offset:23552
	global_load_lds_dwordx4 v[176:177], off
	s_add_i32 m0, s28, 0x2000
	s_add_u32 s40, s50, 0x4000
	v_lshl_add_u64 v[176:177], s[50:51], 0, v[152:153]
	s_addc_u32 s41, s51, 0
	s_add_i32 s28, s66, s56
	global_load_lds_dwordx4 v[176:177], off
	v_lshl_add_u64 v[176:177], s[40:41], 0, v[148:149]
	s_mov_b32 m0, s28
	s_nop 0
	global_load_lds_dwordx4 v[176:177], off
	v_lshl_add_u64 v[176:177], s[40:41], 0, v[152:153]
	s_add_i32 m0, s28, 0x2000
	s_nop 0
	global_load_lds_dwordx4 v[176:177], off
	v_lshl_add_u64 v[176:177], s[52:53], 0, v[146:147]
	s_mov_b32 m0, s57
	s_nop 0
	global_load_lds_dwordx4 v[176:177], off
	v_lshl_add_u64 v[176:177], s[52:53], 0, v[150:151]
	s_mov_b32 m0, s58
	s_nop 0
	global_load_lds_dwordx4 v[176:177], off
	s_waitcnt vmcnt(8)
	s_waitcnt lgkmcnt(0)
	s_barrier
	s_setprio 1
	v_mfma_f32_16x16x32_bf16 v[62:65], v[130:133], v[186:189], v[62:65]
	v_mfma_f32_16x16x32_bf16 v[58:61], v[138:141], v[186:189], v[58:61]
	v_mfma_f32_16x16x32_bf16 v[54:57], v[130:133], v[194:197], v[54:57]
	v_mfma_f32_16x16x32_bf16 v[46:49], v[138:141], v[194:197], v[46:49]
	v_mfma_f32_16x16x32_bf16 v[38:41], v[130:133], v[202:205], v[38:41]
	v_mfma_f32_16x16x32_bf16 v[30:33], v[138:141], v[202:205], v[30:33]
	v_mfma_f32_16x16x32_bf16 v[22:25], v[130:133], v[210:213], v[22:25]
	v_mfma_f32_16x16x32_bf16 v[14:17], v[138:141], v[210:213], v[14:17]
	v_mfma_f32_16x16x32_bf16 v[62:65], v[134:137], v[190:193], v[62:65]
	v_mfma_f32_16x16x32_bf16 v[58:61], v[142:145], v[190:193], v[58:61]
	v_mfma_f32_16x16x32_bf16 v[54:57], v[134:137], v[198:201], v[54:57]
	v_mfma_f32_16x16x32_bf16 v[46:49], v[142:145], v[198:201], v[46:49]
	v_mfma_f32_16x16x32_bf16 v[38:41], v[134:137], v[206:209], v[38:41]
	v_mfma_f32_16x16x32_bf16 v[30:33], v[142:145], v[206:209], v[30:33]
	v_mfma_f32_16x16x32_bf16 v[22:25], v[134:137], v[214:217], v[22:25]
	v_mfma_f32_16x16x32_bf16 v[14:17], v[142:145], v[214:217], v[14:17]
	s_setprio 0
	s_setprio 1
	v_mfma_f32_16x16x32_bf16 v[50:53], v[162:165], v[186:189], v[50:53]
	v_mfma_f32_16x16x32_bf16 v[42:45], v[172:175], v[186:189], v[42:45]
	v_mfma_f32_16x16x32_bf16 v[34:37], v[162:165], v[194:197], v[34:37]
	v_mfma_f32_16x16x32_bf16 v[26:29], v[172:175], v[194:197], v[26:29]
	v_mfma_f32_16x16x32_bf16 v[18:21], v[162:165], v[202:205], v[18:21]
	v_mfma_f32_16x16x32_bf16 v[10:13], v[172:175], v[202:205], v[10:13]
	v_mfma_f32_16x16x32_bf16 v[6:9], v[162:165], v[210:213], v[6:9]
	v_mfma_f32_16x16x32_bf16 v[2:5], v[172:175], v[210:213], v[2:5]
	v_mfma_f32_16x16x32_bf16 v[50:53], v[166:169], v[190:193], v[50:53]
	v_mfma_f32_16x16x32_bf16 v[42:45], v[182:185], v[190:193], v[42:45]
	v_mfma_f32_16x16x32_bf16 v[34:37], v[166:169], v[198:201], v[34:37]
	v_mfma_f32_16x16x32_bf16 v[26:29], v[182:185], v[198:201], v[26:29]
	v_mfma_f32_16x16x32_bf16 v[18:21], v[166:169], v[206:209], v[18:21]
	v_mfma_f32_16x16x32_bf16 v[10:13], v[182:185], v[206:209], v[10:13]
	v_mfma_f32_16x16x32_bf16 v[6:9], v[166:169], v[214:217], v[6:9]
	v_mfma_f32_16x16x32_bf16 v[2:5], v[182:185], v[214:217], v[2:5]
	s_setprio 0
	s_barrier
	s_add_i32 s28, 0, 0x18000
	s_add_i32 s78, 0, 0x1c000
	v_add_u32_e32 v142, s28, v171
	v_add_u32_e32 v176, s78, v171
	ds_read_b128 v[130:133], v142
	ds_read_b128 v[134:137], v142 offset:1024
	ds_read_b128 v[138:141], v142 offset:2048
	ds_read_b128 v[142:145], v142 offset:3072
	ds_read_b128 v[162:165], v176
	ds_read_b128 v[166:169], v176 offset:1024
	ds_read_b128 v[172:175], v176 offset:2048
	ds_read_b128 v[182:185], v176 offset:3072
	s_add_u32 s40, s52, 0x4000
	s_addc_u32 s41, s53, 0
	s_mov_b32 m0, s59
	v_lshl_add_u64 v[176:177], s[40:41], 0, v[146:147]
	ds_read_b128 v[186:189], v181 offset:32768
	ds_read_b128 v[190:193], v181 offset:33792
	ds_read_b128 v[194:197], v181 offset:34816
	ds_read_b128 v[198:201], v181 offset:35840
	ds_read_b128 v[202:205], v181 offset:36864
	ds_read_b128 v[206:209], v181 offset:37888
	ds_read_b128 v[210:213], v181 offset:38912
	ds_read_b128 v[214:217], v181 offset:39936
	global_load_lds_dwordx4 v[176:177], off
	v_lshl_add_u64 v[176:177], s[40:41], 0, v[150:151]
	s_mov_b32 m0, s60
	s_nop 0
	global_load_lds_dwordx4 v[176:177], off
	s_waitcnt vmcnt(8)
	s_waitcnt lgkmcnt(0)
	s_barrier
	s_setprio 1
	v_mfma_f32_16x16x32_bf16 v[126:129], v[130:133], v[186:189], v[126:129]
	v_mfma_f32_16x16x32_bf16 v[122:125], v[138:141], v[186:189], v[122:125]
	v_mfma_f32_16x16x32_bf16 v[118:121], v[130:133], v[194:197], v[118:121]
	v_mfma_f32_16x16x32_bf16 v[110:113], v[138:141], v[194:197], v[110:113]
	v_mfma_f32_16x16x32_bf16 v[102:105], v[130:133], v[202:205], v[102:105]
	v_mfma_f32_16x16x32_bf16 v[94:97], v[138:141], v[202:205], v[94:97]
	v_mfma_f32_16x16x32_bf16 v[86:89], v[130:133], v[210:213], v[86:89]
	v_mfma_f32_16x16x32_bf16 v[78:81], v[138:141], v[210:213], v[78:81]
	v_mfma_f32_16x16x32_bf16 v[126:129], v[134:137], v[190:193], v[126:129]
	v_mfma_f32_16x16x32_bf16 v[122:125], v[142:145], v[190:193], v[122:125]
	v_mfma_f32_16x16x32_bf16 v[118:121], v[134:137], v[198:201], v[118:121]
	v_mfma_f32_16x16x32_bf16 v[110:113], v[142:145], v[198:201], v[110:113]
	v_mfma_f32_16x16x32_bf16 v[102:105], v[134:137], v[206:209], v[102:105]
	v_mfma_f32_16x16x32_bf16 v[94:97], v[142:145], v[206:209], v[94:97]
	v_mfma_f32_16x16x32_bf16 v[86:89], v[134:137], v[214:217], v[86:89]
	v_mfma_f32_16x16x32_bf16 v[78:81], v[142:145], v[214:217], v[78:81]
	s_setprio 0
	s_setprio 1
	v_mfma_f32_16x16x32_bf16 v[114:117], v[162:165], v[186:189], v[114:117]
	v_mfma_f32_16x16x32_bf16 v[106:109], v[172:175], v[186:189], v[106:109]
	v_mfma_f32_16x16x32_bf16 v[98:101], v[162:165], v[194:197], v[98:101]
	v_mfma_f32_16x16x32_bf16 v[90:93], v[172:175], v[194:197], v[90:93]
	v_mfma_f32_16x16x32_bf16 v[82:85], v[162:165], v[202:205], v[82:85]
	v_mfma_f32_16x16x32_bf16 v[74:77], v[172:175], v[202:205], v[74:77]
	v_mfma_f32_16x16x32_bf16 v[70:73], v[162:165], v[210:213], v[70:73]
	v_mfma_f32_16x16x32_bf16 v[66:69], v[172:175], v[210:213], v[66:69]
	v_mfma_f32_16x16x32_bf16 v[114:117], v[166:169], v[190:193], v[114:117]
	v_mfma_f32_16x16x32_bf16 v[106:109], v[182:185], v[190:193], v[106:109]
	v_mfma_f32_16x16x32_bf16 v[98:101], v[166:169], v[198:201], v[98:101]
	v_mfma_f32_16x16x32_bf16 v[90:93], v[182:185], v[198:201], v[90:93]
	v_mfma_f32_16x16x32_bf16 v[82:85], v[166:169], v[206:209], v[82:85]
	v_mfma_f32_16x16x32_bf16 v[74:77], v[182:185], v[206:209], v[74:77]
	v_mfma_f32_16x16x32_bf16 v[70:73], v[166:169], v[214:217], v[70:73]
	v_mfma_f32_16x16x32_bf16 v[66:69], v[182:185], v[214:217], v[66:69]
	s_setprio 0
	s_barrier
	s_add_u32 s40, s50, 0x8000
	s_addc_u32 s41, s51, 0
	s_add_i32 s28, s28, s56
	v_lshl_add_u64 v[176:177], s[40:41], 0, v[148:149]
	s_mov_b32 m0, s28
	ds_read_b128 v[186:189], v181 offset:49152
	ds_read_b128 v[190:193], v181 offset:50176
	ds_read_b128 v[194:197], v181 offset:51200
	ds_read_b128 v[198:201], v181 offset:52224
	ds_read_b128 v[202:205], v181 offset:53248
	ds_read_b128 v[206:209], v181 offset:54272
	ds_read_b128 v[210:213], v181 offset:55296
	ds_read_b128 v[214:217], v181 offset:56320
	global_load_lds_dwordx4 v[176:177], off
	s_add_i32 m0, s28, 0x2000
	v_lshl_add_u64 v[176:177], s[40:41], 0, v[152:153]
	s_add_u32 s40, s50, 0xc000
	s_addc_u32 s41, s51, 0
	s_add_i32 s28, s78, s56
	global_load_lds_dwordx4 v[176:177], off
	v_lshl_add_u64 v[176:177], s[40:41], 0, v[148:149]
	s_mov_b32 m0, s28
	s_nop 0
	global_load_lds_dwordx4 v[176:177], off
	v_lshl_add_u64 v[176:177], s[40:41], 0, v[152:153]
	s_add_i32 m0, s28, 0x2000
	s_nop 0
	global_load_lds_dwordx4 v[176:177], off
	v_lshl_add_u64 v[176:177], s[48:49], 0, v[146:147]
	s_mov_b32 m0, s30
	s_nop 0
	global_load_lds_dwordx4 v[176:177], off
	v_lshl_add_u64 v[176:177], s[48:49], 0, v[150:151]
	s_mov_b32 m0, s31
	s_nop 0
	global_load_lds_dwordx4 v[176:177], off
	s_waitcnt vmcnt(8)
	s_waitcnt lgkmcnt(0)
	s_barrier
	s_setprio 1
	v_mfma_f32_16x16x32_bf16 v[62:65], v[130:133], v[186:189], v[62:65]
	v_mfma_f32_16x16x32_bf16 v[58:61], v[138:141], v[186:189], v[58:61]
	v_mfma_f32_16x16x32_bf16 v[54:57], v[130:133], v[194:197], v[54:57]
	v_mfma_f32_16x16x32_bf16 v[46:49], v[138:141], v[194:197], v[46:49]
	v_mfma_f32_16x16x32_bf16 v[38:41], v[130:133], v[202:205], v[38:41]
	v_mfma_f32_16x16x32_bf16 v[30:33], v[138:141], v[202:205], v[30:33]
	v_mfma_f32_16x16x32_bf16 v[22:25], v[130:133], v[210:213], v[22:25]
	v_mfma_f32_16x16x32_bf16 v[14:17], v[138:141], v[210:213], v[14:17]
	v_mfma_f32_16x16x32_bf16 v[62:65], v[134:137], v[190:193], v[62:65]
	v_mfma_f32_16x16x32_bf16 v[58:61], v[142:145], v[190:193], v[58:61]
	v_mfma_f32_16x16x32_bf16 v[54:57], v[134:137], v[198:201], v[54:57]
	v_mfma_f32_16x16x32_bf16 v[46:49], v[142:145], v[198:201], v[46:49]
	v_mfma_f32_16x16x32_bf16 v[38:41], v[134:137], v[206:209], v[38:41]
	v_mfma_f32_16x16x32_bf16 v[30:33], v[142:145], v[206:209], v[30:33]
	v_mfma_f32_16x16x32_bf16 v[22:25], v[134:137], v[214:217], v[22:25]
	v_mfma_f32_16x16x32_bf16 v[14:17], v[142:145], v[214:217], v[14:17]
	s_setprio 0
	s_setprio 1
	v_mfma_f32_16x16x32_bf16 v[50:53], v[162:165], v[186:189], v[50:53]
	v_mfma_f32_16x16x32_bf16 v[42:45], v[172:175], v[186:189], v[42:45]
	v_mfma_f32_16x16x32_bf16 v[34:37], v[162:165], v[194:197], v[34:37]
	v_mfma_f32_16x16x32_bf16 v[26:29], v[172:175], v[194:197], v[26:29]
	v_mfma_f32_16x16x32_bf16 v[18:21], v[162:165], v[202:205], v[18:21]
	v_mfma_f32_16x16x32_bf16 v[10:13], v[172:175], v[202:205], v[10:13]
	v_mfma_f32_16x16x32_bf16 v[6:9], v[162:165], v[210:213], v[6:9]
	v_mfma_f32_16x16x32_bf16 v[2:5], v[172:175], v[210:213], v[2:5]
	v_mfma_f32_16x16x32_bf16 v[50:53], v[166:169], v[190:193], v[50:53]
	v_mfma_f32_16x16x32_bf16 v[42:45], v[182:185], v[190:193], v[42:45]
	v_mfma_f32_16x16x32_bf16 v[34:37], v[166:169], v[198:201], v[34:37]
	v_mfma_f32_16x16x32_bf16 v[26:29], v[182:185], v[198:201], v[26:29]
	v_mfma_f32_16x16x32_bf16 v[18:21], v[166:169], v[206:209], v[18:21]
	v_mfma_f32_16x16x32_bf16 v[10:13], v[182:185], v[206:209], v[10:13]
	v_mfma_f32_16x16x32_bf16 v[6:9], v[166:169], v[214:217], v[6:9]
	v_mfma_f32_16x16x32_bf16 v[2:5], v[182:185], v[214:217], v[2:5]
	s_setprio 0
	s_barrier
	s_add_u32 s46, s46, 0x10000
	s_addc_u32 s47, s47, 0
	s_add_u32 s76, s76, 0x10000
	s_addc_u32 s77, s77, 0
	s_cmp_ge_u32 s29, s23
	s_mov_b32 s28, s29
	s_cbranch_scc0 .LBB0_824
	s_and_b64 vcc, exec, s[12:13]
	s_cbranch_vccz .LBB0_827
	s_barrier

.LBB0_958:
	ds_read_b128 v[152:155], v148
	ds_read_b128 v[156:159], v148 offset:1024
	ds_read_b128 v[160:163], v148 offset:2048
	ds_read_b128 v[164:167], v148 offset:3072
	ds_read_b128 v[172:175], v149
	ds_read_b128 v[176:179], v149 offset:1024
	ds_read_b128 v[180:183], v149 offset:2048
	ds_read_b128 v[184:187], v149 offset:3072
	s_add_u32 s29, s42, 0xfffc0080
	s_addc_u32 s40, s43, -1
	s_cmp_eq_u32 s28, 12
	s_cselect_b32 s47, s19, s40
	s_cselect_b32 s46, s56, s29
	s_cselect_b32 s45, s17, s59
	s_cselect_b32 s44, s57, s58
	v_lshl_add_u64 v[168:169], s[42:43], 0, v[138:139]
	s_add_i32 m0, s11, 0xc000
	ds_read_b128 v[188:191], v150
	ds_read_b128 v[192:195], v150 offset:1024
	ds_read_b128 v[196:199], v150 offset:2048
	ds_read_b128 v[200:203], v150 offset:3072
	ds_read_b128 v[204:207], v150 offset:4096
	ds_read_b128 v[208:211], v150 offset:5120
	ds_read_b128 v[212:215], v150 offset:6144
	ds_read_b128 v[216:219], v150 offset:7168
	global_load_lds_dwordx4 v[168:169], off
	v_lshl_add_u64 v[168:169], s[42:43], 0, v[140:141]
	s_add_i32 m0, s11, 0xe000
	s_nop 0
	global_load_lds_dwordx4 v[168:169], off
	s_waitcnt vmcnt(8)
	s_waitcnt lgkmcnt(0)
	s_barrier
	s_setprio 1
	v_mfma_f32_16x16x32_bf16 v[126:129], v[152:155], v[188:191], v[126:129]
	v_mfma_f32_16x16x32_bf16 v[122:125], v[160:163], v[188:191], v[122:125]
	v_mfma_f32_16x16x32_bf16 v[118:121], v[152:155], v[196:199], v[118:121]
	v_mfma_f32_16x16x32_bf16 v[114:117], v[160:163], v[196:199], v[114:117]
	v_mfma_f32_16x16x32_bf16 v[110:113], v[152:155], v[204:207], v[110:113]
	v_mfma_f32_16x16x32_bf16 v[106:109], v[160:163], v[204:207], v[106:109]
	v_mfma_f32_16x16x32_bf16 v[94:97], v[152:155], v[212:215], v[94:97]
	v_mfma_f32_16x16x32_bf16 v[90:93], v[160:163], v[212:215], v[90:93]
	v_mfma_f32_16x16x32_bf16 v[126:129], v[156:159], v[192:195], v[126:129]
	v_mfma_f32_16x16x32_bf16 v[122:125], v[164:167], v[192:195], v[122:125]
	v_mfma_f32_16x16x32_bf16 v[118:121], v[156:159], v[200:203], v[118:121]
	v_mfma_f32_16x16x32_bf16 v[114:117], v[164:167], v[200:203], v[114:117]
	v_mfma_f32_16x16x32_bf16 v[110:113], v[156:159], v[208:211], v[110:113]
	v_mfma_f32_16x16x32_bf16 v[106:109], v[164:167], v[208:211], v[106:109]
	v_mfma_f32_16x16x32_bf16 v[94:97], v[156:159], v[216:219], v[94:97]
	v_mfma_f32_16x16x32_bf16 v[90:93], v[164:167], v[216:219], v[90:93]
	s_setprio 0
	s_setprio 1
	v_mfma_f32_16x16x32_bf16 v[102:105], v[172:175], v[188:191], v[102:105]
	v_mfma_f32_16x16x32_bf16 v[98:101], v[180:183], v[188:191], v[98:101]
	v_mfma_f32_16x16x32_bf16 v[86:89], v[172:175], v[196:199], v[86:89]
	v_mfma_f32_16x16x32_bf16 v[82:85], v[180:183], v[196:199], v[82:85]
	v_mfma_f32_16x16x32_bf16 v[78:81], v[172:175], v[204:207], v[78:81]
	v_mfma_f32_16x16x32_bf16 v[74:77], v[180:183], v[204:207], v[74:77]
	v_mfma_f32_16x16x32_bf16 v[70:73], v[172:175], v[212:215], v[70:73]
	v_mfma_f32_16x16x32_bf16 v[66:69], v[180:183], v[212:215], v[66:69]
	v_mfma_f32_16x16x32_bf16 v[102:105], v[176:179], v[192:195], v[102:105]
	v_mfma_f32_16x16x32_bf16 v[98:101], v[184:187], v[192:195], v[98:101]
	v_mfma_f32_16x16x32_bf16 v[86:89], v[176:179], v[200:203], v[86:89]
	v_mfma_f32_16x16x32_bf16 v[82:85], v[184:187], v[200:203], v[82:85]
	v_mfma_f32_16x16x32_bf16 v[78:81], v[176:179], v[208:211], v[78:81]
	v_mfma_f32_16x16x32_bf16 v[74:77], v[184:187], v[208:211], v[74:77]
	v_mfma_f32_16x16x32_bf16 v[70:73], v[176:179], v[216:219], v[70:73]
	v_mfma_f32_16x16x32_bf16 v[66:69], v[184:187], v[216:219], v[66:69]
	s_setprio 0
	s_barrier
	s_add_i32 s29, s52, s31
	v_lshl_add_u64 v[168:169], s[44:45], 0, v[134:135]
	s_mov_b32 m0, s29
	ds_read_b128 v[188:191], v150 offset:16384
	ds_read_b128 v[192:195], v150 offset:17408
	ds_read_b128 v[196:199], v150 offset:18432
	ds_read_b128 v[200:203], v150 offset:19456
	ds_read_b128 v[204:207], v150 offset:20480
	ds_read_b128 v[208:211], v150 offset:21504
	ds_read_b128 v[212:215], v150 offset:22528
	ds_read_b128 v[216:219], v150 offset:23552
	global_load_lds_dwordx4 v[168:169], off
	s_add_i32 m0, s29, 0x2000
	s_add_u32 s40, s44, 0x4000
	v_lshl_add_u64 v[168:169], s[44:45], 0, v[130:131]
	s_addc_u32 s41, s45, 0
	s_add_i32 s29, s53, s31
	global_load_lds_dwordx4 v[168:169], off
	v_lshl_add_u64 v[168:169], s[40:41], 0, v[134:135]
	s_mov_b32 m0, s29
	v_lshl_add_u64 v[220:221], s[46:47], 0, v[132:133]
	global_load_lds_dwordx4 v[168:169], off
	v_lshl_add_u64 v[168:169], s[40:41], 0, v[130:131]
	s_add_i32 m0, s29, 0x2000
	s_nop 0
	global_load_lds_dwordx4 v[168:169], off
	v_lshl_add_u64 v[168:169], s[46:47], 0, v[136:137]
	s_mov_b32 m0, s11
	s_nop 0
	global_load_lds_dwordx4 v[168:169], off
	s_mov_b32 m0, s35
	s_nop 0
	global_load_lds_dwordx4 v[220:221], off
	s_waitcnt vmcnt(8)
	s_waitcnt lgkmcnt(0)
	s_barrier
	s_setprio 1
	v_mfma_f32_16x16x32_bf16 v[62:65], v[152:155], v[188:191], v[62:65]
	v_mfma_f32_16x16x32_bf16 v[58:61], v[160:163], v[188:191], v[58:61]
	v_mfma_f32_16x16x32_bf16 v[54:57], v[152:155], v[196:199], v[54:57]
	v_mfma_f32_16x16x32_bf16 v[50:53], v[160:163], v[196:199], v[50:53]
	v_mfma_f32_16x16x32_bf16 v[46:49], v[152:155], v[204:207], v[46:49]
	v_mfma_f32_16x16x32_bf16 v[42:45], v[160:163], v[204:207], v[42:45]
	v_mfma_f32_16x16x32_bf16 v[30:33], v[152:155], v[212:215], v[30:33]
	v_mfma_f32_16x16x32_bf16 v[26:29], v[160:163], v[212:215], v[26:29]
	v_mfma_f32_16x16x32_bf16 v[62:65], v[156:159], v[192:195], v[62:65]
	v_mfma_f32_16x16x32_bf16 v[58:61], v[164:167], v[192:195], v[58:61]
	v_mfma_f32_16x16x32_bf16 v[54:57], v[156:159], v[200:203], v[54:57]
	v_mfma_f32_16x16x32_bf16 v[50:53], v[164:167], v[200:203], v[50:53]
	v_mfma_f32_16x16x32_bf16 v[46:49], v[156:159], v[208:211], v[46:49]
	v_mfma_f32_16x16x32_bf16 v[42:45], v[164:167], v[208:211], v[42:45]
	v_mfma_f32_16x16x32_bf16 v[30:33], v[156:159], v[216:219], v[30:33]
	v_mfma_f32_16x16x32_bf16 v[26:29], v[164:167], v[216:219], v[26:29]
	s_setprio 0
	s_setprio 1
	v_mfma_f32_16x16x32_bf16 v[38:41], v[172:175], v[188:191], v[38:41]
	v_mfma_f32_16x16x32_bf16 v[34:37], v[180:183], v[188:191], v[34:37]
	v_mfma_f32_16x16x32_bf16 v[22:25], v[172:175], v[196:199], v[22:25]
	v_mfma_f32_16x16x32_bf16 v[18:21], v[180:183], v[196:199], v[18:21]
	v_mfma_f32_16x16x32_bf16 v[14:17], v[172:175], v[204:207], v[14:17]
	v_mfma_f32_16x16x32_bf16 v[10:13], v[180:183], v[204:207], v[10:13]
	v_mfma_f32_16x16x32_bf16 v[6:9], v[172:175], v[212:215], v[6:9]
	v_mfma_f32_16x16x32_bf16 v[2:5], v[180:183], v[212:215], v[2:5]
	v_mfma_f32_16x16x32_bf16 v[38:41], v[176:179], v[192:195], v[38:41]
	v_mfma_f32_16x16x32_bf16 v[34:37], v[184:187], v[192:195], v[34:37]
	v_mfma_f32_16x16x32_bf16 v[22:25], v[176:179], v[200:203], v[22:25]
	v_mfma_f32_16x16x32_bf16 v[18:21], v[184:187], v[200:203], v[18:21]
	v_mfma_f32_16x16x32_bf16 v[14:17], v[176:179], v[208:211], v[14:17]
	v_mfma_f32_16x16x32_bf16 v[10:13], v[184:187], v[208:211], v[10:13]
	v_mfma_f32_16x16x32_bf16 v[6:9], v[176:179], v[216:219], v[6:9]
	v_mfma_f32_16x16x32_bf16 v[2:5], v[184:187], v[216:219], v[2:5]
	s_setprio 0
	s_barrier
	s_add_i32 s29, 0, 0x18000
	v_add_u32_e32 v151, s29, v146
	s_add_i32 s60, 0, 0x1c000
	ds_read_b128 v[152:155], v151
	ds_read_b128 v[156:159], v151 offset:1024
	ds_read_b128 v[160:163], v151 offset:2048
	ds_read_b128 v[164:167], v151 offset:3072
	v_add_u32_e32 v151, s60, v146
	ds_read_b128 v[172:175], v151
	ds_read_b128 v[176:179], v151 offset:1024
	ds_read_b128 v[180:183], v151 offset:2048
	ds_read_b128 v[184:187], v151 offset:3072
	s_add_u32 s40, s46, 0x40000
	s_addc_u32 s41, s47, 0
	s_mov_b32 m0, s36
	v_lshl_add_u64 v[222:223], s[40:41], 0, v[136:137]
	ds_read_b128 v[188:191], v150 offset:32768
	ds_read_b128 v[192:195], v150 offset:33792
	ds_read_b128 v[196:199], v150 offset:34816
	ds_read_b128 v[200:203], v150 offset:35840
	ds_read_b128 v[204:207], v150 offset:36864
	ds_read_b128 v[208:211], v150 offset:37888
	ds_read_b128 v[212:215], v150 offset:38912
	ds_read_b128 v[216:219], v150 offset:39936
	global_load_lds_dwordx4 v[222:223], off
	v_lshl_add_u64 v[222:223], s[40:41], 0, v[132:133]
	s_mov_b32 m0, s37
	s_nop 0
	global_load_lds_dwordx4 v[222:223], off
	s_waitcnt vmcnt(8)
	s_waitcnt lgkmcnt(0)
	s_barrier
	s_setprio 1
	v_mfma_f32_16x16x32_bf16 v[126:129], v[152:155], v[188:191], v[126:129]
	v_mfma_f32_16x16x32_bf16 v[122:125], v[160:163], v[188:191], v[122:125]
	v_mfma_f32_16x16x32_bf16 v[118:121], v[152:155], v[196:199], v[118:121]
	v_mfma_f32_16x16x32_bf16 v[114:117], v[160:163], v[196:199], v[114:117]
	v_mfma_f32_16x16x32_bf16 v[110:113], v[152:155], v[204:207], v[110:113]
	v_mfma_f32_16x16x32_bf16 v[106:109], v[160:163], v[204:207], v[106:109]
	v_mfma_f32_16x16x32_bf16 v[94:97], v[152:155], v[212:215], v[94:97]
	v_mfma_f32_16x16x32_bf16 v[90:93], v[160:163], v[212:215], v[90:93]
	v_mfma_f32_16x16x32_bf16 v[126:129], v[156:159], v[192:195], v[126:129]
	v_mfma_f32_16x16x32_bf16 v[122:125], v[164:167], v[192:195], v[122:125]
	v_mfma_f32_16x16x32_bf16 v[118:121], v[156:159], v[200:203], v[118:121]
	v_mfma_f32_16x16x32_bf16 v[114:117], v[164:167], v[200:203], v[114:117]
	v_mfma_f32_16x16x32_bf16 v[110:113], v[156:159], v[208:211], v[110:113]
	v_mfma_f32_16x16x32_bf16 v[106:109], v[164:167], v[208:211], v[106:109]
	v_mfma_f32_16x16x32_bf16 v[94:97], v[156:159], v[216:219], v[94:97]
	v_mfma_f32_16x16x32_bf16 v[90:93], v[164:167], v[216:219], v[90:93]
	s_setprio 0
	s_setprio 1
	v_mfma_f32_16x16x32_bf16 v[102:105], v[172:175], v[188:191], v[102:105]
	v_mfma_f32_16x16x32_bf16 v[98:101], v[180:183], v[188:191], v[98:101]
	v_mfma_f32_16x16x32_bf16 v[86:89], v[172:175], v[196:199], v[86:89]
	v_mfma_f32_16x16x32_bf16 v[82:85], v[180:183], v[196:199], v[82:85]
	v_mfma_f32_16x16x32_bf16 v[78:81], v[172:175], v[204:207], v[78:81]
	v_mfma_f32_16x16x32_bf16 v[74:77], v[180:183], v[204:207], v[74:77]
	v_mfma_f32_16x16x32_bf16 v[70:73], v[172:175], v[212:215], v[70:73]
	v_mfma_f32_16x16x32_bf16 v[66:69], v[180:183], v[212:215], v[66:69]
	v_mfma_f32_16x16x32_bf16 v[102:105], v[176:179], v[192:195], v[102:105]
	v_mfma_f32_16x16x32_bf16 v[98:101], v[184:187], v[192:195], v[98:101]
	v_mfma_f32_16x16x32_bf16 v[86:89], v[176:179], v[200:203], v[86:89]
	v_mfma_f32_16x16x32_bf16 v[82:85], v[184:187], v[200:203], v[82:85]
	v_mfma_f32_16x16x32_bf16 v[78:81], v[176:179], v[208:211], v[78:81]
	v_mfma_f32_16x16x32_bf16 v[74:77], v[184:187], v[208:211], v[74:77]
	v_mfma_f32_16x16x32_bf16 v[70:73], v[176:179], v[216:219], v[70:73]
	v_mfma_f32_16x16x32_bf16 v[66:69], v[184:187], v[216:219], v[66:69]
	s_setprio 0
	s_barrier
	s_add_u32 s40, s44, 0x8000
	s_addc_u32 s41, s45, 0
	s_add_i32 s29, s29, s31
	v_lshl_add_u64 v[222:223], s[40:41], 0, v[134:135]
	s_mov_b32 m0, s29
	ds_read_b128 v[188:191], v150 offset:49152
	ds_read_b128 v[192:195], v150 offset:50176
	ds_read_b128 v[196:199], v150 offset:51200
	ds_read_b128 v[200:203], v150 offset:52224
	ds_read_b128 v[204:207], v150 offset:53248
	ds_read_b128 v[208:211], v150 offset:54272
	ds_read_b128 v[212:215], v150 offset:55296
	ds_read_b128 v[216:219], v150 offset:56320
	global_load_lds_dwordx4 v[222:223], off
	s_add_i32 m0, s29, 0x2000
	v_lshl_add_u64 v[222:223], s[40:41], 0, v[130:131]
	s_add_u32 s40, s44, 0xc000
	s_addc_u32 s41, s45, 0
	s_add_i32 s29, s60, s31
	global_load_lds_dwordx4 v[222:223], off
	v_lshl_add_u64 v[222:223], s[40:41], 0, v[134:135]
	s_mov_b32 m0, s29
	v_lshl_add_u64 v[168:169], v[168:169], 0, s[12:13]
	global_load_lds_dwordx4 v[222:223], off
	v_lshl_add_u64 v[222:223], s[40:41], 0, v[130:131]
	s_add_i32 m0, s29, 0x2000
	s_nop 0
	global_load_lds_dwordx4 v[222:223], off
	s_mov_b32 m0, s50
	s_nop 0
	global_load_lds_dwordx4 v[168:169], off
	v_lshl_add_u64 v[168:169], v[220:221], 0, s[12:13]
	s_mov_b32 m0, s51
	s_nop 0
	global_load_lds_dwordx4 v[168:169], off
	s_waitcnt vmcnt(8)
	s_waitcnt lgkmcnt(0)
	s_barrier
	s_setprio 1
	v_mfma_f32_16x16x32_bf16 v[62:65], v[152:155], v[188:191], v[62:65]
	v_mfma_f32_16x16x32_bf16 v[58:61], v[160:163], v[188:191], v[58:61]
	v_mfma_f32_16x16x32_bf16 v[54:57], v[152:155], v[196:199], v[54:57]
	v_mfma_f32_16x16x32_bf16 v[50:53], v[160:163], v[196:199], v[50:53]
	v_mfma_f32_16x16x32_bf16 v[46:49], v[152:155], v[204:207], v[46:49]
	v_mfma_f32_16x16x32_bf16 v[42:45], v[160:163], v[204:207], v[42:45]
	v_mfma_f32_16x16x32_bf16 v[30:33], v[152:155], v[212:215], v[30:33]
	v_mfma_f32_16x16x32_bf16 v[26:29], v[160:163], v[212:215], v[26:29]
	v_mfma_f32_16x16x32_bf16 v[62:65], v[156:159], v[192:195], v[62:65]
	v_mfma_f32_16x16x32_bf16 v[58:61], v[164:167], v[192:195], v[58:61]
	v_mfma_f32_16x16x32_bf16 v[54:57], v[156:159], v[200:203], v[54:57]
	v_mfma_f32_16x16x32_bf16 v[50:53], v[164:167], v[200:203], v[50:53]
	v_mfma_f32_16x16x32_bf16 v[46:49], v[156:159], v[208:211], v[46:49]
	v_mfma_f32_16x16x32_bf16 v[42:45], v[164:167], v[208:211], v[42:45]
	v_mfma_f32_16x16x32_bf16 v[30:33], v[156:159], v[216:219], v[30:33]
	v_mfma_f32_16x16x32_bf16 v[26:29], v[164:167], v[216:219], v[26:29]
	s_setprio 0
	s_setprio 1
	v_mfma_f32_16x16x32_bf16 v[38:41], v[172:175], v[188:191], v[38:41]
	v_mfma_f32_16x16x32_bf16 v[34:37], v[180:183], v[188:191], v[34:37]
	v_mfma_f32_16x16x32_bf16 v[22:25], v[172:175], v[196:199], v[22:25]
	v_mfma_f32_16x16x32_bf16 v[18:21], v[180:183], v[196:199], v[18:21]
	v_mfma_f32_16x16x32_bf16 v[14:17], v[172:175], v[204:207], v[14:17]
	v_mfma_f32_16x16x32_bf16 v[10:13], v[180:183], v[204:207], v[10:13]
	v_mfma_f32_16x16x32_bf16 v[6:9], v[172:175], v[212:215], v[6:9]
	v_mfma_f32_16x16x32_bf16 v[2:5], v[180:183], v[212:215], v[2:5]
	v_mfma_f32_16x16x32_bf16 v[38:41], v[176:179], v[192:195], v[38:41]
	v_mfma_f32_16x16x32_bf16 v[34:37], v[184:187], v[192:195], v[34:37]
	v_mfma_f32_16x16x32_bf16 v[22:25], v[176:179], v[200:203], v[22:25]
	v_mfma_f32_16x16x32_bf16 v[18:21], v[184:187], v[200:203], v[18:21]
	v_mfma_f32_16x16x32_bf16 v[14:17], v[176:179], v[208:211], v[14:17]
	v_mfma_f32_16x16x32_bf16 v[10:13], v[184:187], v[208:211], v[10:13]
	v_mfma_f32_16x16x32_bf16 v[6:9], v[176:179], v[216:219], v[6:9]
	v_mfma_f32_16x16x32_bf16 v[2:5], v[184:187], v[216:219], v[2:5]
	s_setprio 0
	s_barrier
	s_add_i32 s28, s28, 2
	s_add_u32 s58, s58, 0x10000
	s_addc_u32 s59, s59, 0
	s_add_u32 s42, s42, 0x100
	s_addc_u32 s43, s43, 0
	s_cmp_gt_u32 s28, 13
	s_cbranch_scc0 .LBB0_958
	s_and_b64 vcc, exec, s[14:15]
	s_cbranch_vccz .LBB0_961
	s_barrier

.LBB0_1100:
	s_lshl_b32 s19, s6, 7
	s_add_i32 s6, s6, 2
	s_lshl_b64 s[28:29], s[6:7], 7
	s_add_u32 s21, s46, s28
	s_addc_u32 s40, s47, s29
	s_and_b64 s[28:29], s[52:53], exec
	s_cselect_b32 s59, s23, s40
	s_cselect_b32 s58, s22, s21
	s_lshl_b64 s[28:29], s[6:7], 15
	s_add_u32 s6, s48, s28
	s_addc_u32 s21, s49, s29
	s_and_b64 s[28:29], s[52:53], exec
	s_cselect_b32 s61, s43, s21
	s_cselect_b32 s60, s42, s6
	s_add_u32 s6, s46, s19
	s_addc_u32 s19, s47, 0
	s_add_u32 s64, s6, 0x10080
	s_addc_u32 s65, s19, 0
	s_add_i32 s79, s72, s36
	s_add_i32 m0, s33, 0xc000
	s_add_i32 s82, s33, 0xe000
	s_add_i32 s29, s79, 0x2000
	ds_read_b128 v[130:133], v152
	ds_read_b128 v[146:149], v152 offset:1024
	ds_read_b128 v[156:159], v152 offset:2048
	ds_read_b128 v[160:163], v152 offset:3072
	ds_read_b128 v[164:167], v153
	ds_read_b128 v[172:175], v153 offset:1024
	ds_read_b128 v[176:179], v153 offset:2048
	ds_read_b128 v[180:183], v153 offset:3072
	s_add_u32 s62, s60, 0x4000
	s_addc_u32 s63, s61, 0
	s_add_i32 s41, s73, s36
	s_add_i32 s40, s41, 0x2000
	s_add_i32 s28, 0, 0x18000
	s_add_i32 s21, 0, 0x1c000
	s_add_u32 s56, s58, 0x10000
	s_addc_u32 s57, s59, 0
	s_add_u32 s52, s60, 0x8000
	s_addc_u32 s53, s61, 0
	s_add_i32 s19, s28, s36
	s_add_i32 s6, s19, 0x2000
	s_add_u32 s54, s60, 0xc000
	s_addc_u32 s55, s61, 0
	s_add_i32 s81, s21, s36
	s_add_i32 s80, s81, 0x2000
	v_lshl_add_u64 v[168:169], s[64:65], 0, v[134:135]
	ds_read_b128 v[184:187], v154
	ds_read_b128 v[188:191], v154 offset:1024
	ds_read_b128 v[192:195], v154 offset:2048
	ds_read_b128 v[196:199], v154 offset:3072
	ds_read_b128 v[200:203], v154 offset:4096
	ds_read_b128 v[204:207], v154 offset:5120
	ds_read_b128 v[208:211], v154 offset:6144
	ds_read_b128 v[212:215], v154 offset:7168
	global_load_lds_dwordx4 v[168:169], off
	v_lshl_add_u64 v[168:169], s[64:65], 0, v[138:139]
	s_mov_b32 m0, s82
	s_nop 0
	global_load_lds_dwordx4 v[168:169], off
	s_waitcnt vmcnt(8)
	s_waitcnt lgkmcnt(0)
	s_barrier
	s_setprio 1
	v_mfma_f32_16x16x32_bf16 v[126:129], v[130:133], v[184:187], v[126:129]
	v_mfma_f32_16x16x32_bf16 v[122:125], v[156:159], v[184:187], v[122:125]
	v_mfma_f32_16x16x32_bf16 v[118:121], v[130:133], v[192:195], v[118:121]
	v_mfma_f32_16x16x32_bf16 v[110:113], v[156:159], v[192:195], v[110:113]
	v_mfma_f32_16x16x32_bf16 v[102:105], v[130:133], v[200:203], v[102:105]
	v_mfma_f32_16x16x32_bf16 v[94:97], v[156:159], v[200:203], v[94:97]
	v_mfma_f32_16x16x32_bf16 v[86:89], v[130:133], v[208:211], v[86:89]
	v_mfma_f32_16x16x32_bf16 v[78:81], v[156:159], v[208:211], v[78:81]
	v_mfma_f32_16x16x32_bf16 v[126:129], v[146:149], v[188:191], v[126:129]
	v_mfma_f32_16x16x32_bf16 v[122:125], v[160:163], v[188:191], v[122:125]
	v_mfma_f32_16x16x32_bf16 v[118:121], v[146:149], v[196:199], v[118:121]
	v_mfma_f32_16x16x32_bf16 v[110:113], v[160:163], v[196:199], v[110:113]
	v_mfma_f32_16x16x32_bf16 v[102:105], v[146:149], v[204:207], v[102:105]
	v_mfma_f32_16x16x32_bf16 v[94:97], v[160:163], v[204:207], v[94:97]
	v_mfma_f32_16x16x32_bf16 v[86:89], v[146:149], v[212:215], v[86:89]
	v_mfma_f32_16x16x32_bf16 v[78:81], v[160:163], v[212:215], v[78:81]
	s_setprio 0
	s_setprio 1
	v_mfma_f32_16x16x32_bf16 v[114:117], v[164:167], v[184:187], v[114:117]
	v_mfma_f32_16x16x32_bf16 v[106:109], v[176:179], v[184:187], v[106:109]
	v_mfma_f32_16x16x32_bf16 v[98:101], v[164:167], v[192:195], v[98:101]
	v_mfma_f32_16x16x32_bf16 v[90:93], v[176:179], v[192:195], v[90:93]
	v_mfma_f32_16x16x32_bf16 v[82:85], v[164:167], v[200:203], v[82:85]
	v_mfma_f32_16x16x32_bf16 v[74:77], v[176:179], v[200:203], v[74:77]
	v_mfma_f32_16x16x32_bf16 v[70:73], v[164:167], v[208:211], v[70:73]
	v_mfma_f32_16x16x32_bf16 v[66:69], v[176:179], v[208:211], v[66:69]
	v_mfma_f32_16x16x32_bf16 v[114:117], v[172:175], v[188:191], v[114:117]
	v_mfma_f32_16x16x32_bf16 v[106:109], v[180:183], v[188:191], v[106:109]
	v_mfma_f32_16x16x32_bf16 v[98:101], v[172:175], v[196:199], v[98:101]
	v_mfma_f32_16x16x32_bf16 v[90:93], v[180:183], v[196:199], v[90:93]
	v_mfma_f32_16x16x32_bf16 v[82:85], v[172:175], v[204:207], v[82:85]
	v_mfma_f32_16x16x32_bf16 v[74:77], v[180:183], v[204:207], v[74:77]
	v_mfma_f32_16x16x32_bf16 v[70:73], v[172:175], v[212:215], v[70:73]
	v_mfma_f32_16x16x32_bf16 v[66:69], v[180:183], v[212:215], v[66:69]
	s_setprio 0
	s_barrier
	s_mov_b32 m0, s79
	v_lshl_add_u64 v[168:169], s[60:61], 0, v[136:137]
	ds_read_b128 v[184:187], v154 offset:16384
	ds_read_b128 v[188:191], v154 offset:17408
	ds_read_b128 v[192:195], v154 offset:18432
	ds_read_b128 v[196:199], v154 offset:19456
	ds_read_b128 v[200:203], v154 offset:20480
	ds_read_b128 v[204:207], v154 offset:21504
	ds_read_b128 v[208:211], v154 offset:22528
	ds_read_b128 v[212:215], v154 offset:23552
	global_load_lds_dwordx4 v[168:169], off
	v_lshl_add_u64 v[168:169], s[60:61], 0, v[140:141]
	s_mov_b32 m0, s29
	v_lshl_add_u64 v[216:217], s[58:59], 0, v[138:139]
	global_load_lds_dwordx4 v[168:169], off
	v_lshl_add_u64 v[168:169], s[62:63], 0, v[136:137]
	s_mov_b32 m0, s41
	s_nop 0
	global_load_lds_dwordx4 v[168:169], off
	v_lshl_add_u64 v[168:169], s[62:63], 0, v[140:141]
	s_mov_b32 m0, s40
	s_nop 0
	global_load_lds_dwordx4 v[168:169], off
	v_lshl_add_u64 v[168:169], s[58:59], 0, v[134:135]
	s_mov_b32 m0, s33
	s_nop 0
	global_load_lds_dwordx4 v[168:169], off
	s_mov_b32 m0, s37
	s_nop 0
	global_load_lds_dwordx4 v[216:217], off
	s_waitcnt vmcnt(8)
	s_waitcnt lgkmcnt(0)
	s_barrier
	s_setprio 1
	v_mfma_f32_16x16x32_bf16 v[62:65], v[130:133], v[184:187], v[62:65]
	v_mfma_f32_16x16x32_bf16 v[58:61], v[156:159], v[184:187], v[58:61]
	v_mfma_f32_16x16x32_bf16 v[54:57], v[130:133], v[192:195], v[54:57]
	v_mfma_f32_16x16x32_bf16 v[46:49], v[156:159], v[192:195], v[46:49]
	v_mfma_f32_16x16x32_bf16 v[38:41], v[130:133], v[200:203], v[38:41]
	v_mfma_f32_16x16x32_bf16 v[30:33], v[156:159], v[200:203], v[30:33]
	v_mfma_f32_16x16x32_bf16 v[22:25], v[130:133], v[208:211], v[22:25]
	v_mfma_f32_16x16x32_bf16 v[14:17], v[156:159], v[208:211], v[14:17]
	v_mfma_f32_16x16x32_bf16 v[62:65], v[146:149], v[188:191], v[62:65]
	v_mfma_f32_16x16x32_bf16 v[58:61], v[160:163], v[188:191], v[58:61]
	v_mfma_f32_16x16x32_bf16 v[54:57], v[146:149], v[196:199], v[54:57]
	v_mfma_f32_16x16x32_bf16 v[46:49], v[160:163], v[196:199], v[46:49]
	v_mfma_f32_16x16x32_bf16 v[38:41], v[146:149], v[204:207], v[38:41]
	v_mfma_f32_16x16x32_bf16 v[30:33], v[160:163], v[204:207], v[30:33]
	v_mfma_f32_16x16x32_bf16 v[22:25], v[146:149], v[212:215], v[22:25]
	v_mfma_f32_16x16x32_bf16 v[14:17], v[160:163], v[212:215], v[14:17]
	s_setprio 0
	s_setprio 1
	v_mfma_f32_16x16x32_bf16 v[50:53], v[164:167], v[184:187], v[50:53]
	v_mfma_f32_16x16x32_bf16 v[42:45], v[176:179], v[184:187], v[42:45]
	v_mfma_f32_16x16x32_bf16 v[34:37], v[164:167], v[192:195], v[34:37]
	v_mfma_f32_16x16x32_bf16 v[26:29], v[176:179], v[192:195], v[26:29]
	v_mfma_f32_16x16x32_bf16 v[18:21], v[164:167], v[200:203], v[18:21]
	v_mfma_f32_16x16x32_bf16 v[10:13], v[176:179], v[200:203], v[10:13]
	v_mfma_f32_16x16x32_bf16 v[6:9], v[164:167], v[208:211], v[6:9]
	v_mfma_f32_16x16x32_bf16 v[2:5], v[176:179], v[208:211], v[2:5]
	v_mfma_f32_16x16x32_bf16 v[50:53], v[172:175], v[188:191], v[50:53]
	v_mfma_f32_16x16x32_bf16 v[42:45], v[180:183], v[188:191], v[42:45]
	v_mfma_f32_16x16x32_bf16 v[34:37], v[172:175], v[196:199], v[34:37]
	v_mfma_f32_16x16x32_bf16 v[26:29], v[180:183], v[196:199], v[26:29]
	v_mfma_f32_16x16x32_bf16 v[18:21], v[172:175], v[204:207], v[18:21]
	v_mfma_f32_16x16x32_bf16 v[10:13], v[180:183], v[204:207], v[10:13]
	v_mfma_f32_16x16x32_bf16 v[6:9], v[172:175], v[212:215], v[6:9]
	v_mfma_f32_16x16x32_bf16 v[2:5], v[180:183], v[212:215], v[2:5]
	s_setprio 0
	s_barrier
	v_add_u32_e32 v155, s28, v150
	ds_read_b128 v[130:133], v155
	ds_read_b128 v[146:149], v155 offset:1024
	ds_read_b128 v[156:159], v155 offset:2048
	ds_read_b128 v[160:163], v155 offset:3072
	v_add_u32_e32 v155, s21, v150
	ds_read_b128 v[164:167], v155
	ds_read_b128 v[172:175], v155 offset:1024
	ds_read_b128 v[176:179], v155 offset:2048
	ds_read_b128 v[180:183], v155 offset:3072
	s_mov_b32 m0, s66
	v_lshl_add_u64 v[218:219], s[56:57], 0, v[134:135]
	ds_read_b128 v[184:187], v154 offset:32768
	ds_read_b128 v[188:191], v154 offset:33792
	ds_read_b128 v[192:195], v154 offset:34816
	ds_read_b128 v[196:199], v154 offset:35840
	ds_read_b128 v[200:203], v154 offset:36864
	ds_read_b128 v[204:207], v154 offset:37888
	ds_read_b128 v[208:211], v154 offset:38912
	ds_read_b128 v[212:215], v154 offset:39936
	global_load_lds_dwordx4 v[218:219], off
	v_lshl_add_u64 v[218:219], s[56:57], 0, v[138:139]
	s_mov_b32 m0, s67
	s_nop 0
	global_load_lds_dwordx4 v[218:219], off
	s_waitcnt vmcnt(8)
	s_waitcnt lgkmcnt(0)
	s_barrier
	s_setprio 1
	v_mfma_f32_16x16x32_bf16 v[126:129], v[130:133], v[184:187], v[126:129]
	v_mfma_f32_16x16x32_bf16 v[122:125], v[156:159], v[184:187], v[122:125]
	v_mfma_f32_16x16x32_bf16 v[118:121], v[130:133], v[192:195], v[118:121]
	v_mfma_f32_16x16x32_bf16 v[110:113], v[156:159], v[192:195], v[110:113]
	v_mfma_f32_16x16x32_bf16 v[102:105], v[130:133], v[200:203], v[102:105]
	v_mfma_f32_16x16x32_bf16 v[94:97], v[156:159], v[200:203], v[94:97]
	v_mfma_f32_16x16x32_bf16 v[86:89], v[130:133], v[208:211], v[86:89]
	v_mfma_f32_16x16x32_bf16 v[78:81], v[156:159], v[208:211], v[78:81]
	v_mfma_f32_16x16x32_bf16 v[126:129], v[146:149], v[188:191], v[126:129]
	v_mfma_f32_16x16x32_bf16 v[122:125], v[160:163], v[188:191], v[122:125]
	v_mfma_f32_16x16x32_bf16 v[118:121], v[146:149], v[196:199], v[118:121]
	v_mfma_f32_16x16x32_bf16 v[110:113], v[160:163], v[196:199], v[110:113]
	v_mfma_f32_16x16x32_bf16 v[102:105], v[146:149], v[204:207], v[102:105]
	v_mfma_f32_16x16x32_bf16 v[94:97], v[160:163], v[204:207], v[94:97]
	v_mfma_f32_16x16x32_bf16 v[86:89], v[146:149], v[212:215], v[86:89]
	v_mfma_f32_16x16x32_bf16 v[78:81], v[160:163], v[212:215], v[78:81]
	s_setprio 0
	s_setprio 1
	v_mfma_f32_16x16x32_bf16 v[114:117], v[164:167], v[184:187], v[114:117]
	v_mfma_f32_16x16x32_bf16 v[106:109], v[176:179], v[184:187], v[106:109]
	v_mfma_f32_16x16x32_bf16 v[98:101], v[164:167], v[192:195], v[98:101]
	v_mfma_f32_16x16x32_bf16 v[90:93], v[176:179], v[192:195], v[90:93]
	v_mfma_f32_16x16x32_bf16 v[82:85], v[164:167], v[200:203], v[82:85]
	v_mfma_f32_16x16x32_bf16 v[74:77], v[176:179], v[200:203], v[74:77]
	v_mfma_f32_16x16x32_bf16 v[70:73], v[164:167], v[208:211], v[70:73]
	v_mfma_f32_16x16x32_bf16 v[66:69], v[176:179], v[208:211], v[66:69]
	v_mfma_f32_16x16x32_bf16 v[114:117], v[172:175], v[188:191], v[114:117]
	v_mfma_f32_16x16x32_bf16 v[106:109], v[180:183], v[188:191], v[106:109]
	v_mfma_f32_16x16x32_bf16 v[98:101], v[172:175], v[196:199], v[98:101]
	v_mfma_f32_16x16x32_bf16 v[90:93], v[180:183], v[196:199], v[90:93]
	v_mfma_f32_16x16x32_bf16 v[82:85], v[172:175], v[204:207], v[82:85]
	v_mfma_f32_16x16x32_bf16 v[74:77], v[180:183], v[204:207], v[74:77]
	v_mfma_f32_16x16x32_bf16 v[70:73], v[172:175], v[212:215], v[70:73]
	v_mfma_f32_16x16x32_bf16 v[66:69], v[180:183], v[212:215], v[66:69]
	s_setprio 0
	s_barrier
	s_mov_b32 m0, s19
	v_lshl_add_u64 v[218:219], s[52:53], 0, v[136:137]
	ds_read_b128 v[184:187], v154 offset:49152
	ds_read_b128 v[188:191], v154 offset:50176
	ds_read_b128 v[192:195], v154 offset:51200
	ds_read_b128 v[196:199], v154 offset:52224
	ds_read_b128 v[200:203], v154 offset:53248
	ds_read_b128 v[204:207], v154 offset:54272
	ds_read_b128 v[208:211], v154 offset:55296
	ds_read_b128 v[212:215], v154 offset:56320
	global_load_lds_dwordx4 v[218:219], off
	v_lshl_add_u64 v[218:219], s[52:53], 0, v[140:141]
	s_mov_b32 m0, s6
	v_lshl_add_u64 v[168:169], v[168:169], 0, s[14:15]
	global_load_lds_dwordx4 v[218:219], off
	v_lshl_add_u64 v[218:219], s[54:55], 0, v[136:137]
	s_mov_b32 m0, s81
	s_nop 0
	global_load_lds_dwordx4 v[218:219], off
	v_lshl_add_u64 v[218:219], s[54:55], 0, v[140:141]
	s_mov_b32 m0, s80
	s_nop 0
	global_load_lds_dwordx4 v[218:219], off
	s_mov_b32 m0, s70
	s_nop 0
	global_load_lds_dwordx4 v[168:169], off
	v_lshl_add_u64 v[168:169], v[216:217], 0, s[14:15]
	s_mov_b32 m0, s71
	s_nop 0
	global_load_lds_dwordx4 v[168:169], off
	s_waitcnt vmcnt(8)
	s_waitcnt lgkmcnt(0)
	s_barrier
	s_setprio 1
	v_mfma_f32_16x16x32_bf16 v[62:65], v[130:133], v[184:187], v[62:65]
	v_mfma_f32_16x16x32_bf16 v[58:61], v[156:159], v[184:187], v[58:61]
	v_mfma_f32_16x16x32_bf16 v[54:57], v[130:133], v[192:195], v[54:57]
	v_mfma_f32_16x16x32_bf16 v[46:49], v[156:159], v[192:195], v[46:49]
	v_mfma_f32_16x16x32_bf16 v[38:41], v[130:133], v[200:203], v[38:41]
	v_mfma_f32_16x16x32_bf16 v[30:33], v[156:159], v[200:203], v[30:33]
	v_mfma_f32_16x16x32_bf16 v[22:25], v[130:133], v[208:211], v[22:25]
	v_mfma_f32_16x16x32_bf16 v[14:17], v[156:159], v[208:211], v[14:17]
	v_mfma_f32_16x16x32_bf16 v[62:65], v[146:149], v[188:191], v[62:65]
	v_mfma_f32_16x16x32_bf16 v[58:61], v[160:163], v[188:191], v[58:61]
	v_mfma_f32_16x16x32_bf16 v[54:57], v[146:149], v[196:199], v[54:57]
	v_mfma_f32_16x16x32_bf16 v[46:49], v[160:163], v[196:199], v[46:49]
	v_mfma_f32_16x16x32_bf16 v[38:41], v[146:149], v[204:207], v[38:41]
	v_mfma_f32_16x16x32_bf16 v[30:33], v[160:163], v[204:207], v[30:33]
	v_mfma_f32_16x16x32_bf16 v[22:25], v[146:149], v[212:215], v[22:25]
	v_mfma_f32_16x16x32_bf16 v[14:17], v[160:163], v[212:215], v[14:17]
	s_setprio 0
	s_setprio 1
	v_mfma_f32_16x16x32_bf16 v[50:53], v[164:167], v[184:187], v[50:53]
	v_mfma_f32_16x16x32_bf16 v[42:45], v[176:179], v[184:187], v[42:45]
	v_mfma_f32_16x16x32_bf16 v[34:37], v[164:167], v[192:195], v[34:37]
	v_mfma_f32_16x16x32_bf16 v[26:29], v[176:179], v[192:195], v[26:29]
	v_mfma_f32_16x16x32_bf16 v[18:21], v[164:167], v[200:203], v[18:21]
	v_mfma_f32_16x16x32_bf16 v[10:13], v[176:179], v[200:203], v[10:13]
	v_mfma_f32_16x16x32_bf16 v[6:9], v[164:167], v[208:211], v[6:9]
	v_mfma_f32_16x16x32_bf16 v[2:5], v[176:179], v[208:211], v[2:5]
	v_mfma_f32_16x16x32_bf16 v[50:53], v[172:175], v[188:191], v[50:53]
	v_mfma_f32_16x16x32_bf16 v[42:45], v[180:183], v[188:191], v[42:45]
	v_mfma_f32_16x16x32_bf16 v[34:37], v[172:175], v[196:199], v[34:37]
	v_mfma_f32_16x16x32_bf16 v[26:29], v[180:183], v[196:199], v[26:29]
	v_mfma_f32_16x16x32_bf16 v[18:21], v[172:175], v[204:207], v[18:21]
	v_mfma_f32_16x16x32_bf16 v[10:13], v[180:183], v[204:207], v[10:13]
	v_mfma_f32_16x16x32_bf16 v[6:9], v[172:175], v[212:215], v[6:9]
	v_mfma_f32_16x16x32_bf16 v[2:5], v[180:183], v[212:215], v[2:5]
	s_setprio 0
	s_barrier
	s_andn2_b64 vcc, exec, s[50:51]
	s_mov_b64 s[52:53], -1
	s_mov_b64 s[50:51], 0
	s_mov_b32 s6, 2
	s_cbranch_vccz .LBB0_1100
	s_and_b64 vcc, exec, s[16:17]
	s_cbranch_vccz .LBB0_1103
	s_barrier

.LBB0_1267:
	ds_read_b128 v[130:133], v177
	ds_read_b128 v[134:137], v177 offset:1024
	ds_read_b128 v[138:141], v177 offset:2048
	ds_read_b128 v[142:145], v177 offset:3072
	ds_read_b128 v[160:163], v178
	ds_read_b128 v[164:167], v178 offset:1024
	ds_read_b128 v[172:175], v178 offset:2048
	ds_read_b128 v[180:183], v178 offset:3072
	s_add_i32 s29, s28, 2
	s_add_u32 s40, s56, 0xfffc0080
	s_addc_u32 s41, s57, -1
	s_cmp_eq_u32 s43, s28
	s_cselect_b32 s61, s49, s41
	s_cselect_b32 s60, s48, s40
	s_cselect_b32 s59, s51, s47
	s_cselect_b32 s58, s50, s45
	v_lshl_add_u64 v[168:169], s[56:57], 0, v[154:155]
	s_add_i32 m0, s65, 0xc000
	ds_read_b128 v[184:187], v179
	ds_read_b128 v[188:191], v179 offset:1024
	ds_read_b128 v[192:195], v179 offset:2048
	ds_read_b128 v[196:199], v179 offset:3072
	ds_read_b128 v[200:203], v179 offset:4096
	ds_read_b128 v[204:207], v179 offset:5120
	ds_read_b128 v[208:211], v179 offset:6144
	ds_read_b128 v[212:215], v179 offset:7168
	global_load_lds_dwordx4 v[168:169], off
	v_lshl_add_u64 v[168:169], s[56:57], 0, v[156:157]
	s_add_i32 m0, s65, 0xe000
	s_nop 0
	global_load_lds_dwordx4 v[168:169], off
	s_waitcnt vmcnt(8)
	s_waitcnt lgkmcnt(0)
	s_barrier
	s_setprio 1
	v_mfma_f32_16x16x32_bf16 v[126:129], v[130:133], v[184:187], v[126:129]
	v_mfma_f32_16x16x32_bf16 v[122:125], v[138:141], v[184:187], v[122:125]
	v_mfma_f32_16x16x32_bf16 v[118:121], v[130:133], v[192:195], v[118:121]
	v_mfma_f32_16x16x32_bf16 v[110:113], v[138:141], v[192:195], v[110:113]
	v_mfma_f32_16x16x32_bf16 v[102:105], v[130:133], v[200:203], v[102:105]
	v_mfma_f32_16x16x32_bf16 v[94:97], v[138:141], v[200:203], v[94:97]
	v_mfma_f32_16x16x32_bf16 v[86:89], v[130:133], v[208:211], v[86:89]
	v_mfma_f32_16x16x32_bf16 v[78:81], v[138:141], v[208:211], v[78:81]
	v_mfma_f32_16x16x32_bf16 v[126:129], v[134:137], v[188:191], v[126:129]
	v_mfma_f32_16x16x32_bf16 v[122:125], v[142:145], v[188:191], v[122:125]
	v_mfma_f32_16x16x32_bf16 v[118:121], v[134:137], v[196:199], v[118:121]
	v_mfma_f32_16x16x32_bf16 v[110:113], v[142:145], v[196:199], v[110:113]
	v_mfma_f32_16x16x32_bf16 v[102:105], v[134:137], v[204:207], v[102:105]
	v_mfma_f32_16x16x32_bf16 v[94:97], v[142:145], v[204:207], v[94:97]
	v_mfma_f32_16x16x32_bf16 v[86:89], v[134:137], v[212:215], v[86:89]
	v_mfma_f32_16x16x32_bf16 v[78:81], v[142:145], v[212:215], v[78:81]
	s_setprio 0
	s_setprio 1
	v_mfma_f32_16x16x32_bf16 v[114:117], v[160:163], v[184:187], v[114:117]
	v_mfma_f32_16x16x32_bf16 v[106:109], v[172:175], v[184:187], v[106:109]
	v_mfma_f32_16x16x32_bf16 v[98:101], v[160:163], v[192:195], v[98:101]
	v_mfma_f32_16x16x32_bf16 v[90:93], v[172:175], v[192:195], v[90:93]
	v_mfma_f32_16x16x32_bf16 v[82:85], v[160:163], v[200:203], v[82:85]
	v_mfma_f32_16x16x32_bf16 v[74:77], v[172:175], v[200:203], v[74:77]
	v_mfma_f32_16x16x32_bf16 v[70:73], v[160:163], v[208:211], v[70:73]
	v_mfma_f32_16x16x32_bf16 v[66:69], v[172:175], v[208:211], v[66:69]
	v_mfma_f32_16x16x32_bf16 v[114:117], v[164:167], v[188:191], v[114:117]
	v_mfma_f32_16x16x32_bf16 v[106:109], v[180:183], v[188:191], v[106:109]
	v_mfma_f32_16x16x32_bf16 v[98:101], v[164:167], v[196:199], v[98:101]
	v_mfma_f32_16x16x32_bf16 v[90:93], v[180:183], v[196:199], v[90:93]
	v_mfma_f32_16x16x32_bf16 v[82:85], v[164:167], v[204:207], v[82:85]
	v_mfma_f32_16x16x32_bf16 v[74:77], v[180:183], v[204:207], v[74:77]
	v_mfma_f32_16x16x32_bf16 v[70:73], v[164:167], v[212:215], v[70:73]
	v_mfma_f32_16x16x32_bf16 v[66:69], v[180:183], v[212:215], v[66:69]
	s_setprio 0
	s_barrier
	s_add_i32 s28, s74, s64
	v_lshl_add_u64 v[168:169], s[58:59], 0, v[148:149]
	s_mov_b32 m0, s28
	ds_read_b128 v[184:187], v179 offset:16384
	ds_read_b128 v[188:191], v179 offset:17408
	ds_read_b128 v[192:195], v179 offset:18432
	ds_read_b128 v[196:199], v179 offset:19456
	ds_read_b128 v[200:203], v179 offset:20480
	ds_read_b128 v[204:207], v179 offset:21504
	ds_read_b128 v[208:211], v179 offset:22528
	ds_read_b128 v[212:215], v179 offset:23552
	global_load_lds_dwordx4 v[168:169], off
	s_add_i32 m0, s28, 0x2000
	s_add_u32 s40, s58, 0x4000
	v_lshl_add_u64 v[168:169], s[58:59], 0, v[152:153]
	s_addc_u32 s41, s59, 0
	s_add_i32 s28, s75, s64
	global_load_lds_dwordx4 v[168:169], off
	v_lshl_add_u64 v[168:169], s[40:41], 0, v[148:149]
	s_mov_b32 m0, s28
	v_lshl_add_u64 v[216:217], s[60:61], 0, v[150:151]
	global_load_lds_dwordx4 v[168:169], off
	v_lshl_add_u64 v[168:169], s[40:41], 0, v[152:153]
	s_add_i32 m0, s28, 0x2000
	s_nop 0
	global_load_lds_dwordx4 v[168:169], off
	v_lshl_add_u64 v[168:169], s[60:61], 0, v[146:147]
	s_mov_b32 m0, s65
	s_nop 0
	global_load_lds_dwordx4 v[168:169], off
	s_mov_b32 m0, s53
	s_nop 0
	global_load_lds_dwordx4 v[216:217], off
	s_waitcnt vmcnt(8)
	s_waitcnt lgkmcnt(0)
	s_barrier
	s_setprio 1
	v_mfma_f32_16x16x32_bf16 v[62:65], v[130:133], v[184:187], v[62:65]
	v_mfma_f32_16x16x32_bf16 v[58:61], v[138:141], v[184:187], v[58:61]
	v_mfma_f32_16x16x32_bf16 v[54:57], v[130:133], v[192:195], v[54:57]
	v_mfma_f32_16x16x32_bf16 v[46:49], v[138:141], v[192:195], v[46:49]
	v_mfma_f32_16x16x32_bf16 v[38:41], v[130:133], v[200:203], v[38:41]
	v_mfma_f32_16x16x32_bf16 v[30:33], v[138:141], v[200:203], v[30:33]
	v_mfma_f32_16x16x32_bf16 v[22:25], v[130:133], v[208:211], v[22:25]
	v_mfma_f32_16x16x32_bf16 v[14:17], v[138:141], v[208:211], v[14:17]
	v_mfma_f32_16x16x32_bf16 v[62:65], v[134:137], v[188:191], v[62:65]
	v_mfma_f32_16x16x32_bf16 v[58:61], v[142:145], v[188:191], v[58:61]
	v_mfma_f32_16x16x32_bf16 v[54:57], v[134:137], v[196:199], v[54:57]
	v_mfma_f32_16x16x32_bf16 v[46:49], v[142:145], v[196:199], v[46:49]
	v_mfma_f32_16x16x32_bf16 v[38:41], v[134:137], v[204:207], v[38:41]
	v_mfma_f32_16x16x32_bf16 v[30:33], v[142:145], v[204:207], v[30:33]
	v_mfma_f32_16x16x32_bf16 v[22:25], v[134:137], v[212:215], v[22:25]
	v_mfma_f32_16x16x32_bf16 v[14:17], v[142:145], v[212:215], v[14:17]
	s_setprio 0
	s_setprio 1
	v_mfma_f32_16x16x32_bf16 v[50:53], v[160:163], v[184:187], v[50:53]
	v_mfma_f32_16x16x32_bf16 v[42:45], v[172:175], v[184:187], v[42:45]
	v_mfma_f32_16x16x32_bf16 v[34:37], v[160:163], v[192:195], v[34:37]
	v_mfma_f32_16x16x32_bf16 v[26:29], v[172:175], v[192:195], v[26:29]
	v_mfma_f32_16x16x32_bf16 v[18:21], v[160:163], v[200:203], v[18:21]
	v_mfma_f32_16x16x32_bf16 v[10:13], v[172:175], v[200:203], v[10:13]
	v_mfma_f32_16x16x32_bf16 v[6:9], v[160:163], v[208:211], v[6:9]
	v_mfma_f32_16x16x32_bf16 v[2:5], v[172:175], v[208:211], v[2:5]
	v_mfma_f32_16x16x32_bf16 v[50:53], v[164:167], v[188:191], v[50:53]
	v_mfma_f32_16x16x32_bf16 v[42:45], v[180:183], v[188:191], v[42:45]
	v_mfma_f32_16x16x32_bf16 v[34:37], v[164:167], v[196:199], v[34:37]
	v_mfma_f32_16x16x32_bf16 v[26:29], v[180:183], v[196:199], v[26:29]
	v_mfma_f32_16x16x32_bf16 v[18:21], v[164:167], v[204:207], v[18:21]
	v_mfma_f32_16x16x32_bf16 v[10:13], v[180:183], v[204:207], v[10:13]
	v_mfma_f32_16x16x32_bf16 v[6:9], v[164:167], v[212:215], v[6:9]
	v_mfma_f32_16x16x32_bf16 v[2:5], v[180:183], v[212:215], v[2:5]
	s_setprio 0
	s_barrier
	s_add_i32 s28, 0, 0x18000
	s_add_i32 s55, 0, 0x1c000
	v_add_u32_e32 v142, s28, v171
	v_add_u32_e32 v180, s55, v171
	ds_read_b128 v[130:133], v142
	ds_read_b128 v[134:137], v142 offset:1024
	ds_read_b128 v[138:141], v142 offset:2048
	ds_read_b128 v[142:145], v142 offset:3072
	ds_read_b128 v[160:163], v180
	ds_read_b128 v[164:167], v180 offset:1024
	ds_read_b128 v[172:175], v180 offset:2048
	ds_read_b128 v[180:183], v180 offset:3072
	s_add_u32 s40, s60, 0x40000
	s_addc_u32 s41, s61, 0
	s_mov_b32 m0, s66
	v_lshl_add_u64 v[218:219], s[40:41], 0, v[146:147]
	ds_read_b128 v[184:187], v179 offset:32768
	ds_read_b128 v[188:191], v179 offset:33792
	ds_read_b128 v[192:195], v179 offset:34816
	ds_read_b128 v[196:199], v179 offset:35840
	ds_read_b128 v[200:203], v179 offset:36864
	ds_read_b128 v[204:207], v179 offset:37888
	ds_read_b128 v[208:211], v179 offset:38912
	ds_read_b128 v[212:215], v179 offset:39936
	global_load_lds_dwordx4 v[218:219], off
	v_lshl_add_u64 v[218:219], s[40:41], 0, v[150:151]
	s_mov_b32 m0, s67
	s_nop 0
	global_load_lds_dwordx4 v[218:219], off
	s_waitcnt vmcnt(8)
	s_waitcnt lgkmcnt(0)
	s_barrier
	s_setprio 1
	v_mfma_f32_16x16x32_bf16 v[126:129], v[130:133], v[184:187], v[126:129]
	v_mfma_f32_16x16x32_bf16 v[122:125], v[138:141], v[184:187], v[122:125]
	v_mfma_f32_16x16x32_bf16 v[118:121], v[130:133], v[192:195], v[118:121]
	v_mfma_f32_16x16x32_bf16 v[110:113], v[138:141], v[192:195], v[110:113]
	v_mfma_f32_16x16x32_bf16 v[102:105], v[130:133], v[200:203], v[102:105]
	v_mfma_f32_16x16x32_bf16 v[94:97], v[138:141], v[200:203], v[94:97]
	v_mfma_f32_16x16x32_bf16 v[86:89], v[130:133], v[208:211], v[86:89]
	v_mfma_f32_16x16x32_bf16 v[78:81], v[138:141], v[208:211], v[78:81]
	v_mfma_f32_16x16x32_bf16 v[126:129], v[134:137], v[188:191], v[126:129]
	v_mfma_f32_16x16x32_bf16 v[122:125], v[142:145], v[188:191], v[122:125]
	v_mfma_f32_16x16x32_bf16 v[118:121], v[134:137], v[196:199], v[118:121]
	v_mfma_f32_16x16x32_bf16 v[110:113], v[142:145], v[196:199], v[110:113]
	v_mfma_f32_16x16x32_bf16 v[102:105], v[134:137], v[204:207], v[102:105]
	v_mfma_f32_16x16x32_bf16 v[94:97], v[142:145], v[204:207], v[94:97]
	v_mfma_f32_16x16x32_bf16 v[86:89], v[134:137], v[212:215], v[86:89]
	v_mfma_f32_16x16x32_bf16 v[78:81], v[142:145], v[212:215], v[78:81]
	s_setprio 0
	s_setprio 1
	v_mfma_f32_16x16x32_bf16 v[114:117], v[160:163], v[184:187], v[114:117]
	v_mfma_f32_16x16x32_bf16 v[106:109], v[172:175], v[184:187], v[106:109]
	v_mfma_f32_16x16x32_bf16 v[98:101], v[160:163], v[192:195], v[98:101]
	v_mfma_f32_16x16x32_bf16 v[90:93], v[172:175], v[192:195], v[90:93]
	v_mfma_f32_16x16x32_bf16 v[82:85], v[160:163], v[200:203], v[82:85]
	v_mfma_f32_16x16x32_bf16 v[74:77], v[172:175], v[200:203], v[74:77]
	v_mfma_f32_16x16x32_bf16 v[70:73], v[160:163], v[208:211], v[70:73]
	v_mfma_f32_16x16x32_bf16 v[66:69], v[172:175], v[208:211], v[66:69]
	v_mfma_f32_16x16x32_bf16 v[114:117], v[164:167], v[188:191], v[114:117]
	v_mfma_f32_16x16x32_bf16 v[106:109], v[180:183], v[188:191], v[106:109]
	v_mfma_f32_16x16x32_bf16 v[98:101], v[164:167], v[196:199], v[98:101]
	v_mfma_f32_16x16x32_bf16 v[90:93], v[180:183], v[196:199], v[90:93]
	v_mfma_f32_16x16x32_bf16 v[82:85], v[164:167], v[204:207], v[82:85]
	v_mfma_f32_16x16x32_bf16 v[74:77], v[180:183], v[204:207], v[74:77]
	v_mfma_f32_16x16x32_bf16 v[70:73], v[164:167], v[212:215], v[70:73]
	v_mfma_f32_16x16x32_bf16 v[66:69], v[180:183], v[212:215], v[66:69]
	s_setprio 0
	s_barrier
	s_add_u32 s40, s58, 0x8000
	s_addc_u32 s41, s59, 0
	s_add_i32 s28, s28, s64
	v_lshl_add_u64 v[218:219], s[40:41], 0, v[148:149]
	s_mov_b32 m0, s28
	ds_read_b128 v[184:187], v179 offset:49152
	ds_read_b128 v[188:191], v179 offset:50176
	ds_read_b128 v[192:195], v179 offset:51200
	ds_read_b128 v[196:199], v179 offset:52224
	ds_read_b128 v[200:203], v179 offset:53248
	ds_read_b128 v[204:207], v179 offset:54272
	ds_read_b128 v[208:211], v179 offset:55296
	ds_read_b128 v[212:215], v179 offset:56320
	global_load_lds_dwordx4 v[218:219], off
	s_add_i32 m0, s28, 0x2000
	v_lshl_add_u64 v[218:219], s[40:41], 0, v[152:153]
	s_add_u32 s40, s58, 0xc000
	s_addc_u32 s41, s59, 0
	s_add_i32 s28, s55, s64
	global_load_lds_dwordx4 v[218:219], off
	v_lshl_add_u64 v[218:219], s[40:41], 0, v[148:149]
	s_mov_b32 m0, s28
	v_lshl_add_u64 v[168:169], v[168:169], 0, s[14:15]
	global_load_lds_dwordx4 v[218:219], off
	v_lshl_add_u64 v[218:219], s[40:41], 0, v[152:153]
	s_add_i32 m0, s28, 0x2000
	s_nop 0
	global_load_lds_dwordx4 v[218:219], off
	s_mov_b32 m0, s30
	s_nop 0
	global_load_lds_dwordx4 v[168:169], off
	v_lshl_add_u64 v[168:169], v[216:217], 0, s[14:15]
	s_mov_b32 m0, s31
	s_nop 0
	global_load_lds_dwordx4 v[168:169], off
	s_waitcnt vmcnt(8)
	s_waitcnt lgkmcnt(0)
	s_barrier
	s_setprio 1
	v_mfma_f32_16x16x32_bf16 v[62:65], v[130:133], v[184:187], v[62:65]
	v_mfma_f32_16x16x32_bf16 v[58:61], v[138:141], v[184:187], v[58:61]
	v_mfma_f32_16x16x32_bf16 v[54:57], v[130:133], v[192:195], v[54:57]
	v_mfma_f32_16x16x32_bf16 v[46:49], v[138:141], v[192:195], v[46:49]
	v_mfma_f32_16x16x32_bf16 v[38:41], v[130:133], v[200:203], v[38:41]
	v_mfma_f32_16x16x32_bf16 v[30:33], v[138:141], v[200:203], v[30:33]
	v_mfma_f32_16x16x32_bf16 v[22:25], v[130:133], v[208:211], v[22:25]
	v_mfma_f32_16x16x32_bf16 v[14:17], v[138:141], v[208:211], v[14:17]
	v_mfma_f32_16x16x32_bf16 v[62:65], v[134:137], v[188:191], v[62:65]
	v_mfma_f32_16x16x32_bf16 v[58:61], v[142:145], v[188:191], v[58:61]
	v_mfma_f32_16x16x32_bf16 v[54:57], v[134:137], v[196:199], v[54:57]
	v_mfma_f32_16x16x32_bf16 v[46:49], v[142:145], v[196:199], v[46:49]
	v_mfma_f32_16x16x32_bf16 v[38:41], v[134:137], v[204:207], v[38:41]
	v_mfma_f32_16x16x32_bf16 v[30:33], v[142:145], v[204:207], v[30:33]
	v_mfma_f32_16x16x32_bf16 v[22:25], v[134:137], v[212:215], v[22:25]
	v_mfma_f32_16x16x32_bf16 v[14:17], v[142:145], v[212:215], v[14:17]
	s_setprio 0
	s_setprio 1
	v_mfma_f32_16x16x32_bf16 v[50:53], v[160:163], v[184:187], v[50:53]
	v_mfma_f32_16x16x32_bf16 v[42:45], v[172:175], v[184:187], v[42:45]
	v_mfma_f32_16x16x32_bf16 v[34:37], v[160:163], v[192:195], v[34:37]
	v_mfma_f32_16x16x32_bf16 v[26:29], v[172:175], v[192:195], v[26:29]
	v_mfma_f32_16x16x32_bf16 v[18:21], v[160:163], v[200:203], v[18:21]
	v_mfma_f32_16x16x32_bf16 v[10:13], v[172:175], v[200:203], v[10:13]
	v_mfma_f32_16x16x32_bf16 v[6:9], v[160:163], v[208:211], v[6:9]
	v_mfma_f32_16x16x32_bf16 v[2:5], v[172:175], v[208:211], v[2:5]
	v_mfma_f32_16x16x32_bf16 v[50:53], v[164:167], v[188:191], v[50:53]
	v_mfma_f32_16x16x32_bf16 v[42:45], v[180:183], v[188:191], v[42:45]
	v_mfma_f32_16x16x32_bf16 v[34:37], v[164:167], v[196:199], v[34:37]
	v_mfma_f32_16x16x32_bf16 v[26:29], v[180:183], v[196:199], v[26:29]
	v_mfma_f32_16x16x32_bf16 v[18:21], v[164:167], v[204:207], v[18:21]
	v_mfma_f32_16x16x32_bf16 v[10:13], v[180:183], v[204:207], v[10:13]
	v_mfma_f32_16x16x32_bf16 v[6:9], v[164:167], v[212:215], v[6:9]
	v_mfma_f32_16x16x32_bf16 v[2:5], v[180:183], v[212:215], v[2:5]
	s_setprio 0
	s_barrier
	s_add_u32 s45, s45, 0x10000
	s_addc_u32 s47, s47, 0
	s_add_u32 s56, s56, 0x100
	s_addc_u32 s57, s57, 0
	s_cmp_ge_u32 s29, s33
	s_mov_b32 s28, s29
	s_cbranch_scc0 .LBB0_1267
	s_and_b64 vcc, exec, s[16:17]
	s_cbranch_vccz .LBB0_1270
	s_barrier

.LBB0_1521:
	v_add_u32_e32 v134, s33, v167
	ds_read_b128 v[172:175], v134
	ds_read_b128 v[176:179], v134 offset:1024
	ds_read_b128 v[180:183], v134 offset:2048
	ds_read_b128 v[184:187], v134 offset:3072
	v_add_u32_e32 v134, s68, v167
	ds_read_b128 v[188:191], v134
	ds_read_b128 v[192:195], v134 offset:1024
	ds_read_b128 v[196:199], v134 offset:2048
	ds_read_b128 v[200:203], v134 offset:3072
	s_add_u32 s56, s54, 0x100
	s_addc_u32 s57, s55, 0
	s_and_b64 s[28:29], s[8:9], exec
	s_cselect_b32 s29, 0, s56
	s_cselect_b32 s28, 0, s57
	s_add_u32 s58, s38, s29
	v_cndmask_b32_e64 v239, v159, v143, s[8:9]
	v_cndmask_b32_e64 v238, v158, v142, s[8:9]
	s_addc_u32 s59, s39, s28
	v_lshl_add_u64 v[240:241], v[238:239], 0, s[22:23]
	v_cndmask_b32_e64 v134, v141, v147, s[8:9]
	v_cndmask_b32_e64 v242, v144, v149, s[8:9]
	v_cndmask_b32_e64 v145, v146, v169, s[8:9]
	v_cndmask_b32_e64 v233, v148, v171, s[8:9]
	v_lshl_add_u64 v[244:245], v[160:161], 0, s[54:55]
	s_add_i32 m0, s71, 0xc000
	ds_read_b128 v[204:207], v168
	ds_read_b128 v[208:211], v168 offset:1024
	ds_read_b128 v[212:215], v168 offset:2048
	ds_read_b128 v[216:219], v168 offset:3072
	ds_read_b128 v[220:223], v168 offset:4096
	ds_read_b128 v[224:227], v168 offset:5120
	ds_read_b128 v[228:231], v168 offset:6144
	ds_read_b128 v[234:237], v168 offset:7168
	global_load_lds_dwordx4 v[244:245], off
	v_lshl_add_u64 v[244:245], v[162:163], 0, s[54:55]
	s_add_i32 m0, s71, 0xe000
	s_nop 0
	global_load_lds_dwordx4 v[244:245], off
	s_waitcnt vmcnt(8)
	s_waitcnt lgkmcnt(0)
	s_barrier
	s_setprio 1
	v_mfma_f32_16x16x32_bf16 v[126:129], v[172:175], v[204:207], v[126:129]
	v_mfma_f32_16x16x32_bf16 v[122:125], v[180:183], v[204:207], v[122:125]
	v_mfma_f32_16x16x32_bf16 v[118:121], v[172:175], v[212:215], v[118:121]
	v_mfma_f32_16x16x32_bf16 v[114:117], v[180:183], v[212:215], v[114:117]
	v_mfma_f32_16x16x32_bf16 v[94:97], v[172:175], v[220:223], v[94:97]
	v_mfma_f32_16x16x32_bf16 v[90:93], v[180:183], v[220:223], v[90:93]
	v_mfma_f32_16x16x32_bf16 v[86:89], v[172:175], v[228:231], v[86:89]
	v_mfma_f32_16x16x32_bf16 v[82:85], v[180:183], v[228:231], v[82:85]
	v_mfma_f32_16x16x32_bf16 v[126:129], v[176:179], v[208:211], v[126:129]
	v_mfma_f32_16x16x32_bf16 v[122:125], v[184:187], v[208:211], v[122:125]
	v_mfma_f32_16x16x32_bf16 v[118:121], v[176:179], v[216:219], v[118:121]
	v_mfma_f32_16x16x32_bf16 v[114:117], v[184:187], v[216:219], v[114:117]
	v_mfma_f32_16x16x32_bf16 v[94:97], v[176:179], v[224:227], v[94:97]
	v_mfma_f32_16x16x32_bf16 v[90:93], v[184:187], v[224:227], v[90:93]
	v_mfma_f32_16x16x32_bf16 v[86:89], v[176:179], v[234:237], v[86:89]
	v_mfma_f32_16x16x32_bf16 v[82:85], v[184:187], v[234:237], v[82:85]
	s_setprio 0
	s_setprio 1
	v_mfma_f32_16x16x32_bf16 v[110:113], v[188:191], v[204:207], v[110:113]
	v_mfma_f32_16x16x32_bf16 v[106:109], v[196:199], v[204:207], v[106:109]
	v_mfma_f32_16x16x32_bf16 v[102:105], v[188:191], v[212:215], v[102:105]
	v_mfma_f32_16x16x32_bf16 v[98:101], v[196:199], v[212:215], v[98:101]
	v_mfma_f32_16x16x32_bf16 v[78:81], v[188:191], v[220:223], v[78:81]
	v_mfma_f32_16x16x32_bf16 v[74:77], v[196:199], v[220:223], v[74:77]
	v_mfma_f32_16x16x32_bf16 v[70:73], v[188:191], v[228:231], v[70:73]
	v_mfma_f32_16x16x32_bf16 v[66:69], v[196:199], v[228:231], v[66:69]
	v_mfma_f32_16x16x32_bf16 v[110:113], v[192:195], v[208:211], v[110:113]
	v_mfma_f32_16x16x32_bf16 v[106:109], v[200:203], v[208:211], v[106:109]
	v_mfma_f32_16x16x32_bf16 v[102:105], v[192:195], v[216:219], v[102:105]
	v_mfma_f32_16x16x32_bf16 v[98:101], v[200:203], v[216:219], v[98:101]
	v_mfma_f32_16x16x32_bf16 v[78:81], v[192:195], v[224:227], v[78:81]
	v_mfma_f32_16x16x32_bf16 v[74:77], v[200:203], v[224:227], v[74:77]
	v_mfma_f32_16x16x32_bf16 v[70:73], v[192:195], v[234:237], v[70:73]
	v_mfma_f32_16x16x32_bf16 v[66:69], v[200:203], v[234:237], v[66:69]
	s_setprio 0
	s_barrier
	s_add_i32 s8, s33, s69
	v_lshl_add_u64 v[244:245], v[238:239], 0, v[130:131]
	s_mov_b32 m0, s8
	ds_read_b128 v[204:207], v168 offset:16384
	ds_read_b128 v[208:211], v168 offset:17408
	ds_read_b128 v[212:215], v168 offset:18432
	ds_read_b128 v[216:219], v168 offset:19456
	ds_read_b128 v[220:223], v168 offset:20480
	ds_read_b128 v[224:227], v168 offset:21504
	ds_read_b128 v[228:231], v168 offset:22528
	ds_read_b128 v[234:237], v168 offset:23552
	global_load_lds_dwordx4 v[244:245], off
	v_lshl_add_u64 v[244:245], v[238:239], 0, v[132:133]
	s_add_i32 m0, s8, 0x2000
	s_add_i32 s8, s68, s69
	global_load_lds_dwordx4 v[244:245], off
	v_lshl_add_u64 v[244:245], v[238:239], 0, s[16:17]
	v_lshl_add_u64 v[246:247], v[244:245], 0, v[130:131]
	s_mov_b32 m0, s8
	v_lshl_add_u64 v[244:245], v[244:245], 0, v[132:133]
	global_load_lds_dwordx4 v[246:247], off
	s_add_i32 m0, s8, 0x2000
	v_mov_b32_e32 v243, v135
	global_load_lds_dwordx4 v[244:245], off
	s_mov_b32 m0, s71
	v_lshl_add_u64 v[244:245], s[58:59], 0, v[134:135]
	global_load_lds_dwordx4 v134, s[58:59]
	s_mov_b32 m0, s72
	s_nop 0
	global_load_lds_dwordx4 v242, s[58:59]
	s_waitcnt vmcnt(8)
	s_waitcnt lgkmcnt(0)
	v_lshl_add_u64 v[242:243], s[58:59], 0, v[242:243]
	s_barrier
	s_setprio 1
	s_waitcnt lgkmcnt(0)
	v_mfma_f32_16x16x32_bf16 v[62:65], v[172:175], v[204:207], v[62:65]
	v_mfma_f32_16x16x32_bf16 v[58:61], v[180:183], v[204:207], v[58:61]
	v_mfma_f32_16x16x32_bf16 v[54:57], v[172:175], v[212:215], v[54:57]
	v_mfma_f32_16x16x32_bf16 v[50:53], v[180:183], v[212:215], v[50:53]
	v_mfma_f32_16x16x32_bf16 v[30:33], v[172:175], v[220:223], v[30:33]
	v_mfma_f32_16x16x32_bf16 v[26:29], v[180:183], v[220:223], v[26:29]
	v_mfma_f32_16x16x32_bf16 v[22:25], v[172:175], v[228:231], v[22:25]
	v_mfma_f32_16x16x32_bf16 v[18:21], v[180:183], v[228:231], v[18:21]
	v_mfma_f32_16x16x32_bf16 v[62:65], v[176:179], v[208:211], v[62:65]
	v_mfma_f32_16x16x32_bf16 v[58:61], v[184:187], v[208:211], v[58:61]
	v_mfma_f32_16x16x32_bf16 v[54:57], v[176:179], v[216:219], v[54:57]
	v_mfma_f32_16x16x32_bf16 v[50:53], v[184:187], v[216:219], v[50:53]
	v_mfma_f32_16x16x32_bf16 v[30:33], v[176:179], v[224:227], v[30:33]
	v_mfma_f32_16x16x32_bf16 v[26:29], v[184:187], v[224:227], v[26:29]
	v_mfma_f32_16x16x32_bf16 v[22:25], v[176:179], v[234:237], v[22:25]
	v_mfma_f32_16x16x32_bf16 v[18:21], v[184:187], v[234:237], v[18:21]
	s_setprio 0
	s_setprio 1
	v_mfma_f32_16x16x32_bf16 v[46:49], v[188:191], v[204:207], v[46:49]
	v_mfma_f32_16x16x32_bf16 v[42:45], v[196:199], v[204:207], v[42:45]
	v_mfma_f32_16x16x32_bf16 v[38:41], v[188:191], v[212:215], v[38:41]
	v_mfma_f32_16x16x32_bf16 v[34:37], v[196:199], v[212:215], v[34:37]
	v_mfma_f32_16x16x32_bf16 v[14:17], v[188:191], v[220:223], v[14:17]
	v_mfma_f32_16x16x32_bf16 v[10:13], v[196:199], v[220:223], v[10:13]
	v_mfma_f32_16x16x32_bf16 v[6:9], v[188:191], v[228:231], v[6:9]
	v_mfma_f32_16x16x32_bf16 v[2:5], v[196:199], v[228:231], v[2:5]
	v_mfma_f32_16x16x32_bf16 v[46:49], v[192:195], v[208:211], v[46:49]
	v_mfma_f32_16x16x32_bf16 v[42:45], v[200:203], v[208:211], v[42:45]
	v_mfma_f32_16x16x32_bf16 v[38:41], v[192:195], v[216:219], v[38:41]
	v_mfma_f32_16x16x32_bf16 v[34:37], v[200:203], v[216:219], v[34:37]
	v_mfma_f32_16x16x32_bf16 v[14:17], v[192:195], v[224:227], v[14:17]
	v_mfma_f32_16x16x32_bf16 v[10:13], v[200:203], v[224:227], v[10:13]
	v_mfma_f32_16x16x32_bf16 v[6:9], v[192:195], v[234:237], v[6:9]
	v_mfma_f32_16x16x32_bf16 v[2:5], v[200:203], v[234:237], v[2:5]
	s_setprio 0
	s_barrier
	s_add_i32 s8, 0, 0x18000
	v_add_u32_e32 v134, s8, v167
	s_add_i32 s9, 0, 0x1c000
	ds_read_b128 v[172:175], v134
	ds_read_b128 v[176:179], v134 offset:1024
	ds_read_b128 v[180:183], v134 offset:2048
	ds_read_b128 v[184:187], v134 offset:3072
	v_add_u32_e32 v134, s9, v167
	ds_read_b128 v[188:191], v134
	ds_read_b128 v[192:195], v134 offset:1024
	ds_read_b128 v[196:199], v134 offset:2048
	ds_read_b128 v[200:203], v134 offset:3072
	s_mov_b32 m0, s79
	ds_read_b128 v[204:207], v168 offset:32768
	ds_read_b128 v[208:211], v168 offset:33792
	ds_read_b128 v[212:215], v168 offset:34816
	ds_read_b128 v[216:219], v168 offset:35840
	ds_read_b128 v[220:223], v168 offset:36864
	ds_read_b128 v[224:227], v168 offset:37888
	ds_read_b128 v[228:231], v168 offset:38912
	ds_read_b128 v[234:237], v168 offset:39936
	global_load_lds_dwordx4 v145, s[58:59]
	s_mov_b32 m0, s80
	s_nop 0
	global_load_lds_dwordx4 v233, s[58:59]
	s_waitcnt vmcnt(8)
	s_waitcnt lgkmcnt(0)
	s_barrier
	s_setprio 1
	v_mfma_f32_16x16x32_bf16 v[126:129], v[172:175], v[204:207], v[126:129]
	v_mfma_f32_16x16x32_bf16 v[122:125], v[180:183], v[204:207], v[122:125]
	v_mfma_f32_16x16x32_bf16 v[118:121], v[172:175], v[212:215], v[118:121]
	v_mfma_f32_16x16x32_bf16 v[114:117], v[180:183], v[212:215], v[114:117]
	v_mfma_f32_16x16x32_bf16 v[94:97], v[172:175], v[220:223], v[94:97]
	v_mfma_f32_16x16x32_bf16 v[90:93], v[180:183], v[220:223], v[90:93]
	v_mfma_f32_16x16x32_bf16 v[86:89], v[172:175], v[228:231], v[86:89]
	v_mfma_f32_16x16x32_bf16 v[82:85], v[180:183], v[228:231], v[82:85]
	v_mfma_f32_16x16x32_bf16 v[126:129], v[176:179], v[208:211], v[126:129]
	v_mfma_f32_16x16x32_bf16 v[122:125], v[184:187], v[208:211], v[122:125]
	v_mfma_f32_16x16x32_bf16 v[118:121], v[176:179], v[216:219], v[118:121]
	v_mfma_f32_16x16x32_bf16 v[114:117], v[184:187], v[216:219], v[114:117]
	v_mfma_f32_16x16x32_bf16 v[94:97], v[176:179], v[224:227], v[94:97]
	v_mfma_f32_16x16x32_bf16 v[90:93], v[184:187], v[224:227], v[90:93]
	v_mfma_f32_16x16x32_bf16 v[86:89], v[176:179], v[234:237], v[86:89]
	v_mfma_f32_16x16x32_bf16 v[82:85], v[184:187], v[234:237], v[82:85]
	s_setprio 0
	s_setprio 1
	v_mfma_f32_16x16x32_bf16 v[110:113], v[188:191], v[204:207], v[110:113]
	v_mfma_f32_16x16x32_bf16 v[106:109], v[196:199], v[204:207], v[106:109]
	v_mfma_f32_16x16x32_bf16 v[102:105], v[188:191], v[212:215], v[102:105]
	v_mfma_f32_16x16x32_bf16 v[98:101], v[196:199], v[212:215], v[98:101]
	v_mfma_f32_16x16x32_bf16 v[78:81], v[188:191], v[220:223], v[78:81]
	v_mfma_f32_16x16x32_bf16 v[74:77], v[196:199], v[220:223], v[74:77]
	v_mfma_f32_16x16x32_bf16 v[70:73], v[188:191], v[228:231], v[70:73]
	v_mfma_f32_16x16x32_bf16 v[66:69], v[196:199], v[228:231], v[66:69]
	v_mfma_f32_16x16x32_bf16 v[110:113], v[192:195], v[208:211], v[110:113]
	v_mfma_f32_16x16x32_bf16 v[106:109], v[200:203], v[208:211], v[106:109]
	v_mfma_f32_16x16x32_bf16 v[102:105], v[192:195], v[216:219], v[102:105]
	v_mfma_f32_16x16x32_bf16 v[98:101], v[200:203], v[216:219], v[98:101]
	v_mfma_f32_16x16x32_bf16 v[78:81], v[192:195], v[224:227], v[78:81]
	v_mfma_f32_16x16x32_bf16 v[74:77], v[200:203], v[224:227], v[74:77]
	v_mfma_f32_16x16x32_bf16 v[70:73], v[192:195], v[234:237], v[70:73]
	v_mfma_f32_16x16x32_bf16 v[66:69], v[200:203], v[234:237], v[66:69]
	s_setprio 0
	s_barrier
	s_add_i32 s8, s8, s69
	v_lshl_add_u64 v[246:247], v[240:241], 0, v[130:131]
	s_mov_b32 m0, s8
	ds_read_b128 v[204:207], v168 offset:49152
	ds_read_b128 v[208:211], v168 offset:50176
	ds_read_b128 v[212:215], v168 offset:51200
	ds_read_b128 v[216:219], v168 offset:52224
	ds_read_b128 v[220:223], v168 offset:53248
	ds_read_b128 v[224:227], v168 offset:54272
	ds_read_b128 v[228:231], v168 offset:55296
	ds_read_b128 v[234:237], v168 offset:56320
	global_load_lds_dwordx4 v[246:247], off
	v_lshl_add_u64 v[240:241], v[240:241], 0, v[132:133]
	s_add_i32 m0, s8, 0x2000
	v_lshl_add_u64 v[238:239], v[238:239], 0, s[42:43]
	s_add_i32 s8, s9, s69
	global_load_lds_dwordx4 v[240:241], off
	v_lshl_add_u64 v[240:241], v[238:239], 0, v[130:131]
	s_mov_b32 m0, s8
	v_lshl_add_u64 v[238:239], v[238:239], 0, v[132:133]
	global_load_lds_dwordx4 v[240:241], off
	s_add_i32 m0, s8, 0x2000
	s_nop 0
	global_load_lds_dwordx4 v[238:239], off
	v_lshl_add_u64 v[238:239], v[244:245], 0, s[48:49]
	s_mov_b32 m0, s83
	s_nop 0
	global_load_lds_dwordx4 v[238:239], off
	v_lshl_add_u64 v[238:239], v[242:243], 0, s[48:49]
	s_mov_b32 m0, s84
	s_nop 0
	global_load_lds_dwordx4 v[238:239], off
	s_waitcnt vmcnt(8)
	s_waitcnt lgkmcnt(0)
	s_barrier
	s_setprio 1
	v_mfma_f32_16x16x32_bf16 v[62:65], v[172:175], v[204:207], v[62:65]
	v_mfma_f32_16x16x32_bf16 v[58:61], v[180:183], v[204:207], v[58:61]
	v_mfma_f32_16x16x32_bf16 v[54:57], v[172:175], v[212:215], v[54:57]
	v_mfma_f32_16x16x32_bf16 v[50:53], v[180:183], v[212:215], v[50:53]
	v_mfma_f32_16x16x32_bf16 v[30:33], v[172:175], v[220:223], v[30:33]
	v_mfma_f32_16x16x32_bf16 v[26:29], v[180:183], v[220:223], v[26:29]
	v_mfma_f32_16x16x32_bf16 v[22:25], v[172:175], v[228:231], v[22:25]
	v_mfma_f32_16x16x32_bf16 v[18:21], v[180:183], v[228:231], v[18:21]
	v_mfma_f32_16x16x32_bf16 v[62:65], v[176:179], v[208:211], v[62:65]
	v_mfma_f32_16x16x32_bf16 v[58:61], v[184:187], v[208:211], v[58:61]
	v_mfma_f32_16x16x32_bf16 v[54:57], v[176:179], v[216:219], v[54:57]
	v_mfma_f32_16x16x32_bf16 v[50:53], v[184:187], v[216:219], v[50:53]
	v_mfma_f32_16x16x32_bf16 v[30:33], v[176:179], v[224:227], v[30:33]
	v_mfma_f32_16x16x32_bf16 v[26:29], v[184:187], v[224:227], v[26:29]
	v_mfma_f32_16x16x32_bf16 v[22:25], v[176:179], v[234:237], v[22:25]
	v_mfma_f32_16x16x32_bf16 v[18:21], v[184:187], v[234:237], v[18:21]
	s_setprio 0
	s_setprio 1
	v_mfma_f32_16x16x32_bf16 v[46:49], v[188:191], v[204:207], v[46:49]
	v_mfma_f32_16x16x32_bf16 v[42:45], v[196:199], v[204:207], v[42:45]
	v_mfma_f32_16x16x32_bf16 v[38:41], v[188:191], v[212:215], v[38:41]
	v_mfma_f32_16x16x32_bf16 v[34:37], v[196:199], v[212:215], v[34:37]
	v_mfma_f32_16x16x32_bf16 v[14:17], v[188:191], v[220:223], v[14:17]
	v_mfma_f32_16x16x32_bf16 v[10:13], v[196:199], v[220:223], v[10:13]
	v_mfma_f32_16x16x32_bf16 v[6:9], v[188:191], v[228:231], v[6:9]
	v_mfma_f32_16x16x32_bf16 v[2:5], v[196:199], v[228:231], v[2:5]
	v_mfma_f32_16x16x32_bf16 v[46:49], v[192:195], v[208:211], v[46:49]
	v_mfma_f32_16x16x32_bf16 v[42:45], v[200:203], v[208:211], v[42:45]
	v_mfma_f32_16x16x32_bf16 v[38:41], v[192:195], v[216:219], v[38:41]
	v_mfma_f32_16x16x32_bf16 v[34:37], v[200:203], v[216:219], v[34:37]
	v_mfma_f32_16x16x32_bf16 v[14:17], v[192:195], v[224:227], v[14:17]
	v_mfma_f32_16x16x32_bf16 v[10:13], v[200:203], v[224:227], v[10:13]
	v_mfma_f32_16x16x32_bf16 v[6:9], v[192:195], v[234:237], v[6:9]
	v_mfma_f32_16x16x32_bf16 v[2:5], v[200:203], v[234:237], v[2:5]
	s_setprio 0
	s_barrier
	s_add_i32 s51, s51, 2
	s_cmp_gt_u32 s51, 13
	v_lshl_add_u64 v[158:159], v[158:159], 0, s[46:47]
	s_cbranch_scc1 .LBB0_1523
	s_mov_b64 s[54:55], s[56:57]
	s_branch .LBB0_1519

.LBB0_1616:
	ds_read_b128 v[150:153], v157
	ds_read_b128 v[160:163], v157 offset:1024
	ds_read_b128 v[164:167], v157 offset:2048
	ds_read_b128 v[172:175], v157 offset:3072
	ds_read_b128 v[176:179], v158
	ds_read_b128 v[180:183], v158 offset:1024
	ds_read_b128 v[184:187], v158 offset:2048
	ds_read_b128 v[188:191], v158 offset:3072
	s_add_i32 s40, s64, 2
	s_add_u32 s41, s62, 0x4000
	s_addc_u32 s65, s63, 0
	s_cmp_eq_u32 s29, s64
	s_cselect_b32 s66, s60, s41
	s_cselect_b32 s67, s61, s65
	s_cselect_b64 vcc, -1, 0
	s_add_u32 s64, s66, 0x8000
	v_cndmask_b32_e32 v132, v130, v148, vcc
	v_cndmask_b32_e32 v133, v131, v149, vcc
	s_addc_u32 s65, s67, 0
	v_lshl_add_u64 v[168:169], s[62:63], 0, v[144:145]
	s_add_i32 m0, s84, 0xc000
	ds_read_b128 v[192:195], v159
	ds_read_b128 v[196:199], v159 offset:1024
	ds_read_b128 v[200:203], v159 offset:2048
	ds_read_b128 v[204:207], v159 offset:3072
	ds_read_b128 v[208:211], v159 offset:4096
	ds_read_b128 v[212:215], v159 offset:5120
	ds_read_b128 v[216:219], v159 offset:6144
	ds_read_b128 v[220:223], v159 offset:7168
	global_load_lds_dwordx4 v[168:169], off
	v_lshl_add_u64 v[168:169], s[62:63], 0, v[146:147]
	s_add_i32 m0, s84, 0xe000
	s_nop 0
	global_load_lds_dwordx4 v[168:169], off
	s_waitcnt vmcnt(8)
	s_waitcnt lgkmcnt(0)
	s_barrier
	s_setprio 1
	v_mfma_f32_16x16x32_bf16 v[126:129], v[150:153], v[192:195], v[126:129]
	v_mfma_f32_16x16x32_bf16 v[122:125], v[164:167], v[192:195], v[122:125]
	v_mfma_f32_16x16x32_bf16 v[118:121], v[150:153], v[200:203], v[118:121]
	v_mfma_f32_16x16x32_bf16 v[110:113], v[164:167], v[200:203], v[110:113]
	v_mfma_f32_16x16x32_bf16 v[102:105], v[150:153], v[208:211], v[102:105]
	v_mfma_f32_16x16x32_bf16 v[94:97], v[164:167], v[208:211], v[94:97]
	v_mfma_f32_16x16x32_bf16 v[86:89], v[150:153], v[216:219], v[86:89]
	v_mfma_f32_16x16x32_bf16 v[78:81], v[164:167], v[216:219], v[78:81]
	v_mfma_f32_16x16x32_bf16 v[126:129], v[160:163], v[196:199], v[126:129]
	v_mfma_f32_16x16x32_bf16 v[122:125], v[172:175], v[196:199], v[122:125]
	v_mfma_f32_16x16x32_bf16 v[118:121], v[160:163], v[204:207], v[118:121]
	v_mfma_f32_16x16x32_bf16 v[110:113], v[172:175], v[204:207], v[110:113]
	v_mfma_f32_16x16x32_bf16 v[102:105], v[160:163], v[212:215], v[102:105]
	v_mfma_f32_16x16x32_bf16 v[94:97], v[172:175], v[212:215], v[94:97]
	v_mfma_f32_16x16x32_bf16 v[86:89], v[160:163], v[220:223], v[86:89]
	v_mfma_f32_16x16x32_bf16 v[78:81], v[172:175], v[220:223], v[78:81]
	s_setprio 0
	s_setprio 1
	v_mfma_f32_16x16x32_bf16 v[114:117], v[176:179], v[192:195], v[114:117]
	v_mfma_f32_16x16x32_bf16 v[106:109], v[184:187], v[192:195], v[106:109]
	v_mfma_f32_16x16x32_bf16 v[98:101], v[176:179], v[200:203], v[98:101]
	v_mfma_f32_16x16x32_bf16 v[90:93], v[184:187], v[200:203], v[90:93]
	v_mfma_f32_16x16x32_bf16 v[82:85], v[176:179], v[208:211], v[82:85]
	v_mfma_f32_16x16x32_bf16 v[74:77], v[184:187], v[208:211], v[74:77]
	v_mfma_f32_16x16x32_bf16 v[70:73], v[176:179], v[216:219], v[70:73]
	v_mfma_f32_16x16x32_bf16 v[66:69], v[184:187], v[216:219], v[66:69]
	v_mfma_f32_16x16x32_bf16 v[114:117], v[180:183], v[196:199], v[114:117]
	v_mfma_f32_16x16x32_bf16 v[106:109], v[188:191], v[196:199], v[106:109]
	v_mfma_f32_16x16x32_bf16 v[98:101], v[180:183], v[204:207], v[98:101]
	v_mfma_f32_16x16x32_bf16 v[90:93], v[188:191], v[204:207], v[90:93]
	v_mfma_f32_16x16x32_bf16 v[82:85], v[180:183], v[212:215], v[82:85]
	v_mfma_f32_16x16x32_bf16 v[74:77], v[188:191], v[212:215], v[74:77]
	v_mfma_f32_16x16x32_bf16 v[70:73], v[180:183], v[220:223], v[70:73]
	v_mfma_f32_16x16x32_bf16 v[66:69], v[188:191], v[220:223], v[66:69]
	s_setprio 0
	s_barrier
	s_add_i32 s41, s96, s82
	v_lshl_add_u64 v[168:169], v[132:133], 0, v[136:137]
	s_mov_b32 m0, s41
	ds_read_b128 v[192:195], v159 offset:16384
	ds_read_b128 v[196:199], v159 offset:17408
	ds_read_b128 v[200:203], v159 offset:18432
	ds_read_b128 v[204:207], v159 offset:19456
	ds_read_b128 v[208:211], v159 offset:20480
	ds_read_b128 v[212:215], v159 offset:21504
	ds_read_b128 v[216:219], v159 offset:22528
	ds_read_b128 v[220:223], v159 offset:23552
	global_load_lds_dwordx4 v[168:169], off
	v_lshl_add_u64 v[168:169], v[132:133], 0, v[140:141]
	s_add_i32 m0, s41, 0x2000
	s_add_i32 s41, s97, s82
	global_load_lds_dwordx4 v[168:169], off
	v_lshl_add_u64 v[168:169], v[132:133], 0, s[12:13]
	v_lshl_add_u64 v[224:225], v[168:169], 0, v[136:137]
	s_mov_b32 m0, s41
	v_lshl_add_u64 v[168:169], v[168:169], 0, v[140:141]
	global_load_lds_dwordx4 v[224:225], off
	s_add_i32 m0, s41, 0x2000
	s_nop 0
	global_load_lds_dwordx4 v[168:169], off
	v_lshl_add_u64 v[168:169], s[66:67], 0, v[134:135]
	s_mov_b32 m0, s84
	s_nop 0
	global_load_lds_dwordx4 v[168:169], off
	v_lshl_add_u64 v[168:169], s[66:67], 0, v[138:139]
	s_mov_b32 m0, s85
	s_nop 0
	global_load_lds_dwordx4 v[168:169], off
	s_waitcnt vmcnt(8)
	s_waitcnt lgkmcnt(0)
	s_barrier
	s_setprio 1
	v_mfma_f32_16x16x32_bf16 v[62:65], v[150:153], v[192:195], v[62:65]
	v_mfma_f32_16x16x32_bf16 v[58:61], v[164:167], v[192:195], v[58:61]
	v_mfma_f32_16x16x32_bf16 v[54:57], v[150:153], v[200:203], v[54:57]
	v_mfma_f32_16x16x32_bf16 v[46:49], v[164:167], v[200:203], v[46:49]
	v_mfma_f32_16x16x32_bf16 v[38:41], v[150:153], v[208:211], v[38:41]
	v_mfma_f32_16x16x32_bf16 v[30:33], v[164:167], v[208:211], v[30:33]
	v_mfma_f32_16x16x32_bf16 v[22:25], v[150:153], v[216:219], v[22:25]
	v_mfma_f32_16x16x32_bf16 v[14:17], v[164:167], v[216:219], v[14:17]
	v_mfma_f32_16x16x32_bf16 v[62:65], v[160:163], v[196:199], v[62:65]
	v_mfma_f32_16x16x32_bf16 v[58:61], v[172:175], v[196:199], v[58:61]
	v_mfma_f32_16x16x32_bf16 v[54:57], v[160:163], v[204:207], v[54:57]
	v_mfma_f32_16x16x32_bf16 v[46:49], v[172:175], v[204:207], v[46:49]
	v_mfma_f32_16x16x32_bf16 v[38:41], v[160:163], v[212:215], v[38:41]
	v_mfma_f32_16x16x32_bf16 v[30:33], v[172:175], v[212:215], v[30:33]
	v_mfma_f32_16x16x32_bf16 v[22:25], v[160:163], v[220:223], v[22:25]
	v_mfma_f32_16x16x32_bf16 v[14:17], v[172:175], v[220:223], v[14:17]
	s_setprio 0
	s_setprio 1
	v_mfma_f32_16x16x32_bf16 v[50:53], v[176:179], v[192:195], v[50:53]
	v_mfma_f32_16x16x32_bf16 v[42:45], v[184:187], v[192:195], v[42:45]
	v_mfma_f32_16x16x32_bf16 v[34:37], v[176:179], v[200:203], v[34:37]
	v_mfma_f32_16x16x32_bf16 v[26:29], v[184:187], v[200:203], v[26:29]
	v_mfma_f32_16x16x32_bf16 v[18:21], v[176:179], v[208:211], v[18:21]
	v_mfma_f32_16x16x32_bf16 v[10:13], v[184:187], v[208:211], v[10:13]
	v_mfma_f32_16x16x32_bf16 v[6:9], v[176:179], v[216:219], v[6:9]
	v_mfma_f32_16x16x32_bf16 v[2:5], v[184:187], v[216:219], v[2:5]
	v_mfma_f32_16x16x32_bf16 v[50:53], v[180:183], v[196:199], v[50:53]
	v_mfma_f32_16x16x32_bf16 v[42:45], v[188:191], v[196:199], v[42:45]
	v_mfma_f32_16x16x32_bf16 v[34:37], v[180:183], v[204:207], v[34:37]
	v_mfma_f32_16x16x32_bf16 v[26:29], v[188:191], v[204:207], v[26:29]
	v_mfma_f32_16x16x32_bf16 v[18:21], v[180:183], v[212:215], v[18:21]
	v_mfma_f32_16x16x32_bf16 v[10:13], v[188:191], v[212:215], v[10:13]
	v_mfma_f32_16x16x32_bf16 v[6:9], v[180:183], v[220:223], v[6:9]
	v_mfma_f32_16x16x32_bf16 v[2:5], v[188:191], v[220:223], v[2:5]
	s_setprio 0
	s_barrier
	s_add_i32 s41, 0, 0x18000
	v_add_u32_e32 v142, s41, v154
	s_add_i32 vcc_lo, 0, 0x1c000
	ds_read_b128 v[150:153], v142
	ds_read_b128 v[160:163], v142 offset:1024
	ds_read_b128 v[164:167], v142 offset:2048
	ds_read_b128 v[172:175], v142 offset:3072
	v_add_u32_e32 v142, vcc_lo, v154
	ds_read_b128 v[176:179], v142
	ds_read_b128 v[180:183], v142 offset:1024
	ds_read_b128 v[184:187], v142 offset:2048
	ds_read_b128 v[188:191], v142 offset:3072
	s_add_u32 s66, s66, 0x4000
	s_addc_u32 s67, s67, 0
	s_mov_b32 m0, s86
	v_lshl_add_u64 v[168:169], s[66:67], 0, v[134:135]
	ds_read_b128 v[192:195], v159 offset:32768
	ds_read_b128 v[196:199], v159 offset:33792
	ds_read_b128 v[200:203], v159 offset:34816
	ds_read_b128 v[204:207], v159 offset:35840
	ds_read_b128 v[208:211], v159 offset:36864
	ds_read_b128 v[212:215], v159 offset:37888
	ds_read_b128 v[216:219], v159 offset:38912
	ds_read_b128 v[220:223], v159 offset:39936
	global_load_lds_dwordx4 v[168:169], off
	v_lshl_add_u64 v[168:169], s[66:67], 0, v[138:139]
	s_mov_b32 m0, s87
	s_nop 0
	global_load_lds_dwordx4 v[168:169], off
	s_waitcnt vmcnt(8)
	s_waitcnt lgkmcnt(0)
	s_barrier
	s_setprio 1
	v_mfma_f32_16x16x32_bf16 v[126:129], v[150:153], v[192:195], v[126:129]
	v_mfma_f32_16x16x32_bf16 v[122:125], v[164:167], v[192:195], v[122:125]
	v_mfma_f32_16x16x32_bf16 v[118:121], v[150:153], v[200:203], v[118:121]
	v_mfma_f32_16x16x32_bf16 v[110:113], v[164:167], v[200:203], v[110:113]
	v_mfma_f32_16x16x32_bf16 v[102:105], v[150:153], v[208:211], v[102:105]
	v_mfma_f32_16x16x32_bf16 v[94:97], v[164:167], v[208:211], v[94:97]
	v_mfma_f32_16x16x32_bf16 v[86:89], v[150:153], v[216:219], v[86:89]
	v_mfma_f32_16x16x32_bf16 v[78:81], v[164:167], v[216:219], v[78:81]
	v_mfma_f32_16x16x32_bf16 v[126:129], v[160:163], v[196:199], v[126:129]
	v_mfma_f32_16x16x32_bf16 v[122:125], v[172:175], v[196:199], v[122:125]
	v_mfma_f32_16x16x32_bf16 v[118:121], v[160:163], v[204:207], v[118:121]
	v_mfma_f32_16x16x32_bf16 v[110:113], v[172:175], v[204:207], v[110:113]
	v_mfma_f32_16x16x32_bf16 v[102:105], v[160:163], v[212:215], v[102:105]
	v_mfma_f32_16x16x32_bf16 v[94:97], v[172:175], v[212:215], v[94:97]
	v_mfma_f32_16x16x32_bf16 v[86:89], v[160:163], v[220:223], v[86:89]
	v_mfma_f32_16x16x32_bf16 v[78:81], v[172:175], v[220:223], v[78:81]
	s_setprio 0
	s_setprio 1
	v_mfma_f32_16x16x32_bf16 v[114:117], v[176:179], v[192:195], v[114:117]
	v_mfma_f32_16x16x32_bf16 v[106:109], v[184:187], v[192:195], v[106:109]
	v_mfma_f32_16x16x32_bf16 v[98:101], v[176:179], v[200:203], v[98:101]
	v_mfma_f32_16x16x32_bf16 v[90:93], v[184:187], v[200:203], v[90:93]
	v_mfma_f32_16x16x32_bf16 v[82:85], v[176:179], v[208:211], v[82:85]
	v_mfma_f32_16x16x32_bf16 v[74:77], v[184:187], v[208:211], v[74:77]
	v_mfma_f32_16x16x32_bf16 v[70:73], v[176:179], v[216:219], v[70:73]
	v_mfma_f32_16x16x32_bf16 v[66:69], v[184:187], v[216:219], v[66:69]
	v_mfma_f32_16x16x32_bf16 v[114:117], v[180:183], v[196:199], v[114:117]
	v_mfma_f32_16x16x32_bf16 v[106:109], v[188:191], v[196:199], v[106:109]
	v_mfma_f32_16x16x32_bf16 v[98:101], v[180:183], v[204:207], v[98:101]
	v_mfma_f32_16x16x32_bf16 v[90:93], v[188:191], v[204:207], v[90:93]
	v_mfma_f32_16x16x32_bf16 v[82:85], v[180:183], v[212:215], v[82:85]
	v_mfma_f32_16x16x32_bf16 v[74:77], v[188:191], v[212:215], v[74:77]
	v_mfma_f32_16x16x32_bf16 v[70:73], v[180:183], v[220:223], v[70:73]
	v_mfma_f32_16x16x32_bf16 v[66:69], v[188:191], v[220:223], v[66:69]
	s_setprio 0
	s_barrier
	v_lshl_add_u64 v[168:169], v[132:133], 0, s[20:21]
	s_add_i32 s41, s41, s82
	v_lshl_add_u64 v[224:225], v[168:169], 0, v[136:137]
	s_mov_b32 m0, s41
	ds_read_b128 v[192:195], v159 offset:49152
	ds_read_b128 v[196:199], v159 offset:50176
	ds_read_b128 v[200:203], v159 offset:51200
	ds_read_b128 v[204:207], v159 offset:52224
	ds_read_b128 v[208:211], v159 offset:53248
	ds_read_b128 v[212:215], v159 offset:54272
	ds_read_b128 v[216:219], v159 offset:55296
	ds_read_b128 v[220:223], v159 offset:56320
	global_load_lds_dwordx4 v[224:225], off
	v_lshl_add_u64 v[168:169], v[168:169], 0, v[140:141]
	s_add_i32 m0, s41, 0x2000
	v_lshl_add_u64 v[132:133], v[132:133], 0, s[22:23]
	s_add_i32 s41, vcc_lo, s82
	global_load_lds_dwordx4 v[168:169], off
	v_lshl_add_u64 v[168:169], v[132:133], 0, v[136:137]
	s_mov_b32 m0, s41
	v_lshl_add_u64 v[132:133], v[132:133], 0, v[140:141]
	global_load_lds_dwordx4 v[168:169], off
	s_add_i32 m0, s41, 0x2000
	s_nop 0
	global_load_lds_dwordx4 v[132:133], off
	v_lshl_add_u64 v[132:133], s[64:65], 0, v[134:135]
	s_mov_b32 m0, s94
	s_nop 0
	global_load_lds_dwordx4 v[132:133], off
	v_lshl_add_u64 v[132:133], s[64:65], 0, v[138:139]
	s_mov_b32 m0, s95
	s_nop 0
	global_load_lds_dwordx4 v[132:133], off
	s_waitcnt vmcnt(8)
	s_waitcnt lgkmcnt(0)
	s_barrier
	s_setprio 1
	v_mfma_f32_16x16x32_bf16 v[62:65], v[150:153], v[192:195], v[62:65]
	v_mfma_f32_16x16x32_bf16 v[58:61], v[164:167], v[192:195], v[58:61]
	v_mfma_f32_16x16x32_bf16 v[54:57], v[150:153], v[200:203], v[54:57]
	v_mfma_f32_16x16x32_bf16 v[46:49], v[164:167], v[200:203], v[46:49]
	v_mfma_f32_16x16x32_bf16 v[38:41], v[150:153], v[208:211], v[38:41]
	v_mfma_f32_16x16x32_bf16 v[30:33], v[164:167], v[208:211], v[30:33]
	v_mfma_f32_16x16x32_bf16 v[22:25], v[150:153], v[216:219], v[22:25]
	v_mfma_f32_16x16x32_bf16 v[14:17], v[164:167], v[216:219], v[14:17]
	v_mfma_f32_16x16x32_bf16 v[62:65], v[160:163], v[196:199], v[62:65]
	v_mfma_f32_16x16x32_bf16 v[58:61], v[172:175], v[196:199], v[58:61]
	v_mfma_f32_16x16x32_bf16 v[54:57], v[160:163], v[204:207], v[54:57]
	v_mfma_f32_16x16x32_bf16 v[46:49], v[172:175], v[204:207], v[46:49]
	v_mfma_f32_16x16x32_bf16 v[38:41], v[160:163], v[212:215], v[38:41]
	v_mfma_f32_16x16x32_bf16 v[30:33], v[172:175], v[212:215], v[30:33]
	v_mfma_f32_16x16x32_bf16 v[22:25], v[160:163], v[220:223], v[22:25]
	v_mfma_f32_16x16x32_bf16 v[14:17], v[172:175], v[220:223], v[14:17]
	s_setprio 0
	s_setprio 1
	v_mfma_f32_16x16x32_bf16 v[50:53], v[176:179], v[192:195], v[50:53]
	v_mfma_f32_16x16x32_bf16 v[42:45], v[184:187], v[192:195], v[42:45]
	v_mfma_f32_16x16x32_bf16 v[34:37], v[176:179], v[200:203], v[34:37]
	v_mfma_f32_16x16x32_bf16 v[26:29], v[184:187], v[200:203], v[26:29]
	v_mfma_f32_16x16x32_bf16 v[18:21], v[176:179], v[208:211], v[18:21]
	v_mfma_f32_16x16x32_bf16 v[10:13], v[184:187], v[208:211], v[10:13]
	v_mfma_f32_16x16x32_bf16 v[6:9], v[176:179], v[216:219], v[6:9]
	v_mfma_f32_16x16x32_bf16 v[2:5], v[184:187], v[216:219], v[2:5]
	v_mfma_f32_16x16x32_bf16 v[50:53], v[180:183], v[196:199], v[50:53]
	v_mfma_f32_16x16x32_bf16 v[42:45], v[188:191], v[196:199], v[42:45]
	v_mfma_f32_16x16x32_bf16 v[34:37], v[180:183], v[204:207], v[34:37]
	v_mfma_f32_16x16x32_bf16 v[26:29], v[188:191], v[204:207], v[26:29]
	v_mfma_f32_16x16x32_bf16 v[18:21], v[180:183], v[212:215], v[18:21]
	v_mfma_f32_16x16x32_bf16 v[10:13], v[188:191], v[212:215], v[10:13]
	v_mfma_f32_16x16x32_bf16 v[6:9], v[180:183], v[220:223], v[6:9]
	v_mfma_f32_16x16x32_bf16 v[2:5], v[188:191], v[220:223], v[2:5]
	s_setprio 0
	s_barrier
	s_add_u32 s62, s62, 0x10000
	s_addc_u32 s63, s63, 0
	v_lshl_add_u64 v[130:131], v[130:131], 0, s[48:49]
	s_cmp_ge_u32 s40, s28
	s_mov_b32 s64, s40
	s_cbranch_scc0 .LBB0_1616
	s_and_b64 vcc, exec, s[42:43]
	s_cbranch_vccz .LBB0_1619
	s_barrier

.LBB0_1794:
	ds_read_b128 v[150:153], v171
	ds_read_b128 v[154:157], v171 offset:1024
	ds_read_b128 v[158:161], v171 offset:2048
	ds_read_b128 v[162:165], v171 offset:3072
	ds_read_b128 v[166:169], v220
	ds_read_b128 v[172:175], v220 offset:1024
	ds_read_b128 v[176:179], v220 offset:2048
	ds_read_b128 v[180:183], v220 offset:3072
	s_add_u32 s29, s46, 0xfffc0080
	s_addc_u32 s31, s47, -1
	s_cmp_eq_u32 s28, 12
	s_cselect_b32 s51, s23, s31
	s_cselect_b32 s50, s22, s29
	s_cselect_b32 s49, s43, s21
	s_cselect_b32 s48, s42, s19
	v_lshl_add_u64 v[216:217], s[46:47], 0, v[142:143]
	s_add_i32 m0, s9, 0xc000
	ds_read_b128 v[184:187], v221
	ds_read_b128 v[188:191], v221 offset:1024
	ds_read_b128 v[192:195], v221 offset:2048
	ds_read_b128 v[196:199], v221 offset:3072
	ds_read_b128 v[200:203], v221 offset:4096
	ds_read_b128 v[204:207], v221 offset:5120
	ds_read_b128 v[208:211], v221 offset:6144
	ds_read_b128 v[212:215], v221 offset:7168
	global_load_lds_dwordx4 v[216:217], off
	v_lshl_add_u64 v[216:217], s[46:47], 0, v[144:145]
	s_add_i32 m0, s9, 0xe000
	s_nop 0
	global_load_lds_dwordx4 v[216:217], off
	s_waitcnt vmcnt(8)
	s_waitcnt lgkmcnt(0)
	s_barrier
	s_setprio 1
	v_mfma_f32_16x16x32_bf16 v[126:129], v[150:153], v[184:187], v[126:129]
	v_mfma_f32_16x16x32_bf16 v[122:125], v[158:161], v[184:187], v[122:125]
	v_mfma_f32_16x16x32_bf16 v[110:113], v[150:153], v[192:195], v[110:113]
	v_mfma_f32_16x16x32_bf16 v[106:109], v[158:161], v[192:195], v[106:109]
	v_mfma_f32_16x16x32_bf16 v[94:97], v[150:153], v[200:203], v[94:97]
	v_mfma_f32_16x16x32_bf16 v[90:93], v[158:161], v[200:203], v[90:93]
	v_mfma_f32_16x16x32_bf16 v[58:61], v[150:153], v[208:211], v[58:61]
	v_mfma_f32_16x16x32_bf16 v[22:25], v[158:161], v[208:211], v[22:25]
	v_mfma_f32_16x16x32_bf16 v[126:129], v[154:157], v[188:191], v[126:129]
	v_mfma_f32_16x16x32_bf16 v[122:125], v[162:165], v[188:191], v[122:125]
	v_mfma_f32_16x16x32_bf16 v[110:113], v[154:157], v[196:199], v[110:113]
	v_mfma_f32_16x16x32_bf16 v[106:109], v[162:165], v[196:199], v[106:109]
	v_mfma_f32_16x16x32_bf16 v[94:97], v[154:157], v[204:207], v[94:97]
	v_mfma_f32_16x16x32_bf16 v[90:93], v[162:165], v[204:207], v[90:93]
	v_mfma_f32_16x16x32_bf16 v[58:61], v[154:157], v[212:215], v[58:61]
	v_mfma_f32_16x16x32_bf16 v[22:25], v[162:165], v[212:215], v[22:25]
	s_setprio 0
	s_setprio 1
	v_mfma_f32_16x16x32_bf16 v[118:121], v[166:169], v[184:187], v[118:121]
	v_mfma_f32_16x16x32_bf16 v[114:117], v[176:179], v[184:187], v[114:117]
	v_mfma_f32_16x16x32_bf16 v[102:105], v[166:169], v[192:195], v[102:105]
	v_mfma_f32_16x16x32_bf16 v[98:101], v[176:179], v[192:195], v[98:101]
	v_mfma_f32_16x16x32_bf16 v[86:89], v[166:169], v[200:203], v[86:89]
	v_mfma_f32_16x16x32_bf16 v[82:85], v[176:179], v[200:203], v[82:85]
	v_mfma_f32_16x16x32_bf16 v[78:81], v[166:169], v[208:211], v[78:81]
	v_mfma_f32_16x16x32_bf16 v[74:77], v[176:179], v[208:211], v[74:77]
	v_mfma_f32_16x16x32_bf16 v[118:121], v[172:175], v[188:191], v[118:121]
	v_mfma_f32_16x16x32_bf16 v[114:117], v[180:183], v[188:191], v[114:117]
	v_mfma_f32_16x16x32_bf16 v[102:105], v[172:175], v[196:199], v[102:105]
	v_mfma_f32_16x16x32_bf16 v[98:101], v[180:183], v[196:199], v[98:101]
	v_mfma_f32_16x16x32_bf16 v[86:89], v[172:175], v[204:207], v[86:89]
	v_mfma_f32_16x16x32_bf16 v[82:85], v[180:183], v[204:207], v[82:85]
	v_mfma_f32_16x16x32_bf16 v[78:81], v[172:175], v[212:215], v[78:81]
	v_mfma_f32_16x16x32_bf16 v[74:77], v[180:183], v[212:215], v[74:77]
	s_setprio 0
	s_barrier
	s_add_i32 s29, s66, s54
	v_lshl_add_u64 v[216:217], s[48:49], 0, v[132:133]
	s_mov_b32 m0, s29
	ds_read_b128 v[184:187], v221 offset:16384
	ds_read_b128 v[188:191], v221 offset:17408
	ds_read_b128 v[192:195], v221 offset:18432
	ds_read_b128 v[196:199], v221 offset:19456
	ds_read_b128 v[200:203], v221 offset:20480
	ds_read_b128 v[204:207], v221 offset:21504
	ds_read_b128 v[208:211], v221 offset:22528
	ds_read_b128 v[212:215], v221 offset:23552
	global_load_lds_dwordx4 v[216:217], off
	s_add_i32 m0, s29, 0x2000
	s_add_u32 s36, s48, 0x40000
	v_lshl_add_u64 v[218:219], s[48:49], 0, v[136:137]
	s_addc_u32 s37, s49, 0
	s_add_i32 s29, s67, s54
	global_load_lds_dwordx4 v[218:219], off
	v_lshl_add_u64 v[224:225], s[36:37], 0, v[132:133]
	s_mov_b32 m0, s29
	v_lshl_add_u64 v[226:227], s[50:51], 0, v[134:135]
	global_load_lds_dwordx4 v[224:225], off
	v_lshl_add_u64 v[224:225], s[36:37], 0, v[136:137]
	s_add_i32 m0, s29, 0x2000
	s_nop 0
	global_load_lds_dwordx4 v[224:225], off
	v_lshl_add_u64 v[224:225], s[50:51], 0, v[130:131]
	s_mov_b32 m0, s9
	s_nop 0
	global_load_lds_dwordx4 v[224:225], off
	s_mov_b32 m0, s55
	s_nop 0
	global_load_lds_dwordx4 v[226:227], off
	s_waitcnt vmcnt(8)
	s_waitcnt lgkmcnt(0)
	s_barrier
	s_setprio 1
	v_mfma_f32_16x16x32_bf16 v[38:41], v[150:153], v[184:187], v[38:41]
	v_mfma_f32_16x16x32_bf16 v[14:17], v[158:161], v[184:187], v[14:17]
	v_mfma_f32_16x16x32_bf16 v[30:33], v[150:153], v[192:195], v[30:33]
	v_mfma_f32_16x16x32_bf16 v[10:13], v[158:161], v[192:195], v[10:13]
	v_mfma_f32_16x16x32_bf16 v[26:29], v[150:153], v[200:203], v[26:29]
	v_mfma_f32_16x16x32_bf16 v[6:9], v[158:161], v[200:203], v[6:9]
	v_mfma_f32_16x16x32_bf16 v[18:21], v[150:153], v[208:211], v[18:21]
	v_mfma_f32_16x16x32_bf16 v[2:5], v[158:161], v[208:211], v[2:5]
	v_mfma_f32_16x16x32_bf16 v[38:41], v[154:157], v[188:191], v[38:41]
	v_mfma_f32_16x16x32_bf16 v[14:17], v[162:165], v[188:191], v[14:17]
	v_mfma_f32_16x16x32_bf16 v[30:33], v[154:157], v[196:199], v[30:33]
	v_mfma_f32_16x16x32_bf16 v[10:13], v[162:165], v[196:199], v[10:13]
	v_mfma_f32_16x16x32_bf16 v[26:29], v[154:157], v[204:207], v[26:29]
	v_mfma_f32_16x16x32_bf16 v[6:9], v[162:165], v[204:207], v[6:9]
	v_mfma_f32_16x16x32_bf16 v[18:21], v[154:157], v[212:215], v[18:21]
	v_mfma_f32_16x16x32_bf16 v[2:5], v[162:165], v[212:215], v[2:5]
	s_setprio 0
	s_setprio 1
	v_mfma_f32_16x16x32_bf16 v[70:73], v[166:169], v[184:187], v[70:73]
	v_mfma_f32_16x16x32_bf16 v[54:57], v[176:179], v[184:187], v[54:57]
	v_mfma_f32_16x16x32_bf16 v[66:69], v[166:169], v[192:195], v[66:69]
	v_mfma_f32_16x16x32_bf16 v[46:49], v[176:179], v[192:195], v[46:49]
	v_mfma_f32_16x16x32_bf16 v[62:65], v[166:169], v[200:203], v[62:65]
	v_mfma_f32_16x16x32_bf16 v[42:45], v[176:179], v[200:203], v[42:45]
	v_mfma_f32_16x16x32_bf16 v[50:53], v[166:169], v[208:211], v[50:53]
	v_mfma_f32_16x16x32_bf16 v[34:37], v[176:179], v[208:211], v[34:37]
	v_mfma_f32_16x16x32_bf16 v[70:73], v[172:175], v[188:191], v[70:73]
	v_mfma_f32_16x16x32_bf16 v[54:57], v[180:183], v[188:191], v[54:57]
	v_mfma_f32_16x16x32_bf16 v[66:69], v[172:175], v[196:199], v[66:69]
	v_mfma_f32_16x16x32_bf16 v[46:49], v[180:183], v[196:199], v[46:49]
	v_mfma_f32_16x16x32_bf16 v[62:65], v[172:175], v[204:207], v[62:65]
	v_mfma_f32_16x16x32_bf16 v[42:45], v[180:183], v[204:207], v[42:45]
	v_mfma_f32_16x16x32_bf16 v[50:53], v[172:175], v[212:215], v[50:53]
	v_mfma_f32_16x16x32_bf16 v[34:37], v[180:183], v[212:215], v[34:37]
	s_setprio 0
	s_barrier
	s_add_i32 s29, 0, 0x18000
	v_add_u32_e32 v138, s29, v141
	s_add_i32 s31, 0, 0x1c000
	ds_read_b128 v[150:153], v138
	ds_read_b128 v[154:157], v138 offset:1024
	ds_read_b128 v[158:161], v138 offset:2048
	ds_read_b128 v[162:165], v138 offset:3072
	v_add_u32_e32 v138, s31, v141
	ds_read_b128 v[166:169], v138
	ds_read_b128 v[172:175], v138 offset:1024
	ds_read_b128 v[176:179], v138 offset:2048
	ds_read_b128 v[180:183], v138 offset:3072
	s_add_u32 s36, s50, 0x40000
	s_addc_u32 s37, s51, 0
	s_mov_b32 m0, s56
	v_lshl_add_u64 v[228:229], s[36:37], 0, v[130:131]
	ds_read_b128 v[184:187], v221 offset:32768
	ds_read_b128 v[188:191], v221 offset:33792
	ds_read_b128 v[192:195], v221 offset:34816
	ds_read_b128 v[196:199], v221 offset:35840
	ds_read_b128 v[200:203], v221 offset:36864
	ds_read_b128 v[204:207], v221 offset:37888
	ds_read_b128 v[208:211], v221 offset:38912
	ds_read_b128 v[212:215], v221 offset:39936
	global_load_lds_dwordx4 v[228:229], off
	v_lshl_add_u64 v[228:229], s[36:37], 0, v[134:135]
	s_mov_b32 m0, s57
	s_nop 0
	global_load_lds_dwordx4 v[228:229], off
	s_waitcnt vmcnt(8)
	s_waitcnt lgkmcnt(0)
	s_barrier
	s_setprio 1
	v_mfma_f32_16x16x32_bf16 v[126:129], v[150:153], v[184:187], v[126:129]
	v_mfma_f32_16x16x32_bf16 v[122:125], v[158:161], v[184:187], v[122:125]
	v_mfma_f32_16x16x32_bf16 v[110:113], v[150:153], v[192:195], v[110:113]
	v_mfma_f32_16x16x32_bf16 v[106:109], v[158:161], v[192:195], v[106:109]
	v_mfma_f32_16x16x32_bf16 v[94:97], v[150:153], v[200:203], v[94:97]
	v_mfma_f32_16x16x32_bf16 v[90:93], v[158:161], v[200:203], v[90:93]
	v_mfma_f32_16x16x32_bf16 v[58:61], v[150:153], v[208:211], v[58:61]
	v_mfma_f32_16x16x32_bf16 v[22:25], v[158:161], v[208:211], v[22:25]
	v_mfma_f32_16x16x32_bf16 v[126:129], v[154:157], v[188:191], v[126:129]
	v_mfma_f32_16x16x32_bf16 v[122:125], v[162:165], v[188:191], v[122:125]
	v_mfma_f32_16x16x32_bf16 v[110:113], v[154:157], v[196:199], v[110:113]
	v_mfma_f32_16x16x32_bf16 v[106:109], v[162:165], v[196:199], v[106:109]
	v_mfma_f32_16x16x32_bf16 v[94:97], v[154:157], v[204:207], v[94:97]
	v_mfma_f32_16x16x32_bf16 v[90:93], v[162:165], v[204:207], v[90:93]
	v_mfma_f32_16x16x32_bf16 v[58:61], v[154:157], v[212:215], v[58:61]
	v_mfma_f32_16x16x32_bf16 v[22:25], v[162:165], v[212:215], v[22:25]
	s_setprio 0
	s_setprio 1
	v_mfma_f32_16x16x32_bf16 v[118:121], v[166:169], v[184:187], v[118:121]
	v_mfma_f32_16x16x32_bf16 v[114:117], v[176:179], v[184:187], v[114:117]
	v_mfma_f32_16x16x32_bf16 v[102:105], v[166:169], v[192:195], v[102:105]
	v_mfma_f32_16x16x32_bf16 v[98:101], v[176:179], v[192:195], v[98:101]
	v_mfma_f32_16x16x32_bf16 v[86:89], v[166:169], v[200:203], v[86:89]
	v_mfma_f32_16x16x32_bf16 v[82:85], v[176:179], v[200:203], v[82:85]
	v_mfma_f32_16x16x32_bf16 v[78:81], v[166:169], v[208:211], v[78:81]
	v_mfma_f32_16x16x32_bf16 v[74:77], v[176:179], v[208:211], v[74:77]
	v_mfma_f32_16x16x32_bf16 v[118:121], v[172:175], v[188:191], v[118:121]
	v_mfma_f32_16x16x32_bf16 v[114:117], v[180:183], v[188:191], v[114:117]
	v_mfma_f32_16x16x32_bf16 v[102:105], v[172:175], v[196:199], v[102:105]
	v_mfma_f32_16x16x32_bf16 v[98:101], v[180:183], v[196:199], v[98:101]
	v_mfma_f32_16x16x32_bf16 v[86:89], v[172:175], v[204:207], v[86:89]
	v_mfma_f32_16x16x32_bf16 v[82:85], v[180:183], v[204:207], v[82:85]
	v_mfma_f32_16x16x32_bf16 v[78:81], v[172:175], v[212:215], v[78:81]
	v_mfma_f32_16x16x32_bf16 v[74:77], v[180:183], v[212:215], v[74:77]
	s_setprio 0
	s_barrier
	s_add_i32 s29, s29, s54
	v_lshl_add_u64 v[216:217], v[216:217], 0, s[14:15]
	s_mov_b32 m0, s29
	ds_read_b128 v[184:187], v221 offset:49152
	ds_read_b128 v[188:191], v221 offset:50176
	ds_read_b128 v[192:195], v221 offset:51200
	ds_read_b128 v[196:199], v221 offset:52224
	ds_read_b128 v[200:203], v221 offset:53248
	ds_read_b128 v[204:207], v221 offset:54272
	ds_read_b128 v[208:211], v221 offset:55296
	ds_read_b128 v[212:215], v221 offset:56320
	global_load_lds_dwordx4 v[216:217], off
	s_add_i32 m0, s29, 0x2000
	s_add_u32 s36, s48, 0x40080
	v_lshl_add_u64 v[216:217], v[218:219], 0, s[14:15]
	s_addc_u32 s37, s49, 0
	s_add_i32 s29, s31, s54
	global_load_lds_dwordx4 v[216:217], off
	v_lshl_add_u64 v[216:217], s[36:37], 0, v[132:133]
	s_mov_b32 m0, s29
	s_nop 0
	global_load_lds_dwordx4 v[216:217], off
	v_lshl_add_u64 v[216:217], s[36:37], 0, v[136:137]
	s_add_i32 m0, s29, 0x2000
	s_nop 0
	global_load_lds_dwordx4 v[216:217], off
	v_lshl_add_u64 v[216:217], v[224:225], 0, s[14:15]
	s_mov_b32 m0, s63
	s_nop 0
	global_load_lds_dwordx4 v[216:217], off
	v_lshl_add_u64 v[216:217], v[226:227], 0, s[14:15]
	s_mov_b32 m0, s64
	s_nop 0
	global_load_lds_dwordx4 v[216:217], off
	s_waitcnt vmcnt(8)
	s_waitcnt lgkmcnt(0)
	s_barrier
	s_setprio 1
	v_mfma_f32_16x16x32_bf16 v[38:41], v[150:153], v[184:187], v[38:41]
	v_mfma_f32_16x16x32_bf16 v[14:17], v[158:161], v[184:187], v[14:17]
	v_mfma_f32_16x16x32_bf16 v[30:33], v[150:153], v[192:195], v[30:33]
	v_mfma_f32_16x16x32_bf16 v[10:13], v[158:161], v[192:195], v[10:13]
	v_mfma_f32_16x16x32_bf16 v[26:29], v[150:153], v[200:203], v[26:29]
	v_mfma_f32_16x16x32_bf16 v[6:9], v[158:161], v[200:203], v[6:9]
	v_mfma_f32_16x16x32_bf16 v[18:21], v[150:153], v[208:211], v[18:21]
	v_mfma_f32_16x16x32_bf16 v[2:5], v[158:161], v[208:211], v[2:5]
	v_mfma_f32_16x16x32_bf16 v[38:41], v[154:157], v[188:191], v[38:41]
	v_mfma_f32_16x16x32_bf16 v[14:17], v[162:165], v[188:191], v[14:17]
	v_mfma_f32_16x16x32_bf16 v[30:33], v[154:157], v[196:199], v[30:33]
	v_mfma_f32_16x16x32_bf16 v[10:13], v[162:165], v[196:199], v[10:13]
	v_mfma_f32_16x16x32_bf16 v[26:29], v[154:157], v[204:207], v[26:29]
	v_mfma_f32_16x16x32_bf16 v[6:9], v[162:165], v[204:207], v[6:9]
	v_mfma_f32_16x16x32_bf16 v[18:21], v[154:157], v[212:215], v[18:21]
	v_mfma_f32_16x16x32_bf16 v[2:5], v[162:165], v[212:215], v[2:5]
	s_setprio 0
	s_setprio 1
	v_mfma_f32_16x16x32_bf16 v[70:73], v[166:169], v[184:187], v[70:73]
	v_mfma_f32_16x16x32_bf16 v[54:57], v[176:179], v[184:187], v[54:57]
	v_mfma_f32_16x16x32_bf16 v[66:69], v[166:169], v[192:195], v[66:69]
	v_mfma_f32_16x16x32_bf16 v[46:49], v[176:179], v[192:195], v[46:49]
	v_mfma_f32_16x16x32_bf16 v[62:65], v[166:169], v[200:203], v[62:65]
	v_mfma_f32_16x16x32_bf16 v[42:45], v[176:179], v[200:203], v[42:45]
	v_mfma_f32_16x16x32_bf16 v[50:53], v[166:169], v[208:211], v[50:53]
	v_mfma_f32_16x16x32_bf16 v[34:37], v[176:179], v[208:211], v[34:37]
	v_mfma_f32_16x16x32_bf16 v[70:73], v[172:175], v[188:191], v[70:73]
	v_mfma_f32_16x16x32_bf16 v[54:57], v[180:183], v[188:191], v[54:57]
	v_mfma_f32_16x16x32_bf16 v[66:69], v[172:175], v[196:199], v[66:69]
	v_mfma_f32_16x16x32_bf16 v[46:49], v[180:183], v[196:199], v[46:49]
	v_mfma_f32_16x16x32_bf16 v[62:65], v[172:175], v[204:207], v[62:65]
	v_mfma_f32_16x16x32_bf16 v[42:45], v[180:183], v[204:207], v[42:45]
	v_mfma_f32_16x16x32_bf16 v[50:53], v[172:175], v[212:215], v[50:53]
	v_mfma_f32_16x16x32_bf16 v[34:37], v[180:183], v[212:215], v[34:37]
	s_setprio 0
	s_barrier
	s_add_i32 s28, s28, 2
	s_add_u32 s46, s46, 0x100
	s_addc_u32 s47, s47, 0
	s_add_u32 s19, s19, 0x100
	s_addc_u32 s21, s21, 0
	s_cmp_gt_u32 s28, 13
	s_cbranch_scc0 .LBB0_1794
	v_mov_b32_e32 v146, v170
	v_mov_b32_e32 v170, v250
	s_and_b64 vcc, exec, s[16:17]
	s_cbranch_vccz .LBB0_1797
	s_barrier

.LBB0_1949:
	ds_read_b128 v[130:133], v179
	ds_read_b128 v[134:137], v179 offset:1024
	ds_read_b128 v[138:141], v179 offset:2048
	ds_read_b128 v[142:145], v179 offset:3072
	ds_read_b128 v[162:165], v180
	ds_read_b128 v[166:169], v180 offset:1024
	ds_read_b128 v[172:175], v180 offset:2048
	ds_read_b128 v[182:185], v180 offset:3072
	s_add_i32 s76, s29, 2
	s_add_u32 s48, s46, 0x100
	s_addc_u32 s49, s47, 0
	s_cmp_eq_u32 s73, s29
	s_cselect_b32 s53, s43, s49
	s_cselect_b32 s52, s42, s48
	s_cselect_b32 s51, s45, s28
	s_cselect_b32 s50, s44, s75
	v_lshl_add_u64 v[176:177], s[46:47], 0, v[154:155]
	s_add_i32 m0, s58, 0xc000
	ds_read_b128 v[186:189], v181
	ds_read_b128 v[190:193], v181 offset:1024
	ds_read_b128 v[194:197], v181 offset:2048
	ds_read_b128 v[198:201], v181 offset:3072
	ds_read_b128 v[202:205], v181 offset:4096
	ds_read_b128 v[206:209], v181 offset:5120
	ds_read_b128 v[210:213], v181 offset:6144
	ds_read_b128 v[214:217], v181 offset:7168
	global_load_lds_dwordx4 v[176:177], off
	v_lshl_add_u64 v[176:177], s[46:47], 0, v[156:157]
	s_add_i32 m0, s58, 0xe000
	s_nop 0
	global_load_lds_dwordx4 v[176:177], off
	s_waitcnt vmcnt(8)
	s_waitcnt lgkmcnt(0)
	s_barrier
	s_setprio 1
	v_mfma_f32_16x16x32_bf16 v[126:129], v[130:133], v[186:189], v[126:129]
	v_mfma_f32_16x16x32_bf16 v[122:125], v[138:141], v[186:189], v[122:125]
	v_mfma_f32_16x16x32_bf16 v[118:121], v[130:133], v[194:197], v[118:121]
	v_mfma_f32_16x16x32_bf16 v[110:113], v[138:141], v[194:197], v[110:113]
	v_mfma_f32_16x16x32_bf16 v[102:105], v[130:133], v[202:205], v[102:105]
	v_mfma_f32_16x16x32_bf16 v[94:97], v[138:141], v[202:205], v[94:97]
	v_mfma_f32_16x16x32_bf16 v[86:89], v[130:133], v[210:213], v[86:89]
	v_mfma_f32_16x16x32_bf16 v[78:81], v[138:141], v[210:213], v[78:81]
	v_mfma_f32_16x16x32_bf16 v[126:129], v[134:137], v[190:193], v[126:129]
	v_mfma_f32_16x16x32_bf16 v[122:125], v[142:145], v[190:193], v[122:125]
	v_mfma_f32_16x16x32_bf16 v[118:121], v[134:137], v[198:201], v[118:121]
	v_mfma_f32_16x16x32_bf16 v[110:113], v[142:145], v[198:201], v[110:113]
	v_mfma_f32_16x16x32_bf16 v[102:105], v[134:137], v[206:209], v[102:105]
	v_mfma_f32_16x16x32_bf16 v[94:97], v[142:145], v[206:209], v[94:97]
	v_mfma_f32_16x16x32_bf16 v[86:89], v[134:137], v[214:217], v[86:89]
	v_mfma_f32_16x16x32_bf16 v[78:81], v[142:145], v[214:217], v[78:81]
	s_setprio 0
	s_setprio 1
	v_mfma_f32_16x16x32_bf16 v[114:117], v[162:165], v[186:189], v[114:117]
	v_mfma_f32_16x16x32_bf16 v[106:109], v[172:175], v[186:189], v[106:109]
	v_mfma_f32_16x16x32_bf16 v[98:101], v[162:165], v[194:197], v[98:101]
	v_mfma_f32_16x16x32_bf16 v[90:93], v[172:175], v[194:197], v[90:93]
	v_mfma_f32_16x16x32_bf16 v[82:85], v[162:165], v[202:205], v[82:85]
	v_mfma_f32_16x16x32_bf16 v[74:77], v[172:175], v[202:205], v[74:77]
	v_mfma_f32_16x16x32_bf16 v[70:73], v[162:165], v[210:213], v[70:73]
	v_mfma_f32_16x16x32_bf16 v[66:69], v[172:175], v[210:213], v[66:69]
	v_mfma_f32_16x16x32_bf16 v[114:117], v[166:169], v[190:193], v[114:117]
	v_mfma_f32_16x16x32_bf16 v[106:109], v[182:185], v[190:193], v[106:109]
	v_mfma_f32_16x16x32_bf16 v[98:101], v[166:169], v[198:201], v[98:101]
	v_mfma_f32_16x16x32_bf16 v[90:93], v[182:185], v[198:201], v[90:93]
	v_mfma_f32_16x16x32_bf16 v[82:85], v[166:169], v[206:209], v[82:85]
	v_mfma_f32_16x16x32_bf16 v[74:77], v[182:185], v[206:209], v[74:77]
	v_mfma_f32_16x16x32_bf16 v[70:73], v[166:169], v[214:217], v[70:73]
	v_mfma_f32_16x16x32_bf16 v[66:69], v[182:185], v[214:217], v[66:69]
	s_setprio 0
	s_barrier
	s_add_i32 s29, s66, s57
	v_lshl_add_u64 v[176:177], s[50:51], 0, v[148:149]
	s_mov_b32 m0, s29
	ds_read_b128 v[186:189], v181 offset:16384
	ds_read_b128 v[190:193], v181 offset:17408
	ds_read_b128 v[194:197], v181 offset:18432
	ds_read_b128 v[198:201], v181 offset:19456
	ds_read_b128 v[202:205], v181 offset:20480
	ds_read_b128 v[206:209], v181 offset:21504
	ds_read_b128 v[210:213], v181 offset:22528
	ds_read_b128 v[214:217], v181 offset:23552
	global_load_lds_dwordx4 v[176:177], off
	s_add_i32 m0, s29, 0x2000
	s_add_u32 s46, s50, 0x4000
	v_lshl_add_u64 v[176:177], s[50:51], 0, v[152:153]
	s_addc_u32 s47, s51, 0
	s_add_i32 s29, s67, s57
	global_load_lds_dwordx4 v[176:177], off
	v_lshl_add_u64 v[176:177], s[46:47], 0, v[148:149]
	s_mov_b32 m0, s29
	v_lshl_add_u64 v[218:219], s[52:53], 0, v[150:151]
	global_load_lds_dwordx4 v[176:177], off
	v_lshl_add_u64 v[176:177], s[46:47], 0, v[152:153]
	s_add_i32 m0, s29, 0x2000
	s_nop 0
	global_load_lds_dwordx4 v[176:177], off
	v_lshl_add_u64 v[176:177], s[52:53], 0, v[146:147]
	s_mov_b32 m0, s58
	s_nop 0
	global_load_lds_dwordx4 v[176:177], off
	s_mov_b32 m0, s59
	s_nop 0
	global_load_lds_dwordx4 v[218:219], off
	s_waitcnt vmcnt(8)
	s_waitcnt lgkmcnt(0)
	s_barrier
	s_setprio 1
	v_mfma_f32_16x16x32_bf16 v[62:65], v[130:133], v[186:189], v[62:65]
	v_mfma_f32_16x16x32_bf16 v[58:61], v[138:141], v[186:189], v[58:61]
	v_mfma_f32_16x16x32_bf16 v[54:57], v[130:133], v[194:197], v[54:57]
	v_mfma_f32_16x16x32_bf16 v[46:49], v[138:141], v[194:197], v[46:49]
	v_mfma_f32_16x16x32_bf16 v[38:41], v[130:133], v[202:205], v[38:41]
	v_mfma_f32_16x16x32_bf16 v[30:33], v[138:141], v[202:205], v[30:33]
	v_mfma_f32_16x16x32_bf16 v[22:25], v[130:133], v[210:213], v[22:25]
	v_mfma_f32_16x16x32_bf16 v[14:17], v[138:141], v[210:213], v[14:17]
	v_mfma_f32_16x16x32_bf16 v[62:65], v[134:137], v[190:193], v[62:65]
	v_mfma_f32_16x16x32_bf16 v[58:61], v[142:145], v[190:193], v[58:61]
	v_mfma_f32_16x16x32_bf16 v[54:57], v[134:137], v[198:201], v[54:57]
	v_mfma_f32_16x16x32_bf16 v[46:49], v[142:145], v[198:201], v[46:49]
	v_mfma_f32_16x16x32_bf16 v[38:41], v[134:137], v[206:209], v[38:41]
	v_mfma_f32_16x16x32_bf16 v[30:33], v[142:145], v[206:209], v[30:33]
	v_mfma_f32_16x16x32_bf16 v[22:25], v[134:137], v[214:217], v[22:25]
	v_mfma_f32_16x16x32_bf16 v[14:17], v[142:145], v[214:217], v[14:17]
	s_setprio 0
	s_setprio 1
	v_mfma_f32_16x16x32_bf16 v[50:53], v[162:165], v[186:189], v[50:53]
	v_mfma_f32_16x16x32_bf16 v[42:45], v[172:175], v[186:189], v[42:45]
	v_mfma_f32_16x16x32_bf16 v[34:37], v[162:165], v[194:197], v[34:37]
	v_mfma_f32_16x16x32_bf16 v[26:29], v[172:175], v[194:197], v[26:29]
	v_mfma_f32_16x16x32_bf16 v[18:21], v[162:165], v[202:205], v[18:21]
	v_mfma_f32_16x16x32_bf16 v[10:13], v[172:175], v[202:205], v[10:13]
	v_mfma_f32_16x16x32_bf16 v[6:9], v[162:165], v[210:213], v[6:9]
	v_mfma_f32_16x16x32_bf16 v[2:5], v[172:175], v[210:213], v[2:5]
	v_mfma_f32_16x16x32_bf16 v[50:53], v[166:169], v[190:193], v[50:53]
	v_mfma_f32_16x16x32_bf16 v[42:45], v[182:185], v[190:193], v[42:45]
	v_mfma_f32_16x16x32_bf16 v[34:37], v[166:169], v[198:201], v[34:37]
	v_mfma_f32_16x16x32_bf16 v[26:29], v[182:185], v[198:201], v[26:29]
	v_mfma_f32_16x16x32_bf16 v[18:21], v[166:169], v[206:209], v[18:21]
	v_mfma_f32_16x16x32_bf16 v[10:13], v[182:185], v[206:209], v[10:13]
	v_mfma_f32_16x16x32_bf16 v[6:9], v[166:169], v[214:217], v[6:9]
	v_mfma_f32_16x16x32_bf16 v[2:5], v[182:185], v[214:217], v[2:5]
	s_setprio 0
	s_barrier
	s_add_i32 s29, 0, 0x18000
	s_add_i32 s77, 0, 0x1c000
	v_add_u32_e32 v142, s29, v171
	v_add_u32_e32 v182, s77, v171
	ds_read_b128 v[130:133], v142
	ds_read_b128 v[134:137], v142 offset:1024
	ds_read_b128 v[138:141], v142 offset:2048
	ds_read_b128 v[142:145], v142 offset:3072
	ds_read_b128 v[162:165], v182
	ds_read_b128 v[166:169], v182 offset:1024
	ds_read_b128 v[172:175], v182 offset:2048
	ds_read_b128 v[182:185], v182 offset:3072
	s_add_u32 s46, s52, 0xc0000
	s_addc_u32 s47, s53, 0
	s_mov_b32 m0, s60
	v_lshl_add_u64 v[220:221], s[46:47], 0, v[146:147]
	ds_read_b128 v[186:189], v181 offset:32768
	ds_read_b128 v[190:193], v181 offset:33792
	ds_read_b128 v[194:197], v181 offset:34816
	ds_read_b128 v[198:201], v181 offset:35840
	ds_read_b128 v[202:205], v181 offset:36864
	ds_read_b128 v[206:209], v181 offset:37888
	ds_read_b128 v[210:213], v181 offset:38912
	ds_read_b128 v[214:217], v181 offset:39936
	global_load_lds_dwordx4 v[220:221], off
	v_lshl_add_u64 v[220:221], s[46:47], 0, v[150:151]
	s_mov_b32 m0, s61
	s_nop 0
	global_load_lds_dwordx4 v[220:221], off
	s_waitcnt vmcnt(8)
	s_waitcnt lgkmcnt(0)
	s_barrier
	s_setprio 1
	v_mfma_f32_16x16x32_bf16 v[126:129], v[130:133], v[186:189], v[126:129]
	v_mfma_f32_16x16x32_bf16 v[122:125], v[138:141], v[186:189], v[122:125]
	v_mfma_f32_16x16x32_bf16 v[118:121], v[130:133], v[194:197], v[118:121]
	v_mfma_f32_16x16x32_bf16 v[110:113], v[138:141], v[194:197], v[110:113]
	v_mfma_f32_16x16x32_bf16 v[102:105], v[130:133], v[202:205], v[102:105]
	v_mfma_f32_16x16x32_bf16 v[94:97], v[138:141], v[202:205], v[94:97]
	v_mfma_f32_16x16x32_bf16 v[86:89], v[130:133], v[210:213], v[86:89]
	v_mfma_f32_16x16x32_bf16 v[78:81], v[138:141], v[210:213], v[78:81]
	v_mfma_f32_16x16x32_bf16 v[126:129], v[134:137], v[190:193], v[126:129]
	v_mfma_f32_16x16x32_bf16 v[122:125], v[142:145], v[190:193], v[122:125]
	v_mfma_f32_16x16x32_bf16 v[118:121], v[134:137], v[198:201], v[118:121]
	v_mfma_f32_16x16x32_bf16 v[110:113], v[142:145], v[198:201], v[110:113]
	v_mfma_f32_16x16x32_bf16 v[102:105], v[134:137], v[206:209], v[102:105]
	v_mfma_f32_16x16x32_bf16 v[94:97], v[142:145], v[206:209], v[94:97]
	v_mfma_f32_16x16x32_bf16 v[86:89], v[134:137], v[214:217], v[86:89]
	v_mfma_f32_16x16x32_bf16 v[78:81], v[142:145], v[214:217], v[78:81]
	s_setprio 0
	s_setprio 1
	v_mfma_f32_16x16x32_bf16 v[114:117], v[162:165], v[186:189], v[114:117]
	v_mfma_f32_16x16x32_bf16 v[106:109], v[172:175], v[186:189], v[106:109]
	v_mfma_f32_16x16x32_bf16 v[98:101], v[162:165], v[194:197], v[98:101]
	v_mfma_f32_16x16x32_bf16 v[90:93], v[172:175], v[194:197], v[90:93]
	v_mfma_f32_16x16x32_bf16 v[82:85], v[162:165], v[202:205], v[82:85]
	v_mfma_f32_16x16x32_bf16 v[74:77], v[172:175], v[202:205], v[74:77]
	v_mfma_f32_16x16x32_bf16 v[70:73], v[162:165], v[210:213], v[70:73]
	v_mfma_f32_16x16x32_bf16 v[66:69], v[172:175], v[210:213], v[66:69]
	v_mfma_f32_16x16x32_bf16 v[114:117], v[166:169], v[190:193], v[114:117]
	v_mfma_f32_16x16x32_bf16 v[106:109], v[182:185], v[190:193], v[106:109]
	v_mfma_f32_16x16x32_bf16 v[98:101], v[166:169], v[198:201], v[98:101]
	v_mfma_f32_16x16x32_bf16 v[90:93], v[182:185], v[198:201], v[90:93]
	v_mfma_f32_16x16x32_bf16 v[82:85], v[166:169], v[206:209], v[82:85]
	v_mfma_f32_16x16x32_bf16 v[74:77], v[182:185], v[206:209], v[74:77]
	v_mfma_f32_16x16x32_bf16 v[70:73], v[166:169], v[214:217], v[70:73]
	v_mfma_f32_16x16x32_bf16 v[66:69], v[182:185], v[214:217], v[66:69]
	s_setprio 0
	s_barrier
	s_add_u32 s46, s50, 0x8000
	s_addc_u32 s47, s51, 0
	s_add_i32 s29, s29, s57
	v_lshl_add_u64 v[220:221], s[46:47], 0, v[148:149]
	s_mov_b32 m0, s29
	ds_read_b128 v[186:189], v181 offset:49152
	ds_read_b128 v[190:193], v181 offset:50176
	ds_read_b128 v[194:197], v181 offset:51200
	ds_read_b128 v[198:201], v181 offset:52224
	ds_read_b128 v[202:205], v181 offset:53248
	ds_read_b128 v[206:209], v181 offset:54272
	ds_read_b128 v[210:213], v181 offset:55296
	ds_read_b128 v[214:217], v181 offset:56320
	global_load_lds_dwordx4 v[220:221], off
	s_add_i32 m0, s29, 0x2000
	v_lshl_add_u64 v[220:221], s[46:47], 0, v[152:153]
	s_add_u32 s46, s50, 0xc000
	s_addc_u32 s47, s51, 0
	s_add_i32 s29, s77, s57
	global_load_lds_dwordx4 v[220:221], off
	v_lshl_add_u64 v[220:221], s[46:47], 0, v[148:149]
	s_mov_b32 m0, s29
	v_lshl_add_u64 v[176:177], v[176:177], 0, s[12:13]
	global_load_lds_dwordx4 v[220:221], off
	v_lshl_add_u64 v[220:221], s[46:47], 0, v[152:153]
	s_add_i32 m0, s29, 0x2000
	s_nop 0
	global_load_lds_dwordx4 v[220:221], off
	s_mov_b32 m0, s30
	s_nop 0
	global_load_lds_dwordx4 v[176:177], off
	v_lshl_add_u64 v[176:177], v[218:219], 0, s[12:13]
	s_mov_b32 m0, s31
	s_nop 0
	global_load_lds_dwordx4 v[176:177], off
	s_waitcnt vmcnt(8)
	s_waitcnt lgkmcnt(0)
	s_barrier
	s_setprio 1
	v_mfma_f32_16x16x32_bf16 v[62:65], v[130:133], v[186:189], v[62:65]
	v_mfma_f32_16x16x32_bf16 v[58:61], v[138:141], v[186:189], v[58:61]
	v_mfma_f32_16x16x32_bf16 v[54:57], v[130:133], v[194:197], v[54:57]
	v_mfma_f32_16x16x32_bf16 v[46:49], v[138:141], v[194:197], v[46:49]
	v_mfma_f32_16x16x32_bf16 v[38:41], v[130:133], v[202:205], v[38:41]
	v_mfma_f32_16x16x32_bf16 v[30:33], v[138:141], v[202:205], v[30:33]
	v_mfma_f32_16x16x32_bf16 v[22:25], v[130:133], v[210:213], v[22:25]
	v_mfma_f32_16x16x32_bf16 v[14:17], v[138:141], v[210:213], v[14:17]
	v_mfma_f32_16x16x32_bf16 v[62:65], v[134:137], v[190:193], v[62:65]
	v_mfma_f32_16x16x32_bf16 v[58:61], v[142:145], v[190:193], v[58:61]
	v_mfma_f32_16x16x32_bf16 v[54:57], v[134:137], v[198:201], v[54:57]
	v_mfma_f32_16x16x32_bf16 v[46:49], v[142:145], v[198:201], v[46:49]
	v_mfma_f32_16x16x32_bf16 v[38:41], v[134:137], v[206:209], v[38:41]
	v_mfma_f32_16x16x32_bf16 v[30:33], v[142:145], v[206:209], v[30:33]
	v_mfma_f32_16x16x32_bf16 v[22:25], v[134:137], v[214:217], v[22:25]
	v_mfma_f32_16x16x32_bf16 v[14:17], v[142:145], v[214:217], v[14:17]
	s_setprio 0
	s_setprio 1
	v_mfma_f32_16x16x32_bf16 v[50:53], v[162:165], v[186:189], v[50:53]
	v_mfma_f32_16x16x32_bf16 v[42:45], v[172:175], v[186:189], v[42:45]
	v_mfma_f32_16x16x32_bf16 v[34:37], v[162:165], v[194:197], v[34:37]
	v_mfma_f32_16x16x32_bf16 v[26:29], v[172:175], v[194:197], v[26:29]
	v_mfma_f32_16x16x32_bf16 v[18:21], v[162:165], v[202:205], v[18:21]
	v_mfma_f32_16x16x32_bf16 v[10:13], v[172:175], v[202:205], v[10:13]
	v_mfma_f32_16x16x32_bf16 v[6:9], v[162:165], v[210:213], v[6:9]
	v_mfma_f32_16x16x32_bf16 v[2:5], v[172:175], v[210:213], v[2:5]
	v_mfma_f32_16x16x32_bf16 v[50:53], v[166:169], v[190:193], v[50:53]
	v_mfma_f32_16x16x32_bf16 v[42:45], v[182:185], v[190:193], v[42:45]
	v_mfma_f32_16x16x32_bf16 v[34:37], v[166:169], v[198:201], v[34:37]
	v_mfma_f32_16x16x32_bf16 v[26:29], v[182:185], v[198:201], v[26:29]
	v_mfma_f32_16x16x32_bf16 v[18:21], v[166:169], v[206:209], v[18:21]
	v_mfma_f32_16x16x32_bf16 v[10:13], v[182:185], v[206:209], v[10:13]
	v_mfma_f32_16x16x32_bf16 v[6:9], v[166:169], v[214:217], v[6:9]
	v_mfma_f32_16x16x32_bf16 v[2:5], v[182:185], v[214:217], v[2:5]
	s_setprio 0
	s_barrier
	s_add_u32 s75, s75, 0x10000
	s_addc_u32 s28, s28, 0
	s_cmp_ge_u32 s76, s41
	s_mov_b64 s[46:47], s[48:49]
	s_mov_b32 s29, s76
	s_cbranch_scc0 .LBB0_1949
	s_and_b64 vcc, exec, s[14:15]
	s_cbranch_vccz .LBB0_1952
	s_barrier

.LBB0_2079:
	ds_read_b128 v[156:159], v152
	ds_read_b128 v[160:163], v152 offset:1024
	ds_read_b128 v[164:167], v152 offset:2048
	ds_read_b128 v[172:175], v152 offset:3072
	ds_read_b128 v[176:179], v153
	ds_read_b128 v[180:183], v153 offset:1024
	ds_read_b128 v[184:187], v153 offset:2048
	ds_read_b128 v[188:191], v153 offset:3072
	s_add_u32 s29, s42, 0xfffc0080
	s_addc_u32 s44, s43, -1
	s_cmp_eq_u32 s28, 12
	s_cselect_b32 s47, s17, s44
	s_cselect_b32 s46, s41, s29
	s_cselect_b32 s45, s15, s64
	s_cselect_b32 s44, s62, s63
	v_lshl_add_u64 v[150:151], s[42:43], 0, v[142:143]
	s_add_i32 m0, s23, 0xc000
	ds_read_b128 v[192:195], v154
	ds_read_b128 v[196:199], v154 offset:1024
	ds_read_b128 v[200:203], v154 offset:2048
	ds_read_b128 v[204:207], v154 offset:3072
	ds_read_b128 v[208:211], v154 offset:4096
	ds_read_b128 v[212:215], v154 offset:5120
	ds_read_b128 v[216:219], v154 offset:6144
	ds_read_b128 v[220:223], v154 offset:7168
	global_load_lds_dwordx4 v[150:151], off
	v_lshl_add_u64 v[150:151], s[42:43], 0, v[144:145]
	s_add_i32 m0, s23, 0xe000
	s_nop 0
	global_load_lds_dwordx4 v[150:151], off
	s_waitcnt vmcnt(8)
	s_waitcnt lgkmcnt(0)
	s_barrier
	s_setprio 1
	v_mfma_f32_16x16x32_bf16 v[126:129], v[156:159], v[192:195], v[126:129]
	v_mfma_f32_16x16x32_bf16 v[122:125], v[164:167], v[192:195], v[122:125]
	v_mfma_f32_16x16x32_bf16 v[118:121], v[156:159], v[200:203], v[118:121]
	v_mfma_f32_16x16x32_bf16 v[114:117], v[164:167], v[200:203], v[114:117]
	v_mfma_f32_16x16x32_bf16 v[94:97], v[156:159], v[208:211], v[94:97]
	v_mfma_f32_16x16x32_bf16 v[90:93], v[164:167], v[208:211], v[90:93]
	v_mfma_f32_16x16x32_bf16 v[86:89], v[156:159], v[216:219], v[86:89]
	v_mfma_f32_16x16x32_bf16 v[82:85], v[164:167], v[216:219], v[82:85]
	v_mfma_f32_16x16x32_bf16 v[126:129], v[160:163], v[196:199], v[126:129]
	v_mfma_f32_16x16x32_bf16 v[122:125], v[172:175], v[196:199], v[122:125]
	v_mfma_f32_16x16x32_bf16 v[118:121], v[160:163], v[204:207], v[118:121]
	v_mfma_f32_16x16x32_bf16 v[114:117], v[172:175], v[204:207], v[114:117]
	v_mfma_f32_16x16x32_bf16 v[94:97], v[160:163], v[212:215], v[94:97]
	v_mfma_f32_16x16x32_bf16 v[90:93], v[172:175], v[212:215], v[90:93]
	v_mfma_f32_16x16x32_bf16 v[86:89], v[160:163], v[220:223], v[86:89]
	v_mfma_f32_16x16x32_bf16 v[82:85], v[172:175], v[220:223], v[82:85]
	s_setprio 0
	s_setprio 1
	v_mfma_f32_16x16x32_bf16 v[110:113], v[176:179], v[192:195], v[110:113]
	v_mfma_f32_16x16x32_bf16 v[106:109], v[184:187], v[192:195], v[106:109]
	v_mfma_f32_16x16x32_bf16 v[102:105], v[176:179], v[200:203], v[102:105]
	v_mfma_f32_16x16x32_bf16 v[98:101], v[184:187], v[200:203], v[98:101]
	v_mfma_f32_16x16x32_bf16 v[78:81], v[176:179], v[208:211], v[78:81]
	v_mfma_f32_16x16x32_bf16 v[74:77], v[184:187], v[208:211], v[74:77]
	v_mfma_f32_16x16x32_bf16 v[70:73], v[176:179], v[216:219], v[70:73]
	v_mfma_f32_16x16x32_bf16 v[66:69], v[184:187], v[216:219], v[66:69]
	v_mfma_f32_16x16x32_bf16 v[110:113], v[180:183], v[196:199], v[110:113]
	v_mfma_f32_16x16x32_bf16 v[106:109], v[188:191], v[196:199], v[106:109]
	v_mfma_f32_16x16x32_bf16 v[102:105], v[180:183], v[204:207], v[102:105]
	v_mfma_f32_16x16x32_bf16 v[98:101], v[188:191], v[204:207], v[98:101]
	v_mfma_f32_16x16x32_bf16 v[78:81], v[180:183], v[212:215], v[78:81]
	v_mfma_f32_16x16x32_bf16 v[74:77], v[188:191], v[212:215], v[74:77]
	v_mfma_f32_16x16x32_bf16 v[70:73], v[180:183], v[220:223], v[70:73]
	v_mfma_f32_16x16x32_bf16 v[66:69], v[188:191], v[220:223], v[66:69]
	s_setprio 0
	s_barrier
	s_add_i32 s29, s55, s31
	v_lshl_add_u64 v[150:151], s[44:45], 0, v[134:135]
	s_mov_b32 m0, s29
	ds_read_b128 v[192:195], v154 offset:16384
	ds_read_b128 v[196:199], v154 offset:17408
	ds_read_b128 v[200:203], v154 offset:18432
	ds_read_b128 v[204:207], v154 offset:19456
	ds_read_b128 v[208:211], v154 offset:20480
	ds_read_b128 v[212:215], v154 offset:21504
	ds_read_b128 v[216:219], v154 offset:22528
	ds_read_b128 v[220:223], v154 offset:23552
	global_load_lds_dwordx4 v[150:151], off
	s_add_i32 m0, s29, 0x2000
	s_add_u32 s66, s44, 0x4000
	v_lshl_add_u64 v[150:151], s[44:45], 0, v[130:131]
	s_addc_u32 s67, s45, 0
	s_add_i32 s29, s56, s31
	global_load_lds_dwordx4 v[150:151], off
	v_lshl_add_u64 v[150:151], s[66:67], 0, v[134:135]
	s_mov_b32 m0, s29
	v_lshl_add_u64 v[168:169], s[46:47], 0, v[132:133]
	global_load_lds_dwordx4 v[150:151], off
	v_lshl_add_u64 v[150:151], s[66:67], 0, v[130:131]
	s_add_i32 m0, s29, 0x2000
	s_nop 0
	global_load_lds_dwordx4 v[150:151], off
	v_lshl_add_u64 v[150:151], s[46:47], 0, v[136:137]
	s_mov_b32 m0, s23
	s_nop 0
	global_load_lds_dwordx4 v[150:151], off
	s_mov_b32 m0, s33
	s_nop 0
	global_load_lds_dwordx4 v[168:169], off
	s_waitcnt vmcnt(8)
	s_waitcnt lgkmcnt(0)
	s_barrier
	s_setprio 1
	v_mfma_f32_16x16x32_bf16 v[62:65], v[156:159], v[192:195], v[62:65]
	v_mfma_f32_16x16x32_bf16 v[58:61], v[164:167], v[192:195], v[58:61]
	v_mfma_f32_16x16x32_bf16 v[54:57], v[156:159], v[200:203], v[54:57]
	v_mfma_f32_16x16x32_bf16 v[50:53], v[164:167], v[200:203], v[50:53]
	v_mfma_f32_16x16x32_bf16 v[30:33], v[156:159], v[208:211], v[30:33]
	v_mfma_f32_16x16x32_bf16 v[26:29], v[164:167], v[208:211], v[26:29]
	v_mfma_f32_16x16x32_bf16 v[22:25], v[156:159], v[216:219], v[22:25]
	v_mfma_f32_16x16x32_bf16 v[18:21], v[164:167], v[216:219], v[18:21]
	v_mfma_f32_16x16x32_bf16 v[62:65], v[160:163], v[196:199], v[62:65]
	v_mfma_f32_16x16x32_bf16 v[58:61], v[172:175], v[196:199], v[58:61]
	v_mfma_f32_16x16x32_bf16 v[54:57], v[160:163], v[204:207], v[54:57]
	v_mfma_f32_16x16x32_bf16 v[50:53], v[172:175], v[204:207], v[50:53]
	v_mfma_f32_16x16x32_bf16 v[30:33], v[160:163], v[212:215], v[30:33]
	v_mfma_f32_16x16x32_bf16 v[26:29], v[172:175], v[212:215], v[26:29]
	v_mfma_f32_16x16x32_bf16 v[22:25], v[160:163], v[220:223], v[22:25]
	v_mfma_f32_16x16x32_bf16 v[18:21], v[172:175], v[220:223], v[18:21]
	s_setprio 0
	s_setprio 1
	v_mfma_f32_16x16x32_bf16 v[46:49], v[176:179], v[192:195], v[46:49]
	v_mfma_f32_16x16x32_bf16 v[42:45], v[184:187], v[192:195], v[42:45]
	v_mfma_f32_16x16x32_bf16 v[38:41], v[176:179], v[200:203], v[38:41]
	v_mfma_f32_16x16x32_bf16 v[34:37], v[184:187], v[200:203], v[34:37]
	v_mfma_f32_16x16x32_bf16 v[14:17], v[176:179], v[208:211], v[14:17]
	v_mfma_f32_16x16x32_bf16 v[10:13], v[184:187], v[208:211], v[10:13]
	v_mfma_f32_16x16x32_bf16 v[6:9], v[176:179], v[216:219], v[6:9]
	v_mfma_f32_16x16x32_bf16 v[2:5], v[184:187], v[216:219], v[2:5]
	v_mfma_f32_16x16x32_bf16 v[46:49], v[180:183], v[196:199], v[46:49]
	v_mfma_f32_16x16x32_bf16 v[42:45], v[188:191], v[196:199], v[42:45]
	v_mfma_f32_16x16x32_bf16 v[38:41], v[180:183], v[204:207], v[38:41]
	v_mfma_f32_16x16x32_bf16 v[34:37], v[188:191], v[204:207], v[34:37]
	v_mfma_f32_16x16x32_bf16 v[14:17], v[180:183], v[212:215], v[14:17]
	v_mfma_f32_16x16x32_bf16 v[10:13], v[188:191], v[212:215], v[10:13]
	v_mfma_f32_16x16x32_bf16 v[6:9], v[180:183], v[220:223], v[6:9]
	v_mfma_f32_16x16x32_bf16 v[2:5], v[188:191], v[220:223], v[2:5]
	s_setprio 0
	s_barrier
	s_add_i32 s29, 0, 0x18000
	v_add_u32_e32 v155, s29, v1
	s_add_i32 s65, 0, 0x1c000
	ds_read_b128 v[156:159], v155
	ds_read_b128 v[160:163], v155 offset:1024
	ds_read_b128 v[164:167], v155 offset:2048
	ds_read_b128 v[172:175], v155 offset:3072
	v_add_u32_e32 v155, s65, v1
	ds_read_b128 v[176:179], v155
	ds_read_b128 v[180:183], v155 offset:1024
	ds_read_b128 v[184:187], v155 offset:2048
	ds_read_b128 v[188:191], v155 offset:3072
	s_add_u32 s46, s46, 0x40000
	s_addc_u32 s47, s47, 0
	s_mov_b32 m0, s48
	v_lshl_add_u64 v[224:225], s[46:47], 0, v[136:137]
	ds_read_b128 v[192:195], v154 offset:32768
	ds_read_b128 v[196:199], v154 offset:33792
	ds_read_b128 v[200:203], v154 offset:34816
	ds_read_b128 v[204:207], v154 offset:35840
	ds_read_b128 v[208:211], v154 offset:36864
	ds_read_b128 v[212:215], v154 offset:37888
	ds_read_b128 v[216:219], v154 offset:38912
	ds_read_b128 v[220:223], v154 offset:39936
	global_load_lds_dwordx4 v[224:225], off
	v_lshl_add_u64 v[224:225], s[46:47], 0, v[132:133]
	s_mov_b32 m0, s49
	s_nop 0
	global_load_lds_dwordx4 v[224:225], off
	s_waitcnt vmcnt(8)
	s_waitcnt lgkmcnt(0)
	s_barrier
	s_setprio 1
	v_mfma_f32_16x16x32_bf16 v[126:129], v[156:159], v[192:195], v[126:129]
	v_mfma_f32_16x16x32_bf16 v[122:125], v[164:167], v[192:195], v[122:125]
	v_mfma_f32_16x16x32_bf16 v[118:121], v[156:159], v[200:203], v[118:121]
	v_mfma_f32_16x16x32_bf16 v[114:117], v[164:167], v[200:203], v[114:117]
	v_mfma_f32_16x16x32_bf16 v[94:97], v[156:159], v[208:211], v[94:97]
	v_mfma_f32_16x16x32_bf16 v[90:93], v[164:167], v[208:211], v[90:93]
	v_mfma_f32_16x16x32_bf16 v[86:89], v[156:159], v[216:219], v[86:89]
	v_mfma_f32_16x16x32_bf16 v[82:85], v[164:167], v[216:219], v[82:85]
	v_mfma_f32_16x16x32_bf16 v[126:129], v[160:163], v[196:199], v[126:129]
	v_mfma_f32_16x16x32_bf16 v[122:125], v[172:175], v[196:199], v[122:125]
	v_mfma_f32_16x16x32_bf16 v[118:121], v[160:163], v[204:207], v[118:121]
	v_mfma_f32_16x16x32_bf16 v[114:117], v[172:175], v[204:207], v[114:117]
	v_mfma_f32_16x16x32_bf16 v[94:97], v[160:163], v[212:215], v[94:97]
	v_mfma_f32_16x16x32_bf16 v[90:93], v[172:175], v[212:215], v[90:93]
	v_mfma_f32_16x16x32_bf16 v[86:89], v[160:163], v[220:223], v[86:89]
	v_mfma_f32_16x16x32_bf16 v[82:85], v[172:175], v[220:223], v[82:85]
	s_setprio 0
	s_setprio 1
	v_mfma_f32_16x16x32_bf16 v[110:113], v[176:179], v[192:195], v[110:113]
	v_mfma_f32_16x16x32_bf16 v[106:109], v[184:187], v[192:195], v[106:109]
	v_mfma_f32_16x16x32_bf16 v[102:105], v[176:179], v[200:203], v[102:105]
	v_mfma_f32_16x16x32_bf16 v[98:101], v[184:187], v[200:203], v[98:101]
	v_mfma_f32_16x16x32_bf16 v[78:81], v[176:179], v[208:211], v[78:81]
	v_mfma_f32_16x16x32_bf16 v[74:77], v[184:187], v[208:211], v[74:77]
	v_mfma_f32_16x16x32_bf16 v[70:73], v[176:179], v[216:219], v[70:73]
	v_mfma_f32_16x16x32_bf16 v[66:69], v[184:187], v[216:219], v[66:69]
	v_mfma_f32_16x16x32_bf16 v[110:113], v[180:183], v[196:199], v[110:113]
	v_mfma_f32_16x16x32_bf16 v[106:109], v[188:191], v[196:199], v[106:109]
	v_mfma_f32_16x16x32_bf16 v[102:105], v[180:183], v[204:207], v[102:105]
	v_mfma_f32_16x16x32_bf16 v[98:101], v[188:191], v[204:207], v[98:101]
	v_mfma_f32_16x16x32_bf16 v[78:81], v[180:183], v[212:215], v[78:81]
	v_mfma_f32_16x16x32_bf16 v[74:77], v[188:191], v[212:215], v[74:77]
	v_mfma_f32_16x16x32_bf16 v[70:73], v[180:183], v[220:223], v[70:73]
	v_mfma_f32_16x16x32_bf16 v[66:69], v[188:191], v[220:223], v[66:69]
	s_setprio 0
	s_barrier
	s_add_u32 s46, s44, 0x8000
	s_addc_u32 s47, s45, 0
	s_add_i32 s29, s29, s31
	v_lshl_add_u64 v[224:225], s[46:47], 0, v[134:135]
	s_mov_b32 m0, s29
	ds_read_b128 v[192:195], v154 offset:49152
	ds_read_b128 v[196:199], v154 offset:50176
	ds_read_b128 v[200:203], v154 offset:51200
	ds_read_b128 v[204:207], v154 offset:52224
	ds_read_b128 v[208:211], v154 offset:53248
	ds_read_b128 v[212:215], v154 offset:54272
	ds_read_b128 v[216:219], v154 offset:55296
	ds_read_b128 v[220:223], v154 offset:56320
	global_load_lds_dwordx4 v[224:225], off
	s_add_i32 m0, s29, 0x2000
	s_add_u32 s44, s44, 0xc000
	v_lshl_add_u64 v[224:225], s[46:47], 0, v[130:131]
	s_addc_u32 s45, s45, 0
	s_add_i32 s29, s65, s31
	global_load_lds_dwordx4 v[224:225], off
	v_lshl_add_u64 v[224:225], s[44:45], 0, v[134:135]
	s_mov_b32 m0, s29
	v_lshl_add_u64 v[150:151], v[150:151], 0, s[10:11]
	global_load_lds_dwordx4 v[224:225], off
	v_lshl_add_u64 v[224:225], s[44:45], 0, v[130:131]
	s_add_i32 m0, s29, 0x2000
	s_nop 0
	global_load_lds_dwordx4 v[224:225], off
	s_mov_b32 m0, s53
	s_nop 0
	global_load_lds_dwordx4 v[150:151], off
	v_lshl_add_u64 v[150:151], v[168:169], 0, s[10:11]
	s_mov_b32 m0, s54
	s_nop 0
	global_load_lds_dwordx4 v[150:151], off
	s_waitcnt vmcnt(8)
	s_waitcnt lgkmcnt(0)
	s_barrier
	s_setprio 1
	v_mfma_f32_16x16x32_bf16 v[62:65], v[156:159], v[192:195], v[62:65]
	v_mfma_f32_16x16x32_bf16 v[58:61], v[164:167], v[192:195], v[58:61]
	v_mfma_f32_16x16x32_bf16 v[54:57], v[156:159], v[200:203], v[54:57]
	v_mfma_f32_16x16x32_bf16 v[50:53], v[164:167], v[200:203], v[50:53]
	v_mfma_f32_16x16x32_bf16 v[30:33], v[156:159], v[208:211], v[30:33]
	v_mfma_f32_16x16x32_bf16 v[26:29], v[164:167], v[208:211], v[26:29]
	v_mfma_f32_16x16x32_bf16 v[22:25], v[156:159], v[216:219], v[22:25]
	v_mfma_f32_16x16x32_bf16 v[18:21], v[164:167], v[216:219], v[18:21]
	v_mfma_f32_16x16x32_bf16 v[62:65], v[160:163], v[196:199], v[62:65]
	v_mfma_f32_16x16x32_bf16 v[58:61], v[172:175], v[196:199], v[58:61]
	v_mfma_f32_16x16x32_bf16 v[54:57], v[160:163], v[204:207], v[54:57]
	v_mfma_f32_16x16x32_bf16 v[50:53], v[172:175], v[204:207], v[50:53]
	v_mfma_f32_16x16x32_bf16 v[30:33], v[160:163], v[212:215], v[30:33]
	v_mfma_f32_16x16x32_bf16 v[26:29], v[172:175], v[212:215], v[26:29]
	v_mfma_f32_16x16x32_bf16 v[22:25], v[160:163], v[220:223], v[22:25]
	v_mfma_f32_16x16x32_bf16 v[18:21], v[172:175], v[220:223], v[18:21]
	s_setprio 0
	s_setprio 1
	v_mfma_f32_16x16x32_bf16 v[46:49], v[176:179], v[192:195], v[46:49]
	v_mfma_f32_16x16x32_bf16 v[42:45], v[184:187], v[192:195], v[42:45]
	v_mfma_f32_16x16x32_bf16 v[38:41], v[176:179], v[200:203], v[38:41]
	v_mfma_f32_16x16x32_bf16 v[34:37], v[184:187], v[200:203], v[34:37]
	v_mfma_f32_16x16x32_bf16 v[14:17], v[176:179], v[208:211], v[14:17]
	v_mfma_f32_16x16x32_bf16 v[10:13], v[184:187], v[208:211], v[10:13]
	v_mfma_f32_16x16x32_bf16 v[6:9], v[176:179], v[216:219], v[6:9]
	v_mfma_f32_16x16x32_bf16 v[2:5], v[184:187], v[216:219], v[2:5]
	v_mfma_f32_16x16x32_bf16 v[46:49], v[180:183], v[196:199], v[46:49]
	v_mfma_f32_16x16x32_bf16 v[42:45], v[188:191], v[196:199], v[42:45]
	v_mfma_f32_16x16x32_bf16 v[38:41], v[180:183], v[204:207], v[38:41]
	v_mfma_f32_16x16x32_bf16 v[34:37], v[188:191], v[204:207], v[34:37]
	v_mfma_f32_16x16x32_bf16 v[14:17], v[180:183], v[212:215], v[14:17]
	v_mfma_f32_16x16x32_bf16 v[10:13], v[188:191], v[212:215], v[10:13]
	v_mfma_f32_16x16x32_bf16 v[6:9], v[180:183], v[220:223], v[6:9]
	v_mfma_f32_16x16x32_bf16 v[2:5], v[188:191], v[220:223], v[2:5]
	s_setprio 0
	s_barrier
	s_add_i32 s28, s28, 2
	s_add_u32 s63, s63, 0x10000
	s_addc_u32 s64, s64, 0
	s_add_u32 s42, s42, 0x100
	s_addc_u32 s43, s43, 0
	s_cmp_gt_u32 s28, 13
	s_cbranch_scc0 .LBB0_2079
	s_and_b64 vcc, exec, s[12:13]
	s_cbranch_vccz .LBB0_2082
	s_barrier

.LBB0_2164:
	ds_read_b128 v[130:133], v179
	ds_read_b128 v[134:137], v179 offset:1024
	ds_read_b128 v[138:141], v179 offset:2048
	ds_read_b128 v[142:145], v179 offset:3072
	ds_read_b128 v[162:165], v180
	ds_read_b128 v[166:169], v180 offset:1024
	ds_read_b128 v[172:175], v180 offset:2048
	ds_read_b128 v[182:185], v180 offset:3072
	s_add_i32 s29, s28, 2
	s_add_u32 s46, s44, 0x4000
	s_addc_u32 s47, s45, 0
	s_cmp_eq_u32 s73, s28
	s_cselect_b32 s50, s40, s46
	s_cselect_b32 s51, s41, s47
	s_cselect_b32 s48, s42, s75
	s_cselect_b32 s49, s43, s76
	s_add_u32 s46, s50, 0x8000
	s_addc_u32 s47, s51, 0
	v_lshl_add_u64 v[176:177], s[44:45], 0, v[154:155]
	s_add_i32 m0, s56, 0xc000
	ds_read_b128 v[186:189], v181
	ds_read_b128 v[190:193], v181 offset:1024
	ds_read_b128 v[194:197], v181 offset:2048
	ds_read_b128 v[198:201], v181 offset:3072
	ds_read_b128 v[202:205], v181 offset:4096
	ds_read_b128 v[206:209], v181 offset:5120
	ds_read_b128 v[210:213], v181 offset:6144
	ds_read_b128 v[214:217], v181 offset:7168
	global_load_lds_dwordx4 v[176:177], off
	v_lshl_add_u64 v[176:177], s[44:45], 0, v[156:157]
	s_add_i32 m0, s56, 0xe000
	s_nop 0
	global_load_lds_dwordx4 v[176:177], off
	s_waitcnt vmcnt(8)
	s_waitcnt lgkmcnt(0)
	s_barrier
	s_setprio 1
	v_mfma_f32_16x16x32_bf16 v[126:129], v[130:133], v[186:189], v[126:129]
	v_mfma_f32_16x16x32_bf16 v[122:125], v[138:141], v[186:189], v[122:125]
	v_mfma_f32_16x16x32_bf16 v[118:121], v[130:133], v[194:197], v[118:121]
	v_mfma_f32_16x16x32_bf16 v[110:113], v[138:141], v[194:197], v[110:113]
	v_mfma_f32_16x16x32_bf16 v[102:105], v[130:133], v[202:205], v[102:105]
	v_mfma_f32_16x16x32_bf16 v[94:97], v[138:141], v[202:205], v[94:97]
	v_mfma_f32_16x16x32_bf16 v[86:89], v[130:133], v[210:213], v[86:89]
	v_mfma_f32_16x16x32_bf16 v[78:81], v[138:141], v[210:213], v[78:81]
	v_mfma_f32_16x16x32_bf16 v[126:129], v[134:137], v[190:193], v[126:129]
	v_mfma_f32_16x16x32_bf16 v[122:125], v[142:145], v[190:193], v[122:125]
	v_mfma_f32_16x16x32_bf16 v[118:121], v[134:137], v[198:201], v[118:121]
	v_mfma_f32_16x16x32_bf16 v[110:113], v[142:145], v[198:201], v[110:113]
	v_mfma_f32_16x16x32_bf16 v[102:105], v[134:137], v[206:209], v[102:105]
	v_mfma_f32_16x16x32_bf16 v[94:97], v[142:145], v[206:209], v[94:97]
	v_mfma_f32_16x16x32_bf16 v[86:89], v[134:137], v[214:217], v[86:89]
	v_mfma_f32_16x16x32_bf16 v[78:81], v[142:145], v[214:217], v[78:81]
	s_setprio 0
	s_setprio 1
	v_mfma_f32_16x16x32_bf16 v[114:117], v[162:165], v[186:189], v[114:117]
	v_mfma_f32_16x16x32_bf16 v[106:109], v[172:175], v[186:189], v[106:109]
	v_mfma_f32_16x16x32_bf16 v[98:101], v[162:165], v[194:197], v[98:101]
	v_mfma_f32_16x16x32_bf16 v[90:93], v[172:175], v[194:197], v[90:93]
	v_mfma_f32_16x16x32_bf16 v[82:85], v[162:165], v[202:205], v[82:85]
	v_mfma_f32_16x16x32_bf16 v[74:77], v[172:175], v[202:205], v[74:77]
	v_mfma_f32_16x16x32_bf16 v[70:73], v[162:165], v[210:213], v[70:73]
	v_mfma_f32_16x16x32_bf16 v[66:69], v[172:175], v[210:213], v[66:69]
	v_mfma_f32_16x16x32_bf16 v[114:117], v[166:169], v[190:193], v[114:117]
	v_mfma_f32_16x16x32_bf16 v[106:109], v[182:185], v[190:193], v[106:109]
	v_mfma_f32_16x16x32_bf16 v[98:101], v[166:169], v[198:201], v[98:101]
	v_mfma_f32_16x16x32_bf16 v[90:93], v[182:185], v[198:201], v[90:93]
	v_mfma_f32_16x16x32_bf16 v[82:85], v[166:169], v[206:209], v[82:85]
	v_mfma_f32_16x16x32_bf16 v[74:77], v[182:185], v[206:209], v[74:77]
	v_mfma_f32_16x16x32_bf16 v[70:73], v[166:169], v[214:217], v[70:73]
	v_mfma_f32_16x16x32_bf16 v[66:69], v[182:185], v[214:217], v[66:69]
	s_setprio 0
	s_barrier
	s_add_i32 s28, s64, s55
	v_lshl_add_u64 v[176:177], s[48:49], 0, v[148:149]
	s_mov_b32 m0, s28
	ds_read_b128 v[186:189], v181 offset:16384
	ds_read_b128 v[190:193], v181 offset:17408
	ds_read_b128 v[194:197], v181 offset:18432
	ds_read_b128 v[198:201], v181 offset:19456
	ds_read_b128 v[202:205], v181 offset:20480
	ds_read_b128 v[206:209], v181 offset:21504
	ds_read_b128 v[210:213], v181 offset:22528
	ds_read_b128 v[214:217], v181 offset:23552
	global_load_lds_dwordx4 v[176:177], off
	s_add_i32 m0, s28, 0x2000
	s_add_u32 s82, s48, 0x4000
	v_lshl_add_u64 v[176:177], s[48:49], 0, v[152:153]
	s_addc_u32 s83, s49, 0
	s_add_i32 s28, s65, s55
	global_load_lds_dwordx4 v[176:177], off
	v_lshl_add_u64 v[176:177], s[82:83], 0, v[148:149]
	s_mov_b32 m0, s28
	s_nop 0
	global_load_lds_dwordx4 v[176:177], off
	v_lshl_add_u64 v[176:177], s[82:83], 0, v[152:153]
	s_add_i32 m0, s28, 0x2000
	s_nop 0
	global_load_lds_dwordx4 v[176:177], off
	v_lshl_add_u64 v[176:177], s[50:51], 0, v[146:147]
	s_mov_b32 m0, s56
	s_nop 0
	global_load_lds_dwordx4 v[176:177], off
	v_lshl_add_u64 v[176:177], s[50:51], 0, v[150:151]
	s_mov_b32 m0, s57
	s_nop 0
	global_load_lds_dwordx4 v[176:177], off
	s_waitcnt vmcnt(8)
	s_waitcnt lgkmcnt(0)
	s_barrier
	s_setprio 1
	v_mfma_f32_16x16x32_bf16 v[62:65], v[130:133], v[186:189], v[62:65]
	v_mfma_f32_16x16x32_bf16 v[58:61], v[138:141], v[186:189], v[58:61]
	v_mfma_f32_16x16x32_bf16 v[54:57], v[130:133], v[194:197], v[54:57]
	v_mfma_f32_16x16x32_bf16 v[46:49], v[138:141], v[194:197], v[46:49]
	v_mfma_f32_16x16x32_bf16 v[38:41], v[130:133], v[202:205], v[38:41]
	v_mfma_f32_16x16x32_bf16 v[30:33], v[138:141], v[202:205], v[30:33]
	v_mfma_f32_16x16x32_bf16 v[22:25], v[130:133], v[210:213], v[22:25]
	v_mfma_f32_16x16x32_bf16 v[14:17], v[138:141], v[210:213], v[14:17]
	v_mfma_f32_16x16x32_bf16 v[62:65], v[134:137], v[190:193], v[62:65]
	v_mfma_f32_16x16x32_bf16 v[58:61], v[142:145], v[190:193], v[58:61]
	v_mfma_f32_16x16x32_bf16 v[54:57], v[134:137], v[198:201], v[54:57]
	v_mfma_f32_16x16x32_bf16 v[46:49], v[142:145], v[198:201], v[46:49]
	v_mfma_f32_16x16x32_bf16 v[38:41], v[134:137], v[206:209], v[38:41]
	v_mfma_f32_16x16x32_bf16 v[30:33], v[142:145], v[206:209], v[30:33]
	v_mfma_f32_16x16x32_bf16 v[22:25], v[134:137], v[214:217], v[22:25]
	v_mfma_f32_16x16x32_bf16 v[14:17], v[142:145], v[214:217], v[14:17]
	s_setprio 0
	s_setprio 1
	v_mfma_f32_16x16x32_bf16 v[50:53], v[162:165], v[186:189], v[50:53]
	v_mfma_f32_16x16x32_bf16 v[42:45], v[172:175], v[186:189], v[42:45]
	v_mfma_f32_16x16x32_bf16 v[34:37], v[162:165], v[194:197], v[34:37]
	v_mfma_f32_16x16x32_bf16 v[26:29], v[172:175], v[194:197], v[26:29]
	v_mfma_f32_16x16x32_bf16 v[18:21], v[162:165], v[202:205], v[18:21]
	v_mfma_f32_16x16x32_bf16 v[10:13], v[172:175], v[202:205], v[10:13]
	v_mfma_f32_16x16x32_bf16 v[6:9], v[162:165], v[210:213], v[6:9]
	v_mfma_f32_16x16x32_bf16 v[2:5], v[172:175], v[210:213], v[2:5]
	v_mfma_f32_16x16x32_bf16 v[50:53], v[166:169], v[190:193], v[50:53]
	v_mfma_f32_16x16x32_bf16 v[42:45], v[182:185], v[190:193], v[42:45]
	v_mfma_f32_16x16x32_bf16 v[34:37], v[166:169], v[198:201], v[34:37]
	v_mfma_f32_16x16x32_bf16 v[26:29], v[182:185], v[198:201], v[26:29]
	v_mfma_f32_16x16x32_bf16 v[18:21], v[166:169], v[206:209], v[18:21]
	v_mfma_f32_16x16x32_bf16 v[10:13], v[182:185], v[206:209], v[10:13]
	v_mfma_f32_16x16x32_bf16 v[6:9], v[166:169], v[214:217], v[6:9]
	v_mfma_f32_16x16x32_bf16 v[2:5], v[182:185], v[214:217], v[2:5]
	s_setprio 0
	s_barrier
	s_add_i32 s28, 0, 0x18000
	s_add_i32 s77, 0, 0x1c000
	v_add_u32_e32 v142, s28, v171
	v_add_u32_e32 v176, s77, v171
	ds_read_b128 v[130:133], v142
	ds_read_b128 v[134:137], v142 offset:1024
	ds_read_b128 v[138:141], v142 offset:2048
	ds_read_b128 v[142:145], v142 offset:3072
	ds_read_b128 v[162:165], v176
	ds_read_b128 v[166:169], v176 offset:1024
	ds_read_b128 v[172:175], v176 offset:2048
	ds_read_b128 v[182:185], v176 offset:3072
	s_add_u32 s50, s50, 0x4000
	s_addc_u32 s51, s51, 0
	s_mov_b32 m0, s58
	v_lshl_add_u64 v[176:177], s[50:51], 0, v[146:147]
	ds_read_b128 v[186:189], v181 offset:32768
	ds_read_b128 v[190:193], v181 offset:33792
	ds_read_b128 v[194:197], v181 offset:34816
	ds_read_b128 v[198:201], v181 offset:35840
	ds_read_b128 v[202:205], v181 offset:36864
	ds_read_b128 v[206:209], v181 offset:37888
	ds_read_b128 v[210:213], v181 offset:38912
	ds_read_b128 v[214:217], v181 offset:39936
	global_load_lds_dwordx4 v[176:177], off
	v_lshl_add_u64 v[176:177], s[50:51], 0, v[150:151]
	s_mov_b32 m0, s59
	s_nop 0
	global_load_lds_dwordx4 v[176:177], off
	s_waitcnt vmcnt(8)
	s_waitcnt lgkmcnt(0)
	s_barrier
	s_setprio 1
	v_mfma_f32_16x16x32_bf16 v[126:129], v[130:133], v[186:189], v[126:129]
	v_mfma_f32_16x16x32_bf16 v[122:125], v[138:141], v[186:189], v[122:125]
	v_mfma_f32_16x16x32_bf16 v[118:121], v[130:133], v[194:197], v[118:121]
	v_mfma_f32_16x16x32_bf16 v[110:113], v[138:141], v[194:197], v[110:113]
	v_mfma_f32_16x16x32_bf16 v[102:105], v[130:133], v[202:205], v[102:105]
	v_mfma_f32_16x16x32_bf16 v[94:97], v[138:141], v[202:205], v[94:97]
	v_mfma_f32_16x16x32_bf16 v[86:89], v[130:133], v[210:213], v[86:89]
	v_mfma_f32_16x16x32_bf16 v[78:81], v[138:141], v[210:213], v[78:81]
	v_mfma_f32_16x16x32_bf16 v[126:129], v[134:137], v[190:193], v[126:129]
	v_mfma_f32_16x16x32_bf16 v[122:125], v[142:145], v[190:193], v[122:125]
	v_mfma_f32_16x16x32_bf16 v[118:121], v[134:137], v[198:201], v[118:121]
	v_mfma_f32_16x16x32_bf16 v[110:113], v[142:145], v[198:201], v[110:113]
	v_mfma_f32_16x16x32_bf16 v[102:105], v[134:137], v[206:209], v[102:105]
	v_mfma_f32_16x16x32_bf16 v[94:97], v[142:145], v[206:209], v[94:97]
	v_mfma_f32_16x16x32_bf16 v[86:89], v[134:137], v[214:217], v[86:89]
	v_mfma_f32_16x16x32_bf16 v[78:81], v[142:145], v[214:217], v[78:81]
	s_setprio 0
	s_setprio 1
	v_mfma_f32_16x16x32_bf16 v[114:117], v[162:165], v[186:189], v[114:117]
	v_mfma_f32_16x16x32_bf16 v[106:109], v[172:175], v[186:189], v[106:109]
	v_mfma_f32_16x16x32_bf16 v[98:101], v[162:165], v[194:197], v[98:101]
	v_mfma_f32_16x16x32_bf16 v[90:93], v[172:175], v[194:197], v[90:93]
	v_mfma_f32_16x16x32_bf16 v[82:85], v[162:165], v[202:205], v[82:85]
	v_mfma_f32_16x16x32_bf16 v[74:77], v[172:175], v[202:205], v[74:77]
	v_mfma_f32_16x16x32_bf16 v[70:73], v[162:165], v[210:213], v[70:73]
	v_mfma_f32_16x16x32_bf16 v[66:69], v[172:175], v[210:213], v[66:69]
	v_mfma_f32_16x16x32_bf16 v[114:117], v[166:169], v[190:193], v[114:117]
	v_mfma_f32_16x16x32_bf16 v[106:109], v[182:185], v[190:193], v[106:109]
	v_mfma_f32_16x16x32_bf16 v[98:101], v[166:169], v[198:201], v[98:101]
	v_mfma_f32_16x16x32_bf16 v[90:93], v[182:185], v[198:201], v[90:93]
	v_mfma_f32_16x16x32_bf16 v[82:85], v[166:169], v[206:209], v[82:85]
	v_mfma_f32_16x16x32_bf16 v[74:77], v[182:185], v[206:209], v[74:77]
	v_mfma_f32_16x16x32_bf16 v[70:73], v[166:169], v[214:217], v[70:73]
	v_mfma_f32_16x16x32_bf16 v[66:69], v[182:185], v[214:217], v[66:69]
	s_setprio 0
	s_barrier
	s_add_u32 s50, s48, 0x8000
	s_addc_u32 s51, s49, 0
	s_add_i32 s28, s28, s55
	v_lshl_add_u64 v[176:177], s[50:51], 0, v[148:149]
	s_mov_b32 m0, s28
	ds_read_b128 v[186:189], v181 offset:49152
	ds_read_b128 v[190:193], v181 offset:50176
	ds_read_b128 v[194:197], v181 offset:51200
	ds_read_b128 v[198:201], v181 offset:52224
	ds_read_b128 v[202:205], v181 offset:53248
	ds_read_b128 v[206:209], v181 offset:54272
	ds_read_b128 v[210:213], v181 offset:55296
	ds_read_b128 v[214:217], v181 offset:56320
	global_load_lds_dwordx4 v[176:177], off
	s_add_i32 m0, s28, 0x2000
	s_add_u32 s48, s48, 0xc000
	v_lshl_add_u64 v[176:177], s[50:51], 0, v[152:153]
	s_addc_u32 s49, s49, 0
	s_add_i32 s28, s77, s55
	global_load_lds_dwordx4 v[176:177], off
	v_lshl_add_u64 v[176:177], s[48:49], 0, v[148:149]
	s_mov_b32 m0, s28
	s_nop 0
	global_load_lds_dwordx4 v[176:177], off
	v_lshl_add_u64 v[176:177], s[48:49], 0, v[152:153]
	s_add_i32 m0, s28, 0x2000
	s_nop 0
	global_load_lds_dwordx4 v[176:177], off
	v_lshl_add_u64 v[176:177], s[46:47], 0, v[146:147]
	s_mov_b32 m0, s30
	s_nop 0
	global_load_lds_dwordx4 v[176:177], off
	v_lshl_add_u64 v[176:177], s[46:47], 0, v[150:151]
	s_mov_b32 m0, s31
	s_nop 0
	global_load_lds_dwordx4 v[176:177], off
	s_waitcnt vmcnt(8)
	s_waitcnt lgkmcnt(0)
	s_barrier
	s_setprio 1
	v_mfma_f32_16x16x32_bf16 v[62:65], v[130:133], v[186:189], v[62:65]
	v_mfma_f32_16x16x32_bf16 v[58:61], v[138:141], v[186:189], v[58:61]
	v_mfma_f32_16x16x32_bf16 v[54:57], v[130:133], v[194:197], v[54:57]
	v_mfma_f32_16x16x32_bf16 v[46:49], v[138:141], v[194:197], v[46:49]
	v_mfma_f32_16x16x32_bf16 v[38:41], v[130:133], v[202:205], v[38:41]
	v_mfma_f32_16x16x32_bf16 v[30:33], v[138:141], v[202:205], v[30:33]
	v_mfma_f32_16x16x32_bf16 v[22:25], v[130:133], v[210:213], v[22:25]
	v_mfma_f32_16x16x32_bf16 v[14:17], v[138:141], v[210:213], v[14:17]
	v_mfma_f32_16x16x32_bf16 v[62:65], v[134:137], v[190:193], v[62:65]
	v_mfma_f32_16x16x32_bf16 v[58:61], v[142:145], v[190:193], v[58:61]
	v_mfma_f32_16x16x32_bf16 v[54:57], v[134:137], v[198:201], v[54:57]
	v_mfma_f32_16x16x32_bf16 v[46:49], v[142:145], v[198:201], v[46:49]
	v_mfma_f32_16x16x32_bf16 v[38:41], v[134:137], v[206:209], v[38:41]
	v_mfma_f32_16x16x32_bf16 v[30:33], v[142:145], v[206:209], v[30:33]
	v_mfma_f32_16x16x32_bf16 v[22:25], v[134:137], v[214:217], v[22:25]
	v_mfma_f32_16x16x32_bf16 v[14:17], v[142:145], v[214:217], v[14:17]
	s_setprio 0
	s_setprio 1
	v_mfma_f32_16x16x32_bf16 v[50:53], v[162:165], v[186:189], v[50:53]
	v_mfma_f32_16x16x32_bf16 v[42:45], v[172:175], v[186:189], v[42:45]
	v_mfma_f32_16x16x32_bf16 v[34:37], v[162:165], v[194:197], v[34:37]
	v_mfma_f32_16x16x32_bf16 v[26:29], v[172:175], v[194:197], v[26:29]
	v_mfma_f32_16x16x32_bf16 v[18:21], v[162:165], v[202:205], v[18:21]
	v_mfma_f32_16x16x32_bf16 v[10:13], v[172:175], v[202:205], v[10:13]
	v_mfma_f32_16x16x32_bf16 v[6:9], v[162:165], v[210:213], v[6:9]
	v_mfma_f32_16x16x32_bf16 v[2:5], v[172:175], v[210:213], v[2:5]
	v_mfma_f32_16x16x32_bf16 v[50:53], v[166:169], v[190:193], v[50:53]
	v_mfma_f32_16x16x32_bf16 v[42:45], v[182:185], v[190:193], v[42:45]
	v_mfma_f32_16x16x32_bf16 v[34:37], v[166:169], v[198:201], v[34:37]
	v_mfma_f32_16x16x32_bf16 v[26:29], v[182:185], v[198:201], v[26:29]
	v_mfma_f32_16x16x32_bf16 v[18:21], v[166:169], v[206:209], v[18:21]
	v_mfma_f32_16x16x32_bf16 v[10:13], v[182:185], v[206:209], v[10:13]
	v_mfma_f32_16x16x32_bf16 v[6:9], v[166:169], v[214:217], v[6:9]
	v_mfma_f32_16x16x32_bf16 v[2:5], v[182:185], v[214:217], v[2:5]
	s_setprio 0
	s_barrier
	s_add_u32 s44, s44, 0x10000
	s_addc_u32 s45, s45, 0
	s_add_u32 s75, s75, 0x10000
	s_addc_u32 s76, s76, 0
	s_cmp_ge_u32 s29, s23
	s_mov_b32 s28, s29
	s_cbranch_scc0 .LBB0_2164
	s_and_b64 vcc, exec, s[12:13]
	s_cbranch_vccz .LBB0_2167
	s_barrier

.LBB0_2294:
	ds_read_b128 v[154:157], v151
	ds_read_b128 v[158:161], v151 offset:1024
	ds_read_b128 v[162:165], v151 offset:2048
	ds_read_b128 v[166:169], v151 offset:3072
	ds_read_b128 v[172:175], v152
	ds_read_b128 v[176:179], v152 offset:1024
	ds_read_b128 v[180:183], v152 offset:2048
	ds_read_b128 v[184:187], v152 offset:3072
	s_add_u32 s29, s22, 0xfffc0080
	s_addc_u32 s40, s23, -1
	s_cmp_eq_u32 s28, 12
	s_cselect_b32 s43, s15, s40
	s_cselect_b32 s42, s57, s29
	s_cselect_b32 s41, s13, s60
	s_cselect_b32 s40, s58, s59
	v_lshl_add_u64 v[148:149], s[22:23], 0, v[140:141]
	s_add_i32 m0, s21, 0xc000
	ds_read_b128 v[188:191], v153
	ds_read_b128 v[192:195], v153 offset:1024
	ds_read_b128 v[196:199], v153 offset:2048
	ds_read_b128 v[200:203], v153 offset:3072
	ds_read_b128 v[204:207], v153 offset:4096
	ds_read_b128 v[208:211], v153 offset:5120
	ds_read_b128 v[212:215], v153 offset:6144
	ds_read_b128 v[216:219], v153 offset:7168
	global_load_lds_dwordx4 v[148:149], off
	v_lshl_add_u64 v[148:149], s[22:23], 0, v[142:143]
	s_add_i32 m0, s21, 0xe000
	s_nop 0
	global_load_lds_dwordx4 v[148:149], off
	s_waitcnt vmcnt(8)
	s_waitcnt lgkmcnt(0)
	s_barrier
	s_setprio 1
	v_mfma_f32_16x16x32_bf16 v[126:129], v[154:157], v[188:191], v[126:129]
	v_mfma_f32_16x16x32_bf16 v[122:125], v[162:165], v[188:191], v[122:125]
	v_mfma_f32_16x16x32_bf16 v[118:121], v[154:157], v[196:199], v[118:121]
	v_mfma_f32_16x16x32_bf16 v[110:113], v[162:165], v[196:199], v[110:113]
	v_mfma_f32_16x16x32_bf16 v[102:105], v[154:157], v[204:207], v[102:105]
	v_mfma_f32_16x16x32_bf16 v[94:97], v[162:165], v[204:207], v[94:97]
	v_mfma_f32_16x16x32_bf16 v[86:89], v[154:157], v[212:215], v[86:89]
	v_mfma_f32_16x16x32_bf16 v[78:81], v[162:165], v[212:215], v[78:81]
	v_mfma_f32_16x16x32_bf16 v[126:129], v[158:161], v[192:195], v[126:129]
	v_mfma_f32_16x16x32_bf16 v[122:125], v[166:169], v[192:195], v[122:125]
	v_mfma_f32_16x16x32_bf16 v[118:121], v[158:161], v[200:203], v[118:121]
	v_mfma_f32_16x16x32_bf16 v[110:113], v[166:169], v[200:203], v[110:113]
	v_mfma_f32_16x16x32_bf16 v[102:105], v[158:161], v[208:211], v[102:105]
	v_mfma_f32_16x16x32_bf16 v[94:97], v[166:169], v[208:211], v[94:97]
	v_mfma_f32_16x16x32_bf16 v[86:89], v[158:161], v[216:219], v[86:89]
	v_mfma_f32_16x16x32_bf16 v[78:81], v[166:169], v[216:219], v[78:81]
	s_setprio 0
	s_setprio 1
	v_mfma_f32_16x16x32_bf16 v[114:117], v[172:175], v[188:191], v[114:117]
	v_mfma_f32_16x16x32_bf16 v[106:109], v[180:183], v[188:191], v[106:109]
	v_mfma_f32_16x16x32_bf16 v[98:101], v[172:175], v[196:199], v[98:101]
	v_mfma_f32_16x16x32_bf16 v[90:93], v[180:183], v[196:199], v[90:93]
	v_mfma_f32_16x16x32_bf16 v[82:85], v[172:175], v[204:207], v[82:85]
	v_mfma_f32_16x16x32_bf16 v[74:77], v[180:183], v[204:207], v[74:77]
	v_mfma_f32_16x16x32_bf16 v[70:73], v[172:175], v[212:215], v[70:73]
	v_mfma_f32_16x16x32_bf16 v[66:69], v[180:183], v[212:215], v[66:69]
	v_mfma_f32_16x16x32_bf16 v[114:117], v[176:179], v[192:195], v[114:117]
	v_mfma_f32_16x16x32_bf16 v[106:109], v[184:187], v[192:195], v[106:109]
	v_mfma_f32_16x16x32_bf16 v[98:101], v[176:179], v[200:203], v[98:101]
	v_mfma_f32_16x16x32_bf16 v[90:93], v[184:187], v[200:203], v[90:93]
	v_mfma_f32_16x16x32_bf16 v[82:85], v[176:179], v[208:211], v[82:85]
	v_mfma_f32_16x16x32_bf16 v[74:77], v[184:187], v[208:211], v[74:77]
	v_mfma_f32_16x16x32_bf16 v[70:73], v[176:179], v[216:219], v[70:73]
	v_mfma_f32_16x16x32_bf16 v[66:69], v[184:187], v[216:219], v[66:69]
	s_setprio 0
	s_barrier
	s_add_i32 s29, s54, s31
	v_lshl_add_u64 v[148:149], s[40:41], 0, v[134:135]
	s_mov_b32 m0, s29
	ds_read_b128 v[188:191], v153 offset:16384
	ds_read_b128 v[192:195], v153 offset:17408
	ds_read_b128 v[196:199], v153 offset:18432
	ds_read_b128 v[200:203], v153 offset:19456
	ds_read_b128 v[204:207], v153 offset:20480
	ds_read_b128 v[208:211], v153 offset:21504
	ds_read_b128 v[212:215], v153 offset:22528
	ds_read_b128 v[216:219], v153 offset:23552
	global_load_lds_dwordx4 v[148:149], off
	s_add_i32 m0, s29, 0x2000
	s_add_u32 s62, s40, 0x4000
	v_lshl_add_u64 v[148:149], s[40:41], 0, v[130:131]
	s_addc_u32 s63, s41, 0
	s_add_i32 s29, s55, s31
	global_load_lds_dwordx4 v[148:149], off
	v_lshl_add_u64 v[148:149], s[62:63], 0, v[134:135]
	s_mov_b32 m0, s29
	v_lshl_add_u64 v[220:221], s[42:43], 0, v[132:133]
	global_load_lds_dwordx4 v[148:149], off
	v_lshl_add_u64 v[148:149], s[62:63], 0, v[130:131]
	s_add_i32 m0, s29, 0x2000
	s_nop 0
	global_load_lds_dwordx4 v[148:149], off
	v_lshl_add_u64 v[148:149], s[42:43], 0, v[136:137]
	s_mov_b32 m0, s21
	s_nop 0
	global_load_lds_dwordx4 v[148:149], off
	s_mov_b32 m0, s37
	s_nop 0
	global_load_lds_dwordx4 v[220:221], off
	s_waitcnt vmcnt(8)
	s_waitcnt lgkmcnt(0)
	s_barrier
	s_setprio 1
	v_mfma_f32_16x16x32_bf16 v[62:65], v[154:157], v[188:191], v[62:65]
	v_mfma_f32_16x16x32_bf16 v[58:61], v[162:165], v[188:191], v[58:61]
	v_mfma_f32_16x16x32_bf16 v[50:53], v[154:157], v[196:199], v[50:53]
	v_mfma_f32_16x16x32_bf16 v[42:45], v[162:165], v[196:199], v[42:45]
	v_mfma_f32_16x16x32_bf16 v[34:37], v[154:157], v[204:207], v[34:37]
	v_mfma_f32_16x16x32_bf16 v[26:29], v[162:165], v[204:207], v[26:29]
	v_mfma_f32_16x16x32_bf16 v[18:21], v[154:157], v[212:215], v[18:21]
	v_mfma_f32_16x16x32_bf16 v[10:13], v[162:165], v[212:215], v[10:13]
	v_mfma_f32_16x16x32_bf16 v[62:65], v[158:161], v[192:195], v[62:65]
	v_mfma_f32_16x16x32_bf16 v[58:61], v[166:169], v[192:195], v[58:61]
	v_mfma_f32_16x16x32_bf16 v[50:53], v[158:161], v[200:203], v[50:53]
	v_mfma_f32_16x16x32_bf16 v[42:45], v[166:169], v[200:203], v[42:45]
	v_mfma_f32_16x16x32_bf16 v[34:37], v[158:161], v[208:211], v[34:37]
	v_mfma_f32_16x16x32_bf16 v[26:29], v[166:169], v[208:211], v[26:29]
	v_mfma_f32_16x16x32_bf16 v[18:21], v[158:161], v[216:219], v[18:21]
	v_mfma_f32_16x16x32_bf16 v[10:13], v[166:169], v[216:219], v[10:13]
	s_setprio 0
	s_setprio 1
	v_mfma_f32_16x16x32_bf16 v[54:57], v[172:175], v[188:191], v[54:57]
	v_mfma_f32_16x16x32_bf16 v[46:49], v[180:183], v[188:191], v[46:49]
	v_mfma_f32_16x16x32_bf16 v[38:41], v[172:175], v[196:199], v[38:41]
	v_mfma_f32_16x16x32_bf16 v[30:33], v[180:183], v[196:199], v[30:33]
	v_mfma_f32_16x16x32_bf16 v[22:25], v[172:175], v[204:207], v[22:25]
	v_mfma_f32_16x16x32_bf16 v[14:17], v[180:183], v[204:207], v[14:17]
	v_mfma_f32_16x16x32_bf16 v[6:9], v[172:175], v[212:215], v[6:9]
	v_mfma_f32_16x16x32_bf16 v[2:5], v[180:183], v[212:215], v[2:5]
	v_mfma_f32_16x16x32_bf16 v[54:57], v[176:179], v[192:195], v[54:57]
	v_mfma_f32_16x16x32_bf16 v[46:49], v[184:187], v[192:195], v[46:49]
	v_mfma_f32_16x16x32_bf16 v[38:41], v[176:179], v[200:203], v[38:41]
	v_mfma_f32_16x16x32_bf16 v[30:33], v[184:187], v[200:203], v[30:33]
	v_mfma_f32_16x16x32_bf16 v[22:25], v[176:179], v[208:211], v[22:25]
	v_mfma_f32_16x16x32_bf16 v[14:17], v[184:187], v[208:211], v[14:17]
	v_mfma_f32_16x16x32_bf16 v[6:9], v[176:179], v[216:219], v[6:9]
	v_mfma_f32_16x16x32_bf16 v[2:5], v[184:187], v[216:219], v[2:5]
	s_setprio 0
	s_barrier
	s_add_i32 s29, 0, 0x18000
	s_add_i32 s61, 0, 0x1c000
	v_add_u32_e32 v166, s29, v150
	v_add_u32_e32 v171, s61, v150
	ds_read_b128 v[154:157], v166
	ds_read_b128 v[158:161], v166 offset:1024
	ds_read_b128 v[162:165], v166 offset:2048
	ds_read_b128 v[166:169], v166 offset:3072
	ds_read_b128 v[172:175], v171
	ds_read_b128 v[176:179], v171 offset:1024
	ds_read_b128 v[180:183], v171 offset:2048
	ds_read_b128 v[184:187], v171 offset:3072
	s_add_u32 s42, s42, 0x40000
	s_addc_u32 s43, s43, 0
	s_mov_b32 m0, s44
	v_lshl_add_u64 v[222:223], s[42:43], 0, v[136:137]
	ds_read_b128 v[188:191], v153 offset:32768
	ds_read_b128 v[192:195], v153 offset:33792
	ds_read_b128 v[196:199], v153 offset:34816
	ds_read_b128 v[200:203], v153 offset:35840
	ds_read_b128 v[204:207], v153 offset:36864
	ds_read_b128 v[208:211], v153 offset:37888
	ds_read_b128 v[212:215], v153 offset:38912
	ds_read_b128 v[216:219], v153 offset:39936
	global_load_lds_dwordx4 v[222:223], off
	v_lshl_add_u64 v[222:223], s[42:43], 0, v[132:133]
	s_mov_b32 m0, s45
	s_nop 0
	global_load_lds_dwordx4 v[222:223], off
	s_waitcnt vmcnt(8)
	s_waitcnt lgkmcnt(0)
	s_barrier
	s_setprio 1
	v_mfma_f32_16x16x32_bf16 v[126:129], v[154:157], v[188:191], v[126:129]
	v_mfma_f32_16x16x32_bf16 v[122:125], v[162:165], v[188:191], v[122:125]
	v_mfma_f32_16x16x32_bf16 v[118:121], v[154:157], v[196:199], v[118:121]
	v_mfma_f32_16x16x32_bf16 v[110:113], v[162:165], v[196:199], v[110:113]
	v_mfma_f32_16x16x32_bf16 v[102:105], v[154:157], v[204:207], v[102:105]
	v_mfma_f32_16x16x32_bf16 v[94:97], v[162:165], v[204:207], v[94:97]
	v_mfma_f32_16x16x32_bf16 v[86:89], v[154:157], v[212:215], v[86:89]
	v_mfma_f32_16x16x32_bf16 v[78:81], v[162:165], v[212:215], v[78:81]
	v_mfma_f32_16x16x32_bf16 v[126:129], v[158:161], v[192:195], v[126:129]
	v_mfma_f32_16x16x32_bf16 v[122:125], v[166:169], v[192:195], v[122:125]
	v_mfma_f32_16x16x32_bf16 v[118:121], v[158:161], v[200:203], v[118:121]
	v_mfma_f32_16x16x32_bf16 v[110:113], v[166:169], v[200:203], v[110:113]
	v_mfma_f32_16x16x32_bf16 v[102:105], v[158:161], v[208:211], v[102:105]
	v_mfma_f32_16x16x32_bf16 v[94:97], v[166:169], v[208:211], v[94:97]
	v_mfma_f32_16x16x32_bf16 v[86:89], v[158:161], v[216:219], v[86:89]
	v_mfma_f32_16x16x32_bf16 v[78:81], v[166:169], v[216:219], v[78:81]
	s_setprio 0
	s_setprio 1
	v_mfma_f32_16x16x32_bf16 v[114:117], v[172:175], v[188:191], v[114:117]
	v_mfma_f32_16x16x32_bf16 v[106:109], v[180:183], v[188:191], v[106:109]
	v_mfma_f32_16x16x32_bf16 v[98:101], v[172:175], v[196:199], v[98:101]
	v_mfma_f32_16x16x32_bf16 v[90:93], v[180:183], v[196:199], v[90:93]
	v_mfma_f32_16x16x32_bf16 v[82:85], v[172:175], v[204:207], v[82:85]
	v_mfma_f32_16x16x32_bf16 v[74:77], v[180:183], v[204:207], v[74:77]
	v_mfma_f32_16x16x32_bf16 v[70:73], v[172:175], v[212:215], v[70:73]
	v_mfma_f32_16x16x32_bf16 v[66:69], v[180:183], v[212:215], v[66:69]
	v_mfma_f32_16x16x32_bf16 v[114:117], v[176:179], v[192:195], v[114:117]
	v_mfma_f32_16x16x32_bf16 v[106:109], v[184:187], v[192:195], v[106:109]
	v_mfma_f32_16x16x32_bf16 v[98:101], v[176:179], v[200:203], v[98:101]
	v_mfma_f32_16x16x32_bf16 v[90:93], v[184:187], v[200:203], v[90:93]
	v_mfma_f32_16x16x32_bf16 v[82:85], v[176:179], v[208:211], v[82:85]
	v_mfma_f32_16x16x32_bf16 v[74:77], v[184:187], v[208:211], v[74:77]
	v_mfma_f32_16x16x32_bf16 v[70:73], v[176:179], v[216:219], v[70:73]
	v_mfma_f32_16x16x32_bf16 v[66:69], v[184:187], v[216:219], v[66:69]
	s_setprio 0
	s_barrier
	s_add_u32 s42, s40, 0x8000
	s_addc_u32 s43, s41, 0
	s_add_i32 s29, s29, s31
	v_lshl_add_u64 v[222:223], s[42:43], 0, v[134:135]
	s_mov_b32 m0, s29
	ds_read_b128 v[188:191], v153 offset:49152
	ds_read_b128 v[192:195], v153 offset:50176
	ds_read_b128 v[196:199], v153 offset:51200
	ds_read_b128 v[200:203], v153 offset:52224
	ds_read_b128 v[204:207], v153 offset:53248
	ds_read_b128 v[208:211], v153 offset:54272
	ds_read_b128 v[212:215], v153 offset:55296
	ds_read_b128 v[216:219], v153 offset:56320
	global_load_lds_dwordx4 v[222:223], off
	s_add_i32 m0, s29, 0x2000
	s_add_u32 s40, s40, 0xc000
	v_lshl_add_u64 v[222:223], s[42:43], 0, v[130:131]
	s_addc_u32 s41, s41, 0
	s_add_i32 s29, s61, s31
	global_load_lds_dwordx4 v[222:223], off
	v_lshl_add_u64 v[222:223], s[40:41], 0, v[134:135]
	s_mov_b32 m0, s29
	v_lshl_add_u64 v[148:149], v[148:149], 0, s[8:9]
	global_load_lds_dwordx4 v[222:223], off
	v_lshl_add_u64 v[222:223], s[40:41], 0, v[130:131]
	s_add_i32 m0, s29, 0x2000
	s_nop 0
	global_load_lds_dwordx4 v[222:223], off
	s_mov_b32 m0, s52
	s_nop 0
	global_load_lds_dwordx4 v[148:149], off
	v_lshl_add_u64 v[148:149], v[220:221], 0, s[8:9]
	s_mov_b32 m0, s53
	s_nop 0
	global_load_lds_dwordx4 v[148:149], off
	s_waitcnt vmcnt(8)
	s_waitcnt lgkmcnt(0)
	s_barrier
	s_setprio 1
	v_mfma_f32_16x16x32_bf16 v[62:65], v[154:157], v[188:191], v[62:65]
	v_mfma_f32_16x16x32_bf16 v[58:61], v[162:165], v[188:191], v[58:61]
	v_mfma_f32_16x16x32_bf16 v[50:53], v[154:157], v[196:199], v[50:53]
	v_mfma_f32_16x16x32_bf16 v[42:45], v[162:165], v[196:199], v[42:45]
	v_mfma_f32_16x16x32_bf16 v[34:37], v[154:157], v[204:207], v[34:37]
	v_mfma_f32_16x16x32_bf16 v[26:29], v[162:165], v[204:207], v[26:29]
	v_mfma_f32_16x16x32_bf16 v[18:21], v[154:157], v[212:215], v[18:21]
	v_mfma_f32_16x16x32_bf16 v[10:13], v[162:165], v[212:215], v[10:13]
	v_mfma_f32_16x16x32_bf16 v[62:65], v[158:161], v[192:195], v[62:65]
	v_mfma_f32_16x16x32_bf16 v[58:61], v[166:169], v[192:195], v[58:61]
	v_mfma_f32_16x16x32_bf16 v[50:53], v[158:161], v[200:203], v[50:53]
	v_mfma_f32_16x16x32_bf16 v[42:45], v[166:169], v[200:203], v[42:45]
	v_mfma_f32_16x16x32_bf16 v[34:37], v[158:161], v[208:211], v[34:37]
	v_mfma_f32_16x16x32_bf16 v[26:29], v[166:169], v[208:211], v[26:29]
	v_mfma_f32_16x16x32_bf16 v[18:21], v[158:161], v[216:219], v[18:21]
	v_mfma_f32_16x16x32_bf16 v[10:13], v[166:169], v[216:219], v[10:13]
	s_setprio 0
	s_setprio 1
	v_mfma_f32_16x16x32_bf16 v[54:57], v[172:175], v[188:191], v[54:57]
	v_mfma_f32_16x16x32_bf16 v[46:49], v[180:183], v[188:191], v[46:49]
	v_mfma_f32_16x16x32_bf16 v[38:41], v[172:175], v[196:199], v[38:41]
	v_mfma_f32_16x16x32_bf16 v[30:33], v[180:183], v[196:199], v[30:33]
	v_mfma_f32_16x16x32_bf16 v[22:25], v[172:175], v[204:207], v[22:25]
	v_mfma_f32_16x16x32_bf16 v[14:17], v[180:183], v[204:207], v[14:17]
	v_mfma_f32_16x16x32_bf16 v[6:9], v[172:175], v[212:215], v[6:9]
	v_mfma_f32_16x16x32_bf16 v[2:5], v[180:183], v[212:215], v[2:5]
	v_mfma_f32_16x16x32_bf16 v[54:57], v[176:179], v[192:195], v[54:57]
	v_mfma_f32_16x16x32_bf16 v[46:49], v[184:187], v[192:195], v[46:49]
	v_mfma_f32_16x16x32_bf16 v[38:41], v[176:179], v[200:203], v[38:41]
	v_mfma_f32_16x16x32_bf16 v[30:33], v[184:187], v[200:203], v[30:33]
	v_mfma_f32_16x16x32_bf16 v[22:25], v[176:179], v[208:211], v[22:25]
	v_mfma_f32_16x16x32_bf16 v[14:17], v[184:187], v[208:211], v[14:17]
	v_mfma_f32_16x16x32_bf16 v[6:9], v[176:179], v[216:219], v[6:9]
	v_mfma_f32_16x16x32_bf16 v[2:5], v[184:187], v[216:219], v[2:5]
	s_setprio 0
	s_barrier
	s_add_i32 s28, s28, 2
	s_add_u32 s59, s59, 0x10000
	s_addc_u32 s60, s60, 0
	s_add_u32 s22, s22, 0x100
	s_addc_u32 s23, s23, 0
	s_cmp_gt_u32 s28, 13
	s_cbranch_scc0 .LBB0_2294
	s_and_b64 vcc, exec, s[10:11]
	s_cbranch_vccz .LBB0_2297
	s_barrier

.LBB0_2659:
	ds_read_b128 v[122:125], v171
	ds_read_b128 v[126:129], v171 offset:1024
	ds_read_b128 v[130:133], v171 offset:2048
	ds_read_b128 v[134:137], v171 offset:3072
	ds_read_b128 v[162:165], v172
	ds_read_b128 v[174:177], v172 offset:1024
	ds_read_b128 v[178:181], v172 offset:2048
	ds_read_b128 v[182:185], v172 offset:3072
	s_add_u32 s29, s48, 0xfff80080
	s_addc_u32 s50, s49, -1
	s_cmp_eq_u32 s28, 28
	s_cselect_b32 s53, s41, s50
	s_cselect_b32 s52, s70, s29
	s_cselect_b32 s51, s23, s73
	s_cselect_b32 s50, s71, s72
	v_lshl_add_u64 v[166:167], s[48:49], 0, v[154:155]
	s_add_i32 m0, s47, 0xc000
	ds_read_b128 v[186:189], v173
	ds_read_b128 v[190:193], v173 offset:1024
	ds_read_b128 v[194:197], v173 offset:2048
	ds_read_b128 v[198:201], v173 offset:3072
	ds_read_b128 v[202:205], v173 offset:4096
	ds_read_b128 v[206:209], v173 offset:5120
	ds_read_b128 v[210:213], v173 offset:6144
	ds_read_b128 v[214:217], v173 offset:7168
	global_load_lds_dwordx4 v[166:167], off
	v_lshl_add_u64 v[166:167], s[48:49], 0, v[156:157]
	s_add_i32 m0, s47, 0xe000
	s_nop 0
	global_load_lds_dwordx4 v[166:167], off
	s_waitcnt vmcnt(8)
	s_waitcnt lgkmcnt(0)
	s_barrier
	s_setprio 1
	v_mfma_f32_16x16x32_bf16 v[142:145], v[122:125], v[186:189], v[142:145]
	v_mfma_f32_16x16x32_bf16 v[138:141], v[130:133], v[186:189], v[138:141]
	v_mfma_f32_16x16x32_bf16 v[114:117], v[122:125], v[194:197], v[114:117]
	v_mfma_f32_16x16x32_bf16 v[106:109], v[130:133], v[194:197], v[106:109]
	v_mfma_f32_16x16x32_bf16 v[98:101], v[122:125], v[202:205], v[98:101]
	v_mfma_f32_16x16x32_bf16 v[90:93], v[130:133], v[202:205], v[90:93]
	v_mfma_f32_16x16x32_bf16 v[82:85], v[122:125], v[210:213], v[82:85]
	v_mfma_f32_16x16x32_bf16 v[74:77], v[130:133], v[210:213], v[74:77]
	v_mfma_f32_16x16x32_bf16 v[142:145], v[126:129], v[190:193], v[142:145]
	v_mfma_f32_16x16x32_bf16 v[138:141], v[134:137], v[190:193], v[138:141]
	v_mfma_f32_16x16x32_bf16 v[114:117], v[126:129], v[198:201], v[114:117]
	v_mfma_f32_16x16x32_bf16 v[106:109], v[134:137], v[198:201], v[106:109]
	v_mfma_f32_16x16x32_bf16 v[98:101], v[126:129], v[206:209], v[98:101]
	v_mfma_f32_16x16x32_bf16 v[90:93], v[134:137], v[206:209], v[90:93]
	v_mfma_f32_16x16x32_bf16 v[82:85], v[126:129], v[214:217], v[82:85]
	v_mfma_f32_16x16x32_bf16 v[74:77], v[134:137], v[214:217], v[74:77]
	s_setprio 0
	s_setprio 1
	v_mfma_f32_16x16x32_bf16 v[118:121], v[162:165], v[186:189], v[118:121]
	v_mfma_f32_16x16x32_bf16 v[110:113], v[178:181], v[186:189], v[110:113]
	v_mfma_f32_16x16x32_bf16 v[102:105], v[162:165], v[194:197], v[102:105]
	v_mfma_f32_16x16x32_bf16 v[94:97], v[178:181], v[194:197], v[94:97]
	v_mfma_f32_16x16x32_bf16 v[86:89], v[162:165], v[202:205], v[86:89]
	v_mfma_f32_16x16x32_bf16 v[78:81], v[178:181], v[202:205], v[78:81]
	v_mfma_f32_16x16x32_bf16 v[70:73], v[162:165], v[210:213], v[70:73]
	v_mfma_f32_16x16x32_bf16 v[66:69], v[178:181], v[210:213], v[66:69]
	v_mfma_f32_16x16x32_bf16 v[118:121], v[174:177], v[190:193], v[118:121]
	v_mfma_f32_16x16x32_bf16 v[110:113], v[182:185], v[190:193], v[110:113]
	v_mfma_f32_16x16x32_bf16 v[102:105], v[174:177], v[198:201], v[102:105]
	v_mfma_f32_16x16x32_bf16 v[94:97], v[182:185], v[198:201], v[94:97]
	v_mfma_f32_16x16x32_bf16 v[86:89], v[174:177], v[206:209], v[86:89]
	v_mfma_f32_16x16x32_bf16 v[78:81], v[182:185], v[206:209], v[78:81]
	v_mfma_f32_16x16x32_bf16 v[70:73], v[174:177], v[214:217], v[70:73]
	v_mfma_f32_16x16x32_bf16 v[66:69], v[182:185], v[214:217], v[66:69]
	s_setprio 0
	s_barrier
	s_add_i32 s29, s64, s54
	v_lshl_add_u64 v[166:167], s[50:51], 0, v[148:149]
	s_mov_b32 m0, s29
	ds_read_b128 v[186:189], v173 offset:16384
	ds_read_b128 v[190:193], v173 offset:17408
	ds_read_b128 v[194:197], v173 offset:18432
	ds_read_b128 v[198:201], v173 offset:19456
	ds_read_b128 v[202:205], v173 offset:20480
	ds_read_b128 v[206:209], v173 offset:21504
	ds_read_b128 v[210:213], v173 offset:22528
	ds_read_b128 v[214:217], v173 offset:23552
	global_load_lds_dwordx4 v[166:167], off
	s_add_i32 m0, s29, 0x2000
	s_add_u32 s76, s50, 0x4000
	v_lshl_add_u64 v[166:167], s[50:51], 0, v[152:153]
	s_addc_u32 s77, s51, 0
	s_add_i32 s29, s65, s54
	global_load_lds_dwordx4 v[166:167], off
	v_lshl_add_u64 v[166:167], s[76:77], 0, v[148:149]
	s_mov_b32 m0, s29
	v_lshl_add_u64 v[218:219], s[52:53], 0, v[150:151]
	global_load_lds_dwordx4 v[166:167], off
	v_lshl_add_u64 v[166:167], s[76:77], 0, v[152:153]
	s_add_i32 m0, s29, 0x2000
	s_nop 0
	global_load_lds_dwordx4 v[166:167], off
	v_lshl_add_u64 v[166:167], s[52:53], 0, v[146:147]
	s_mov_b32 m0, s47
	s_nop 0
	global_load_lds_dwordx4 v[166:167], off
	s_mov_b32 m0, s55
	s_nop 0
	global_load_lds_dwordx4 v[218:219], off
	s_waitcnt vmcnt(8)
	s_waitcnt lgkmcnt(0)
	s_barrier
	s_setprio 1
	v_mfma_f32_16x16x32_bf16 v[62:65], v[122:125], v[186:189], v[62:65]
	v_mfma_f32_16x16x32_bf16 v[58:61], v[130:133], v[186:189], v[58:61]
	v_mfma_f32_16x16x32_bf16 v[46:49], v[122:125], v[194:197], v[46:49]
	v_mfma_f32_16x16x32_bf16 v[42:45], v[130:133], v[194:197], v[42:45]
	v_mfma_f32_16x16x32_bf16 v[30:33], v[122:125], v[202:205], v[30:33]
	v_mfma_f32_16x16x32_bf16 v[26:29], v[130:133], v[202:205], v[26:29]
	v_mfma_f32_16x16x32_bf16 v[14:17], v[122:125], v[210:213], v[14:17]
	v_mfma_f32_16x16x32_bf16 v[10:13], v[130:133], v[210:213], v[10:13]
	v_mfma_f32_16x16x32_bf16 v[62:65], v[126:129], v[190:193], v[62:65]
	v_mfma_f32_16x16x32_bf16 v[58:61], v[134:137], v[190:193], v[58:61]
	v_mfma_f32_16x16x32_bf16 v[46:49], v[126:129], v[198:201], v[46:49]
	v_mfma_f32_16x16x32_bf16 v[42:45], v[134:137], v[198:201], v[42:45]
	v_mfma_f32_16x16x32_bf16 v[30:33], v[126:129], v[206:209], v[30:33]
	v_mfma_f32_16x16x32_bf16 v[26:29], v[134:137], v[206:209], v[26:29]
	v_mfma_f32_16x16x32_bf16 v[14:17], v[126:129], v[214:217], v[14:17]
	v_mfma_f32_16x16x32_bf16 v[10:13], v[134:137], v[214:217], v[10:13]
	s_setprio 0
	s_setprio 1
	v_mfma_f32_16x16x32_bf16 v[54:57], v[162:165], v[186:189], v[54:57]
	v_mfma_f32_16x16x32_bf16 v[50:53], v[178:181], v[186:189], v[50:53]
	v_mfma_f32_16x16x32_bf16 v[38:41], v[162:165], v[194:197], v[38:41]
	v_mfma_f32_16x16x32_bf16 v[34:37], v[178:181], v[194:197], v[34:37]
	v_mfma_f32_16x16x32_bf16 v[22:25], v[162:165], v[202:205], v[22:25]
	v_mfma_f32_16x16x32_bf16 v[18:21], v[178:181], v[202:205], v[18:21]
	v_mfma_f32_16x16x32_bf16 v[6:9], v[162:165], v[210:213], v[6:9]
	v_mfma_f32_16x16x32_bf16 v[2:5], v[178:181], v[210:213], v[2:5]
	v_mfma_f32_16x16x32_bf16 v[54:57], v[174:177], v[190:193], v[54:57]
	v_mfma_f32_16x16x32_bf16 v[50:53], v[182:185], v[190:193], v[50:53]
	v_mfma_f32_16x16x32_bf16 v[38:41], v[174:177], v[198:201], v[38:41]
	v_mfma_f32_16x16x32_bf16 v[34:37], v[182:185], v[198:201], v[34:37]
	v_mfma_f32_16x16x32_bf16 v[22:25], v[174:177], v[206:209], v[22:25]
	v_mfma_f32_16x16x32_bf16 v[18:21], v[182:185], v[206:209], v[18:21]
	v_mfma_f32_16x16x32_bf16 v[6:9], v[174:177], v[214:217], v[6:9]
	v_mfma_f32_16x16x32_bf16 v[2:5], v[182:185], v[214:217], v[2:5]
	s_setprio 0
	s_barrier
	s_add_i32 s29, 0, 0x18000
	s_add_i32 s75, 0, 0x1c000
	v_add_u32_e32 v134, s29, v168
	v_add_u32_e32 v182, s75, v168
	ds_read_b128 v[122:125], v134
	ds_read_b128 v[126:129], v134 offset:1024
	ds_read_b128 v[130:133], v134 offset:2048
	ds_read_b128 v[134:137], v134 offset:3072
	ds_read_b128 v[162:165], v182
	ds_read_b128 v[174:177], v182 offset:1024
	ds_read_b128 v[178:181], v182 offset:2048
	ds_read_b128 v[182:185], v182 offset:3072
	s_add_u32 s52, s52, 0x80000
	s_addc_u32 s53, s53, 0
	s_mov_b32 m0, s56
	v_lshl_add_u64 v[220:221], s[52:53], 0, v[146:147]
	ds_read_b128 v[186:189], v173 offset:32768
	ds_read_b128 v[190:193], v173 offset:33792
	ds_read_b128 v[194:197], v173 offset:34816
	ds_read_b128 v[198:201], v173 offset:35840
	ds_read_b128 v[202:205], v173 offset:36864
	ds_read_b128 v[206:209], v173 offset:37888
	ds_read_b128 v[210:213], v173 offset:38912
	ds_read_b128 v[214:217], v173 offset:39936
	global_load_lds_dwordx4 v[220:221], off
	v_lshl_add_u64 v[220:221], s[52:53], 0, v[150:151]
	s_mov_b32 m0, s57
	s_nop 0
	global_load_lds_dwordx4 v[220:221], off
	s_waitcnt vmcnt(8)
	s_waitcnt lgkmcnt(0)
	s_barrier
	s_setprio 1
	v_mfma_f32_16x16x32_bf16 v[142:145], v[122:125], v[186:189], v[142:145]
	v_mfma_f32_16x16x32_bf16 v[138:141], v[130:133], v[186:189], v[138:141]
	v_mfma_f32_16x16x32_bf16 v[114:117], v[122:125], v[194:197], v[114:117]
	v_mfma_f32_16x16x32_bf16 v[106:109], v[130:133], v[194:197], v[106:109]
	v_mfma_f32_16x16x32_bf16 v[98:101], v[122:125], v[202:205], v[98:101]
	v_mfma_f32_16x16x32_bf16 v[90:93], v[130:133], v[202:205], v[90:93]
	v_mfma_f32_16x16x32_bf16 v[82:85], v[122:125], v[210:213], v[82:85]
	v_mfma_f32_16x16x32_bf16 v[74:77], v[130:133], v[210:213], v[74:77]
	v_mfma_f32_16x16x32_bf16 v[142:145], v[126:129], v[190:193], v[142:145]
	v_mfma_f32_16x16x32_bf16 v[138:141], v[134:137], v[190:193], v[138:141]
	v_mfma_f32_16x16x32_bf16 v[114:117], v[126:129], v[198:201], v[114:117]
	v_mfma_f32_16x16x32_bf16 v[106:109], v[134:137], v[198:201], v[106:109]
	v_mfma_f32_16x16x32_bf16 v[98:101], v[126:129], v[206:209], v[98:101]
	v_mfma_f32_16x16x32_bf16 v[90:93], v[134:137], v[206:209], v[90:93]
	v_mfma_f32_16x16x32_bf16 v[82:85], v[126:129], v[214:217], v[82:85]
	v_mfma_f32_16x16x32_bf16 v[74:77], v[134:137], v[214:217], v[74:77]
	s_setprio 0
	s_setprio 1
	v_mfma_f32_16x16x32_bf16 v[118:121], v[162:165], v[186:189], v[118:121]
	v_mfma_f32_16x16x32_bf16 v[110:113], v[178:181], v[186:189], v[110:113]
	v_mfma_f32_16x16x32_bf16 v[102:105], v[162:165], v[194:197], v[102:105]
	v_mfma_f32_16x16x32_bf16 v[94:97], v[178:181], v[194:197], v[94:97]
	v_mfma_f32_16x16x32_bf16 v[86:89], v[162:165], v[202:205], v[86:89]
	v_mfma_f32_16x16x32_bf16 v[78:81], v[178:181], v[202:205], v[78:81]
	v_mfma_f32_16x16x32_bf16 v[70:73], v[162:165], v[210:213], v[70:73]
	v_mfma_f32_16x16x32_bf16 v[66:69], v[178:181], v[210:213], v[66:69]
	v_mfma_f32_16x16x32_bf16 v[118:121], v[174:177], v[190:193], v[118:121]
	v_mfma_f32_16x16x32_bf16 v[110:113], v[182:185], v[190:193], v[110:113]
	v_mfma_f32_16x16x32_bf16 v[102:105], v[174:177], v[198:201], v[102:105]
	v_mfma_f32_16x16x32_bf16 v[94:97], v[182:185], v[198:201], v[94:97]
	v_mfma_f32_16x16x32_bf16 v[86:89], v[174:177], v[206:209], v[86:89]
	v_mfma_f32_16x16x32_bf16 v[78:81], v[182:185], v[206:209], v[78:81]
	v_mfma_f32_16x16x32_bf16 v[70:73], v[174:177], v[214:217], v[70:73]
	v_mfma_f32_16x16x32_bf16 v[66:69], v[182:185], v[214:217], v[66:69]
	s_setprio 0
	s_barrier
	s_add_u32 s52, s50, 0x8000
	s_addc_u32 s53, s51, 0
	s_add_i32 s29, s29, s54
	v_lshl_add_u64 v[220:221], s[52:53], 0, v[148:149]
	s_mov_b32 m0, s29
	ds_read_b128 v[186:189], v173 offset:49152
	ds_read_b128 v[190:193], v173 offset:50176
	ds_read_b128 v[194:197], v173 offset:51200
	ds_read_b128 v[198:201], v173 offset:52224
	ds_read_b128 v[202:205], v173 offset:53248
	ds_read_b128 v[206:209], v173 offset:54272
	ds_read_b128 v[210:213], v173 offset:55296
	ds_read_b128 v[214:217], v173 offset:56320
	global_load_lds_dwordx4 v[220:221], off
	s_add_i32 m0, s29, 0x2000
	s_add_u32 s50, s50, 0xc000
	v_lshl_add_u64 v[220:221], s[52:53], 0, v[152:153]
	s_addc_u32 s51, s51, 0
	s_add_i32 s29, s75, s54
	global_load_lds_dwordx4 v[220:221], off
	v_lshl_add_u64 v[220:221], s[50:51], 0, v[148:149]
	s_mov_b32 m0, s29
	v_lshl_add_u64 v[166:167], v[166:167], 0, s[10:11]
	global_load_lds_dwordx4 v[220:221], off
	v_lshl_add_u64 v[220:221], s[50:51], 0, v[152:153]
	s_add_i32 m0, s29, 0x2000
	s_nop 0
	global_load_lds_dwordx4 v[220:221], off
	s_mov_b32 m0, s61
	s_nop 0
	global_load_lds_dwordx4 v[166:167], off
	v_lshl_add_u64 v[166:167], v[218:219], 0, s[10:11]
	s_mov_b32 m0, s62
	s_nop 0
	global_load_lds_dwordx4 v[166:167], off
	s_waitcnt vmcnt(8)
	s_waitcnt lgkmcnt(0)
	s_barrier
	s_setprio 1
	v_mfma_f32_16x16x32_bf16 v[62:65], v[122:125], v[186:189], v[62:65]
	v_mfma_f32_16x16x32_bf16 v[58:61], v[130:133], v[186:189], v[58:61]
	v_mfma_f32_16x16x32_bf16 v[46:49], v[122:125], v[194:197], v[46:49]
	v_mfma_f32_16x16x32_bf16 v[42:45], v[130:133], v[194:197], v[42:45]
	v_mfma_f32_16x16x32_bf16 v[30:33], v[122:125], v[202:205], v[30:33]
	v_mfma_f32_16x16x32_bf16 v[26:29], v[130:133], v[202:205], v[26:29]
	v_mfma_f32_16x16x32_bf16 v[14:17], v[122:125], v[210:213], v[14:17]
	v_mfma_f32_16x16x32_bf16 v[10:13], v[130:133], v[210:213], v[10:13]
	v_mfma_f32_16x16x32_bf16 v[62:65], v[126:129], v[190:193], v[62:65]
	v_mfma_f32_16x16x32_bf16 v[58:61], v[134:137], v[190:193], v[58:61]
	v_mfma_f32_16x16x32_bf16 v[46:49], v[126:129], v[198:201], v[46:49]
	v_mfma_f32_16x16x32_bf16 v[42:45], v[134:137], v[198:201], v[42:45]
	v_mfma_f32_16x16x32_bf16 v[30:33], v[126:129], v[206:209], v[30:33]
	v_mfma_f32_16x16x32_bf16 v[26:29], v[134:137], v[206:209], v[26:29]
	v_mfma_f32_16x16x32_bf16 v[14:17], v[126:129], v[214:217], v[14:17]
	v_mfma_f32_16x16x32_bf16 v[10:13], v[134:137], v[214:217], v[10:13]
	s_setprio 0
	s_setprio 1
	v_mfma_f32_16x16x32_bf16 v[54:57], v[162:165], v[186:189], v[54:57]
	v_mfma_f32_16x16x32_bf16 v[50:53], v[178:181], v[186:189], v[50:53]
	v_mfma_f32_16x16x32_bf16 v[38:41], v[162:165], v[194:197], v[38:41]
	v_mfma_f32_16x16x32_bf16 v[34:37], v[178:181], v[194:197], v[34:37]
	v_mfma_f32_16x16x32_bf16 v[22:25], v[162:165], v[202:205], v[22:25]
	v_mfma_f32_16x16x32_bf16 v[18:21], v[178:181], v[202:205], v[18:21]
	v_mfma_f32_16x16x32_bf16 v[6:9], v[162:165], v[210:213], v[6:9]
	v_mfma_f32_16x16x32_bf16 v[2:5], v[178:181], v[210:213], v[2:5]
	v_mfma_f32_16x16x32_bf16 v[54:57], v[174:177], v[190:193], v[54:57]
	v_mfma_f32_16x16x32_bf16 v[50:53], v[182:185], v[190:193], v[50:53]
	v_mfma_f32_16x16x32_bf16 v[38:41], v[174:177], v[198:201], v[38:41]
	v_mfma_f32_16x16x32_bf16 v[34:37], v[182:185], v[198:201], v[34:37]
	v_mfma_f32_16x16x32_bf16 v[22:25], v[174:177], v[206:209], v[22:25]
	v_mfma_f32_16x16x32_bf16 v[18:21], v[182:185], v[206:209], v[18:21]
	v_mfma_f32_16x16x32_bf16 v[6:9], v[174:177], v[214:217], v[6:9]
	v_mfma_f32_16x16x32_bf16 v[2:5], v[182:185], v[214:217], v[2:5]
	s_setprio 0
	s_barrier
	s_add_i32 s28, s28, 2
	s_add_u32 s72, s72, 0x10000
	s_addc_u32 s73, s73, 0
	s_add_u32 s48, s48, 0x100
	s_addc_u32 s49, s49, 0
	s_cmp_gt_u32 s28, 29
	s_cbranch_scc0 .LBB0_2659
	s_and_b64 vcc, exec, s[12:13]
	s_cbranch_vccz .LBB0_2662
	s_barrier

.LBB0_2904:
	v_add_u32_e32 v134, s33, v167
	ds_read_b128 v[172:175], v134
	ds_read_b128 v[176:179], v134 offset:1024
	ds_read_b128 v[180:183], v134 offset:2048
	ds_read_b128 v[184:187], v134 offset:3072
	v_add_u32_e32 v134, s81, v167
	ds_read_b128 v[188:191], v134
	ds_read_b128 v[192:195], v134 offset:1024
	ds_read_b128 v[196:199], v134 offset:2048
	ds_read_b128 v[200:203], v134 offset:3072
	s_add_u32 s54, s52, 0x100
	s_addc_u32 s55, s53, 0
	s_and_b64 s[28:29], s[8:9], exec
	s_cselect_b32 s29, 0, s54
	s_cselect_b32 s28, 0, s55
	s_add_u32 s56, s38, s29
	v_cndmask_b32_e64 v239, v159, v143, s[8:9]
	v_cndmask_b32_e64 v238, v158, v142, s[8:9]
	s_addc_u32 s57, s39, s28
	v_lshl_add_u64 v[240:241], v[238:239], 0, s[22:23]
	v_cndmask_b32_e64 v134, v141, v147, s[8:9]
	v_cndmask_b32_e64 v242, v144, v149, s[8:9]
	v_cndmask_b32_e64 v145, v146, v169, s[8:9]
	v_cndmask_b32_e64 v232, v148, v171, s[8:9]
	v_lshl_add_u64 v[244:245], v[160:161], 0, s[52:53]
	s_add_i32 m0, s68, 0xc000
	ds_read_b128 v[204:207], v168
	ds_read_b128 v[208:211], v168 offset:1024
	ds_read_b128 v[212:215], v168 offset:2048
	ds_read_b128 v[216:219], v168 offset:3072
	ds_read_b128 v[220:223], v168 offset:4096
	ds_read_b128 v[224:227], v168 offset:5120
	ds_read_b128 v[228:231], v168 offset:6144
	ds_read_b128 v[234:237], v168 offset:7168
	global_load_lds_dwordx4 v[244:245], off
	v_lshl_add_u64 v[244:245], v[162:163], 0, s[52:53]
	s_add_i32 m0, s68, 0xe000
	s_nop 0
	global_load_lds_dwordx4 v[244:245], off
	s_waitcnt vmcnt(8)
	s_waitcnt lgkmcnt(0)
	s_barrier
	s_setprio 1
	v_mfma_f32_16x16x32_bf16 v[126:129], v[172:175], v[204:207], v[126:129]
	v_mfma_f32_16x16x32_bf16 v[122:125], v[180:183], v[204:207], v[122:125]
	v_mfma_f32_16x16x32_bf16 v[118:121], v[172:175], v[212:215], v[118:121]
	v_mfma_f32_16x16x32_bf16 v[114:117], v[180:183], v[212:215], v[114:117]
	v_mfma_f32_16x16x32_bf16 v[94:97], v[172:175], v[220:223], v[94:97]
	v_mfma_f32_16x16x32_bf16 v[90:93], v[180:183], v[220:223], v[90:93]
	v_mfma_f32_16x16x32_bf16 v[86:89], v[172:175], v[228:231], v[86:89]
	v_mfma_f32_16x16x32_bf16 v[82:85], v[180:183], v[228:231], v[82:85]
	v_mfma_f32_16x16x32_bf16 v[126:129], v[176:179], v[208:211], v[126:129]
	v_mfma_f32_16x16x32_bf16 v[122:125], v[184:187], v[208:211], v[122:125]
	v_mfma_f32_16x16x32_bf16 v[118:121], v[176:179], v[216:219], v[118:121]
	v_mfma_f32_16x16x32_bf16 v[114:117], v[184:187], v[216:219], v[114:117]
	v_mfma_f32_16x16x32_bf16 v[94:97], v[176:179], v[224:227], v[94:97]
	v_mfma_f32_16x16x32_bf16 v[90:93], v[184:187], v[224:227], v[90:93]
	v_mfma_f32_16x16x32_bf16 v[86:89], v[176:179], v[234:237], v[86:89]
	v_mfma_f32_16x16x32_bf16 v[82:85], v[184:187], v[234:237], v[82:85]
	s_setprio 0
	s_setprio 1
	v_mfma_f32_16x16x32_bf16 v[110:113], v[188:191], v[204:207], v[110:113]
	v_mfma_f32_16x16x32_bf16 v[106:109], v[196:199], v[204:207], v[106:109]
	v_mfma_f32_16x16x32_bf16 v[102:105], v[188:191], v[212:215], v[102:105]
	v_mfma_f32_16x16x32_bf16 v[98:101], v[196:199], v[212:215], v[98:101]
	v_mfma_f32_16x16x32_bf16 v[78:81], v[188:191], v[220:223], v[78:81]
	v_mfma_f32_16x16x32_bf16 v[74:77], v[196:199], v[220:223], v[74:77]
	v_mfma_f32_16x16x32_bf16 v[70:73], v[188:191], v[228:231], v[70:73]
	v_mfma_f32_16x16x32_bf16 v[66:69], v[196:199], v[228:231], v[66:69]
	v_mfma_f32_16x16x32_bf16 v[110:113], v[192:195], v[208:211], v[110:113]
	v_mfma_f32_16x16x32_bf16 v[106:109], v[200:203], v[208:211], v[106:109]
	v_mfma_f32_16x16x32_bf16 v[102:105], v[192:195], v[216:219], v[102:105]
	v_mfma_f32_16x16x32_bf16 v[98:101], v[200:203], v[216:219], v[98:101]
	v_mfma_f32_16x16x32_bf16 v[78:81], v[192:195], v[224:227], v[78:81]
	v_mfma_f32_16x16x32_bf16 v[74:77], v[200:203], v[224:227], v[74:77]
	v_mfma_f32_16x16x32_bf16 v[70:73], v[192:195], v[234:237], v[70:73]
	v_mfma_f32_16x16x32_bf16 v[66:69], v[200:203], v[234:237], v[66:69]
	s_setprio 0
	s_barrier
	s_add_i32 s8, s33, s66
	v_lshl_add_u64 v[244:245], v[238:239], 0, v[130:131]
	s_mov_b32 m0, s8
	ds_read_b128 v[204:207], v168 offset:16384
	ds_read_b128 v[208:211], v168 offset:17408
	ds_read_b128 v[212:215], v168 offset:18432
	ds_read_b128 v[216:219], v168 offset:19456
	ds_read_b128 v[220:223], v168 offset:20480
	ds_read_b128 v[224:227], v168 offset:21504
	ds_read_b128 v[228:231], v168 offset:22528
	ds_read_b128 v[234:237], v168 offset:23552
	global_load_lds_dwordx4 v[244:245], off
	v_lshl_add_u64 v[244:245], v[238:239], 0, v[132:133]
	s_add_i32 m0, s8, 0x2000
	s_add_i32 s8, s81, s66
	global_load_lds_dwordx4 v[244:245], off
	v_lshl_add_u64 v[244:245], v[238:239], 0, s[16:17]
	v_lshl_add_u64 v[246:247], v[244:245], 0, v[130:131]
	s_mov_b32 m0, s8
	v_lshl_add_u64 v[244:245], v[244:245], 0, v[132:133]
	global_load_lds_dwordx4 v[246:247], off
	s_add_i32 m0, s8, 0x2000
	v_mov_b32_e32 v243, v135
	global_load_lds_dwordx4 v[244:245], off
	s_mov_b32 m0, s68
	v_lshl_add_u64 v[244:245], s[56:57], 0, v[134:135]
	global_load_lds_dwordx4 v134, s[56:57]
	s_mov_b32 m0, s69
	s_nop 0
	global_load_lds_dwordx4 v242, s[56:57]
	s_waitcnt vmcnt(8)
	s_waitcnt lgkmcnt(0)
	v_lshl_add_u64 v[242:243], s[56:57], 0, v[242:243]
	s_barrier
	s_setprio 1
	s_waitcnt lgkmcnt(0)
	v_mfma_f32_16x16x32_bf16 v[62:65], v[172:175], v[204:207], v[62:65]
	v_mfma_f32_16x16x32_bf16 v[58:61], v[180:183], v[204:207], v[58:61]
	v_mfma_f32_16x16x32_bf16 v[54:57], v[172:175], v[212:215], v[54:57]
	v_mfma_f32_16x16x32_bf16 v[50:53], v[180:183], v[212:215], v[50:53]
	v_mfma_f32_16x16x32_bf16 v[30:33], v[172:175], v[220:223], v[30:33]
	v_mfma_f32_16x16x32_bf16 v[26:29], v[180:183], v[220:223], v[26:29]
	v_mfma_f32_16x16x32_bf16 v[22:25], v[172:175], v[228:231], v[22:25]
	v_mfma_f32_16x16x32_bf16 v[18:21], v[180:183], v[228:231], v[18:21]
	v_mfma_f32_16x16x32_bf16 v[62:65], v[176:179], v[208:211], v[62:65]
	v_mfma_f32_16x16x32_bf16 v[58:61], v[184:187], v[208:211], v[58:61]
	v_mfma_f32_16x16x32_bf16 v[54:57], v[176:179], v[216:219], v[54:57]
	v_mfma_f32_16x16x32_bf16 v[50:53], v[184:187], v[216:219], v[50:53]
	v_mfma_f32_16x16x32_bf16 v[30:33], v[176:179], v[224:227], v[30:33]
	v_mfma_f32_16x16x32_bf16 v[26:29], v[184:187], v[224:227], v[26:29]
	v_mfma_f32_16x16x32_bf16 v[22:25], v[176:179], v[234:237], v[22:25]
	v_mfma_f32_16x16x32_bf16 v[18:21], v[184:187], v[234:237], v[18:21]
	s_setprio 0
	s_setprio 1
	v_mfma_f32_16x16x32_bf16 v[46:49], v[188:191], v[204:207], v[46:49]
	v_mfma_f32_16x16x32_bf16 v[42:45], v[196:199], v[204:207], v[42:45]
	v_mfma_f32_16x16x32_bf16 v[38:41], v[188:191], v[212:215], v[38:41]
	v_mfma_f32_16x16x32_bf16 v[34:37], v[196:199], v[212:215], v[34:37]
	v_mfma_f32_16x16x32_bf16 v[14:17], v[188:191], v[220:223], v[14:17]
	v_mfma_f32_16x16x32_bf16 v[10:13], v[196:199], v[220:223], v[10:13]
	v_mfma_f32_16x16x32_bf16 v[6:9], v[188:191], v[228:231], v[6:9]
	v_mfma_f32_16x16x32_bf16 v[2:5], v[196:199], v[228:231], v[2:5]
	v_mfma_f32_16x16x32_bf16 v[46:49], v[192:195], v[208:211], v[46:49]
	v_mfma_f32_16x16x32_bf16 v[42:45], v[200:203], v[208:211], v[42:45]
	v_mfma_f32_16x16x32_bf16 v[38:41], v[192:195], v[216:219], v[38:41]
	v_mfma_f32_16x16x32_bf16 v[34:37], v[200:203], v[216:219], v[34:37]
	v_mfma_f32_16x16x32_bf16 v[14:17], v[192:195], v[224:227], v[14:17]
	v_mfma_f32_16x16x32_bf16 v[10:13], v[200:203], v[224:227], v[10:13]
	v_mfma_f32_16x16x32_bf16 v[6:9], v[192:195], v[234:237], v[6:9]
	v_mfma_f32_16x16x32_bf16 v[2:5], v[200:203], v[234:237], v[2:5]
	s_setprio 0
	s_barrier
	s_add_i32 s8, 0, 0x18000
	v_add_u32_e32 v134, s8, v167
	s_add_i32 s9, 0, 0x1c000
	ds_read_b128 v[172:175], v134
	ds_read_b128 v[176:179], v134 offset:1024
	ds_read_b128 v[180:183], v134 offset:2048
	ds_read_b128 v[184:187], v134 offset:3072
	v_add_u32_e32 v134, s9, v167
	ds_read_b128 v[188:191], v134
	ds_read_b128 v[192:195], v134 offset:1024
	ds_read_b128 v[196:199], v134 offset:2048
	ds_read_b128 v[200:203], v134 offset:3072
	s_mov_b32 m0, s70
	ds_read_b128 v[204:207], v168 offset:32768
	ds_read_b128 v[208:211], v168 offset:33792
	ds_read_b128 v[212:215], v168 offset:34816
	ds_read_b128 v[216:219], v168 offset:35840
	ds_read_b128 v[220:223], v168 offset:36864
	ds_read_b128 v[224:227], v168 offset:37888
	ds_read_b128 v[228:231], v168 offset:38912
	ds_read_b128 v[234:237], v168 offset:39936
	global_load_lds_dwordx4 v145, s[56:57]
	s_mov_b32 m0, s71
	s_nop 0
	global_load_lds_dwordx4 v232, s[56:57]
	s_waitcnt vmcnt(8)
	s_waitcnt lgkmcnt(0)
	s_barrier
	s_setprio 1
	v_mfma_f32_16x16x32_bf16 v[126:129], v[172:175], v[204:207], v[126:129]
	v_mfma_f32_16x16x32_bf16 v[122:125], v[180:183], v[204:207], v[122:125]
	v_mfma_f32_16x16x32_bf16 v[118:121], v[172:175], v[212:215], v[118:121]
	v_mfma_f32_16x16x32_bf16 v[114:117], v[180:183], v[212:215], v[114:117]
	v_mfma_f32_16x16x32_bf16 v[94:97], v[172:175], v[220:223], v[94:97]
	v_mfma_f32_16x16x32_bf16 v[90:93], v[180:183], v[220:223], v[90:93]
	v_mfma_f32_16x16x32_bf16 v[86:89], v[172:175], v[228:231], v[86:89]
	v_mfma_f32_16x16x32_bf16 v[82:85], v[180:183], v[228:231], v[82:85]
	v_mfma_f32_16x16x32_bf16 v[126:129], v[176:179], v[208:211], v[126:129]
	v_mfma_f32_16x16x32_bf16 v[122:125], v[184:187], v[208:211], v[122:125]
	v_mfma_f32_16x16x32_bf16 v[118:121], v[176:179], v[216:219], v[118:121]
	v_mfma_f32_16x16x32_bf16 v[114:117], v[184:187], v[216:219], v[114:117]
	v_mfma_f32_16x16x32_bf16 v[94:97], v[176:179], v[224:227], v[94:97]
	v_mfma_f32_16x16x32_bf16 v[90:93], v[184:187], v[224:227], v[90:93]
	v_mfma_f32_16x16x32_bf16 v[86:89], v[176:179], v[234:237], v[86:89]
	v_mfma_f32_16x16x32_bf16 v[82:85], v[184:187], v[234:237], v[82:85]
	s_setprio 0
	s_setprio 1
	v_mfma_f32_16x16x32_bf16 v[110:113], v[188:191], v[204:207], v[110:113]
	v_mfma_f32_16x16x32_bf16 v[106:109], v[196:199], v[204:207], v[106:109]
	v_mfma_f32_16x16x32_bf16 v[102:105], v[188:191], v[212:215], v[102:105]
	v_mfma_f32_16x16x32_bf16 v[98:101], v[196:199], v[212:215], v[98:101]
	v_mfma_f32_16x16x32_bf16 v[78:81], v[188:191], v[220:223], v[78:81]
	v_mfma_f32_16x16x32_bf16 v[74:77], v[196:199], v[220:223], v[74:77]
	v_mfma_f32_16x16x32_bf16 v[70:73], v[188:191], v[228:231], v[70:73]
	v_mfma_f32_16x16x32_bf16 v[66:69], v[196:199], v[228:231], v[66:69]
	v_mfma_f32_16x16x32_bf16 v[110:113], v[192:195], v[208:211], v[110:113]
	v_mfma_f32_16x16x32_bf16 v[106:109], v[200:203], v[208:211], v[106:109]
	v_mfma_f32_16x16x32_bf16 v[102:105], v[192:195], v[216:219], v[102:105]
	v_mfma_f32_16x16x32_bf16 v[98:101], v[200:203], v[216:219], v[98:101]
	v_mfma_f32_16x16x32_bf16 v[78:81], v[192:195], v[224:227], v[78:81]
	v_mfma_f32_16x16x32_bf16 v[74:77], v[200:203], v[224:227], v[74:77]
	v_mfma_f32_16x16x32_bf16 v[70:73], v[192:195], v[234:237], v[70:73]
	v_mfma_f32_16x16x32_bf16 v[66:69], v[200:203], v[234:237], v[66:69]
	s_setprio 0
	s_barrier
	s_add_i32 s8, s8, s66
	v_lshl_add_u64 v[246:247], v[240:241], 0, v[130:131]
	s_mov_b32 m0, s8
	ds_read_b128 v[204:207], v168 offset:49152
	ds_read_b128 v[208:211], v168 offset:50176
	ds_read_b128 v[212:215], v168 offset:51200
	ds_read_b128 v[216:219], v168 offset:52224
	ds_read_b128 v[220:223], v168 offset:53248
	ds_read_b128 v[224:227], v168 offset:54272
	ds_read_b128 v[228:231], v168 offset:55296
	ds_read_b128 v[234:237], v168 offset:56320
	global_load_lds_dwordx4 v[246:247], off
	v_lshl_add_u64 v[240:241], v[240:241], 0, v[132:133]
	s_add_i32 m0, s8, 0x2000
	v_lshl_add_u64 v[238:239], v[238:239], 0, s[40:41]
	s_add_i32 s8, s9, s66
	global_load_lds_dwordx4 v[240:241], off
	v_lshl_add_u64 v[240:241], v[238:239], 0, v[130:131]
	s_mov_b32 m0, s8
	v_lshl_add_u64 v[238:239], v[238:239], 0, v[132:133]
	global_load_lds_dwordx4 v[240:241], off
	s_add_i32 m0, s8, 0x2000
	s_nop 0
	global_load_lds_dwordx4 v[238:239], off
	v_lshl_add_u64 v[238:239], v[244:245], 0, s[46:47]
	s_mov_b32 m0, s76
	s_nop 0
	global_load_lds_dwordx4 v[238:239], off
	v_lshl_add_u64 v[238:239], v[242:243], 0, s[46:47]
	s_mov_b32 m0, s77
	s_nop 0
	global_load_lds_dwordx4 v[238:239], off
	s_waitcnt vmcnt(8)
	s_waitcnt lgkmcnt(0)
	s_barrier
	s_setprio 1
	v_mfma_f32_16x16x32_bf16 v[62:65], v[172:175], v[204:207], v[62:65]
	v_mfma_f32_16x16x32_bf16 v[58:61], v[180:183], v[204:207], v[58:61]
	v_mfma_f32_16x16x32_bf16 v[54:57], v[172:175], v[212:215], v[54:57]
	v_mfma_f32_16x16x32_bf16 v[50:53], v[180:183], v[212:215], v[50:53]
	v_mfma_f32_16x16x32_bf16 v[30:33], v[172:175], v[220:223], v[30:33]
	v_mfma_f32_16x16x32_bf16 v[26:29], v[180:183], v[220:223], v[26:29]
	v_mfma_f32_16x16x32_bf16 v[22:25], v[172:175], v[228:231], v[22:25]
	v_mfma_f32_16x16x32_bf16 v[18:21], v[180:183], v[228:231], v[18:21]
	v_mfma_f32_16x16x32_bf16 v[62:65], v[176:179], v[208:211], v[62:65]
	v_mfma_f32_16x16x32_bf16 v[58:61], v[184:187], v[208:211], v[58:61]
	v_mfma_f32_16x16x32_bf16 v[54:57], v[176:179], v[216:219], v[54:57]
	v_mfma_f32_16x16x32_bf16 v[50:53], v[184:187], v[216:219], v[50:53]
	v_mfma_f32_16x16x32_bf16 v[30:33], v[176:179], v[224:227], v[30:33]
	v_mfma_f32_16x16x32_bf16 v[26:29], v[184:187], v[224:227], v[26:29]
	v_mfma_f32_16x16x32_bf16 v[22:25], v[176:179], v[234:237], v[22:25]
	v_mfma_f32_16x16x32_bf16 v[18:21], v[184:187], v[234:237], v[18:21]
	s_setprio 0
	s_setprio 1
	v_mfma_f32_16x16x32_bf16 v[46:49], v[188:191], v[204:207], v[46:49]
	v_mfma_f32_16x16x32_bf16 v[42:45], v[196:199], v[204:207], v[42:45]
	v_mfma_f32_16x16x32_bf16 v[38:41], v[188:191], v[212:215], v[38:41]
	v_mfma_f32_16x16x32_bf16 v[34:37], v[196:199], v[212:215], v[34:37]
	v_mfma_f32_16x16x32_bf16 v[14:17], v[188:191], v[220:223], v[14:17]
	v_mfma_f32_16x16x32_bf16 v[10:13], v[196:199], v[220:223], v[10:13]
	v_mfma_f32_16x16x32_bf16 v[6:9], v[188:191], v[228:231], v[6:9]
	v_mfma_f32_16x16x32_bf16 v[2:5], v[196:199], v[228:231], v[2:5]
	v_mfma_f32_16x16x32_bf16 v[46:49], v[192:195], v[208:211], v[46:49]
	v_mfma_f32_16x16x32_bf16 v[42:45], v[200:203], v[208:211], v[42:45]
	v_mfma_f32_16x16x32_bf16 v[38:41], v[192:195], v[216:219], v[38:41]
	v_mfma_f32_16x16x32_bf16 v[34:37], v[200:203], v[216:219], v[34:37]
	v_mfma_f32_16x16x32_bf16 v[14:17], v[192:195], v[224:227], v[14:17]
	v_mfma_f32_16x16x32_bf16 v[10:13], v[200:203], v[224:227], v[10:13]
	v_mfma_f32_16x16x32_bf16 v[6:9], v[192:195], v[234:237], v[6:9]
	v_mfma_f32_16x16x32_bf16 v[2:5], v[200:203], v[234:237], v[2:5]
	s_setprio 0
	s_barrier
	s_add_i32 s49, s49, 2
	s_cmp_gt_u32 s49, 13
	v_lshl_add_u64 v[158:159], v[158:159], 0, s[44:45]
	s_cbranch_scc1 .LBB0_2906
	s_mov_b64 s[52:53], s[54:55]
	s_branch .LBB0_2902

.LBB0_2999:
	ds_read_b128 v[150:153], v157
	ds_read_b128 v[160:163], v157 offset:1024
	ds_read_b128 v[164:167], v157 offset:2048
	ds_read_b128 v[168:171], v157 offset:3072
	ds_read_b128 v[172:175], v158
	ds_read_b128 v[176:179], v158 offset:1024
	ds_read_b128 v[180:183], v158 offset:2048
	ds_read_b128 v[184:187], v158 offset:3072
	s_add_i32 s96, s60, 2
	s_add_u32 s61, s58, 0x4000
	s_addc_u32 s62, s59, 0
	s_cmp_eq_u32 s29, s60
	s_cselect_b32 s63, s57, s62
	s_cselect_b32 s62, s56, s61
	s_cselect_b64 vcc, -1, 0
	s_add_u32 s60, s62, 0x8000
	v_cndmask_b32_e32 v132, v130, v148, vcc
	v_cndmask_b32_e32 v133, v131, v149, vcc
	s_addc_u32 s61, s63, 0
	v_lshl_add_u64 v[220:221], s[58:59], 0, v[144:145]
	s_add_i32 m0, s75, 0xc000
	ds_read_b128 v[188:191], v159
	ds_read_b128 v[192:195], v159 offset:1024
	ds_read_b128 v[196:199], v159 offset:2048
	ds_read_b128 v[200:203], v159 offset:3072
	ds_read_b128 v[204:207], v159 offset:4096
	ds_read_b128 v[208:211], v159 offset:5120
	ds_read_b128 v[212:215], v159 offset:6144
	ds_read_b128 v[216:219], v159 offset:7168
	global_load_lds_dwordx4 v[220:221], off
	v_lshl_add_u64 v[220:221], s[58:59], 0, v[146:147]
	s_add_i32 m0, s75, 0xe000
	s_nop 0
	global_load_lds_dwordx4 v[220:221], off
	s_waitcnt vmcnt(8)
	s_waitcnt lgkmcnt(0)
	s_barrier
	s_setprio 1
	v_mfma_f32_16x16x32_bf16 v[126:129], v[150:153], v[188:191], v[126:129]
	v_mfma_f32_16x16x32_bf16 v[122:125], v[164:167], v[188:191], v[122:125]
	v_mfma_f32_16x16x32_bf16 v[118:121], v[150:153], v[196:199], v[118:121]
	v_mfma_f32_16x16x32_bf16 v[110:113], v[164:167], v[196:199], v[110:113]
	v_mfma_f32_16x16x32_bf16 v[102:105], v[150:153], v[204:207], v[102:105]
	v_mfma_f32_16x16x32_bf16 v[94:97], v[164:167], v[204:207], v[94:97]
	v_mfma_f32_16x16x32_bf16 v[86:89], v[150:153], v[212:215], v[86:89]
	v_mfma_f32_16x16x32_bf16 v[78:81], v[164:167], v[212:215], v[78:81]
	v_mfma_f32_16x16x32_bf16 v[126:129], v[160:163], v[192:195], v[126:129]
	v_mfma_f32_16x16x32_bf16 v[122:125], v[168:171], v[192:195], v[122:125]
	v_mfma_f32_16x16x32_bf16 v[118:121], v[160:163], v[200:203], v[118:121]
	v_mfma_f32_16x16x32_bf16 v[110:113], v[168:171], v[200:203], v[110:113]
	v_mfma_f32_16x16x32_bf16 v[102:105], v[160:163], v[208:211], v[102:105]
	v_mfma_f32_16x16x32_bf16 v[94:97], v[168:171], v[208:211], v[94:97]
	v_mfma_f32_16x16x32_bf16 v[86:89], v[160:163], v[216:219], v[86:89]
	v_mfma_f32_16x16x32_bf16 v[78:81], v[168:171], v[216:219], v[78:81]
	s_setprio 0
	s_setprio 1
	v_mfma_f32_16x16x32_bf16 v[114:117], v[172:175], v[188:191], v[114:117]
	v_mfma_f32_16x16x32_bf16 v[106:109], v[180:183], v[188:191], v[106:109]
	v_mfma_f32_16x16x32_bf16 v[98:101], v[172:175], v[196:199], v[98:101]
	v_mfma_f32_16x16x32_bf16 v[90:93], v[180:183], v[196:199], v[90:93]
	v_mfma_f32_16x16x32_bf16 v[82:85], v[172:175], v[204:207], v[82:85]
	v_mfma_f32_16x16x32_bf16 v[74:77], v[180:183], v[204:207], v[74:77]
	v_mfma_f32_16x16x32_bf16 v[70:73], v[172:175], v[212:215], v[70:73]
	v_mfma_f32_16x16x32_bf16 v[66:69], v[180:183], v[212:215], v[66:69]
	v_mfma_f32_16x16x32_bf16 v[114:117], v[176:179], v[192:195], v[114:117]
	v_mfma_f32_16x16x32_bf16 v[106:109], v[184:187], v[192:195], v[106:109]
	v_mfma_f32_16x16x32_bf16 v[98:101], v[176:179], v[200:203], v[98:101]
	v_mfma_f32_16x16x32_bf16 v[90:93], v[184:187], v[200:203], v[90:93]
	v_mfma_f32_16x16x32_bf16 v[82:85], v[176:179], v[208:211], v[82:85]
	v_mfma_f32_16x16x32_bf16 v[74:77], v[184:187], v[208:211], v[74:77]
	v_mfma_f32_16x16x32_bf16 v[70:73], v[176:179], v[216:219], v[70:73]
	v_mfma_f32_16x16x32_bf16 v[66:69], v[184:187], v[216:219], v[66:69]
	s_setprio 0
	s_barrier
	s_add_i32 s97, s89, s71
	v_lshl_add_u64 v[220:221], v[132:133], 0, v[136:137]
	s_mov_b32 m0, s97
	ds_read_b128 v[188:191], v159 offset:16384
	ds_read_b128 v[192:195], v159 offset:17408
	ds_read_b128 v[196:199], v159 offset:18432
	ds_read_b128 v[200:203], v159 offset:19456
	ds_read_b128 v[204:207], v159 offset:20480
	ds_read_b128 v[208:211], v159 offset:21504
	ds_read_b128 v[212:215], v159 offset:22528
	ds_read_b128 v[216:219], v159 offset:23552
	global_load_lds_dwordx4 v[220:221], off
	v_lshl_add_u64 v[220:221], v[132:133], 0, v[140:141]
	s_add_i32 m0, s97, 0x2000
	s_add_i32 s97, s90, s71
	global_load_lds_dwordx4 v[220:221], off
	v_lshl_add_u64 v[220:221], v[132:133], 0, s[12:13]
	v_lshl_add_u64 v[222:223], v[220:221], 0, v[136:137]
	s_mov_b32 m0, s97
	v_lshl_add_u64 v[220:221], v[220:221], 0, v[140:141]
	global_load_lds_dwordx4 v[222:223], off
	s_add_i32 m0, s97, 0x2000
	s_nop 0
	global_load_lds_dwordx4 v[220:221], off
	v_lshl_add_u64 v[220:221], s[62:63], 0, v[134:135]
	s_mov_b32 m0, s75
	s_nop 0
	global_load_lds_dwordx4 v[220:221], off
	v_lshl_add_u64 v[220:221], s[62:63], 0, v[138:139]
	s_mov_b32 m0, s76
	s_nop 0
	global_load_lds_dwordx4 v[220:221], off
	s_waitcnt vmcnt(8)
	s_waitcnt lgkmcnt(0)
	s_barrier
	s_setprio 1
	v_mfma_f32_16x16x32_bf16 v[62:65], v[150:153], v[188:191], v[62:65]
	v_mfma_f32_16x16x32_bf16 v[58:61], v[164:167], v[188:191], v[58:61]
	v_mfma_f32_16x16x32_bf16 v[54:57], v[150:153], v[196:199], v[54:57]
	v_mfma_f32_16x16x32_bf16 v[46:49], v[164:167], v[196:199], v[46:49]
	v_mfma_f32_16x16x32_bf16 v[38:41], v[150:153], v[204:207], v[38:41]
	v_mfma_f32_16x16x32_bf16 v[30:33], v[164:167], v[204:207], v[30:33]
	v_mfma_f32_16x16x32_bf16 v[22:25], v[150:153], v[212:215], v[22:25]
	v_mfma_f32_16x16x32_bf16 v[14:17], v[164:167], v[212:215], v[14:17]
	v_mfma_f32_16x16x32_bf16 v[62:65], v[160:163], v[192:195], v[62:65]
	v_mfma_f32_16x16x32_bf16 v[58:61], v[168:171], v[192:195], v[58:61]
	v_mfma_f32_16x16x32_bf16 v[54:57], v[160:163], v[200:203], v[54:57]
	v_mfma_f32_16x16x32_bf16 v[46:49], v[168:171], v[200:203], v[46:49]
	v_mfma_f32_16x16x32_bf16 v[38:41], v[160:163], v[208:211], v[38:41]
	v_mfma_f32_16x16x32_bf16 v[30:33], v[168:171], v[208:211], v[30:33]
	v_mfma_f32_16x16x32_bf16 v[22:25], v[160:163], v[216:219], v[22:25]
	v_mfma_f32_16x16x32_bf16 v[14:17], v[168:171], v[216:219], v[14:17]
	s_setprio 0
	s_setprio 1
	v_mfma_f32_16x16x32_bf16 v[50:53], v[172:175], v[188:191], v[50:53]
	v_mfma_f32_16x16x32_bf16 v[42:45], v[180:183], v[188:191], v[42:45]
	v_mfma_f32_16x16x32_bf16 v[34:37], v[172:175], v[196:199], v[34:37]
	v_mfma_f32_16x16x32_bf16 v[26:29], v[180:183], v[196:199], v[26:29]
	v_mfma_f32_16x16x32_bf16 v[18:21], v[172:175], v[204:207], v[18:21]
	v_mfma_f32_16x16x32_bf16 v[10:13], v[180:183], v[204:207], v[10:13]
	v_mfma_f32_16x16x32_bf16 v[6:9], v[172:175], v[212:215], v[6:9]
	v_mfma_f32_16x16x32_bf16 v[2:5], v[180:183], v[212:215], v[2:5]
	v_mfma_f32_16x16x32_bf16 v[50:53], v[176:179], v[192:195], v[50:53]
	v_mfma_f32_16x16x32_bf16 v[42:45], v[184:187], v[192:195], v[42:45]
	v_mfma_f32_16x16x32_bf16 v[34:37], v[176:179], v[200:203], v[34:37]
	v_mfma_f32_16x16x32_bf16 v[26:29], v[184:187], v[200:203], v[26:29]
	v_mfma_f32_16x16x32_bf16 v[18:21], v[176:179], v[208:211], v[18:21]
	v_mfma_f32_16x16x32_bf16 v[10:13], v[184:187], v[208:211], v[10:13]
	v_mfma_f32_16x16x32_bf16 v[6:9], v[176:179], v[216:219], v[6:9]
	v_mfma_f32_16x16x32_bf16 v[2:5], v[184:187], v[216:219], v[2:5]
	s_setprio 0
	s_barrier
	s_add_i32 s97, 0, 0x18000
	v_add_u32_e32 v142, s97, v154
	s_add_i32 vcc_lo, 0, 0x1c000
	ds_read_b128 v[150:153], v142
	ds_read_b128 v[160:163], v142 offset:1024
	ds_read_b128 v[164:167], v142 offset:2048
	ds_read_b128 v[168:171], v142 offset:3072
	v_add_u32_e32 v142, vcc_lo, v154
	ds_read_b128 v[172:175], v142
	ds_read_b128 v[176:179], v142 offset:1024
	ds_read_b128 v[180:183], v142 offset:2048
	ds_read_b128 v[184:187], v142 offset:3072
	s_add_u32 s62, s62, 0x4000
	s_addc_u32 s63, s63, 0
	s_mov_b32 m0, s77
	v_lshl_add_u64 v[220:221], s[62:63], 0, v[134:135]
	ds_read_b128 v[188:191], v159 offset:32768
	ds_read_b128 v[192:195], v159 offset:33792
	ds_read_b128 v[196:199], v159 offset:34816
	ds_read_b128 v[200:203], v159 offset:35840
	ds_read_b128 v[204:207], v159 offset:36864
	ds_read_b128 v[208:211], v159 offset:37888
	ds_read_b128 v[212:215], v159 offset:38912
	ds_read_b128 v[216:219], v159 offset:39936
	global_load_lds_dwordx4 v[220:221], off
	v_lshl_add_u64 v[220:221], s[62:63], 0, v[138:139]
	s_mov_b32 m0, s78
	s_nop 0
	global_load_lds_dwordx4 v[220:221], off
	s_waitcnt vmcnt(8)
	s_waitcnt lgkmcnt(0)
	s_barrier
	s_setprio 1
	v_mfma_f32_16x16x32_bf16 v[126:129], v[150:153], v[188:191], v[126:129]
	v_mfma_f32_16x16x32_bf16 v[122:125], v[164:167], v[188:191], v[122:125]
	v_mfma_f32_16x16x32_bf16 v[118:121], v[150:153], v[196:199], v[118:121]
	v_mfma_f32_16x16x32_bf16 v[110:113], v[164:167], v[196:199], v[110:113]
	v_mfma_f32_16x16x32_bf16 v[102:105], v[150:153], v[204:207], v[102:105]
	v_mfma_f32_16x16x32_bf16 v[94:97], v[164:167], v[204:207], v[94:97]
	v_mfma_f32_16x16x32_bf16 v[86:89], v[150:153], v[212:215], v[86:89]
	v_mfma_f32_16x16x32_bf16 v[78:81], v[164:167], v[212:215], v[78:81]
	v_mfma_f32_16x16x32_bf16 v[126:129], v[160:163], v[192:195], v[126:129]
	v_mfma_f32_16x16x32_bf16 v[122:125], v[168:171], v[192:195], v[122:125]
	v_mfma_f32_16x16x32_bf16 v[118:121], v[160:163], v[200:203], v[118:121]
	v_mfma_f32_16x16x32_bf16 v[110:113], v[168:171], v[200:203], v[110:113]
	v_mfma_f32_16x16x32_bf16 v[102:105], v[160:163], v[208:211], v[102:105]
	v_mfma_f32_16x16x32_bf16 v[94:97], v[168:171], v[208:211], v[94:97]
	v_mfma_f32_16x16x32_bf16 v[86:89], v[160:163], v[216:219], v[86:89]
	v_mfma_f32_16x16x32_bf16 v[78:81], v[168:171], v[216:219], v[78:81]
	s_setprio 0
	s_setprio 1
	v_mfma_f32_16x16x32_bf16 v[114:117], v[172:175], v[188:191], v[114:117]
	v_mfma_f32_16x16x32_bf16 v[106:109], v[180:183], v[188:191], v[106:109]
	v_mfma_f32_16x16x32_bf16 v[98:101], v[172:175], v[196:199], v[98:101]
	v_mfma_f32_16x16x32_bf16 v[90:93], v[180:183], v[196:199], v[90:93]
	v_mfma_f32_16x16x32_bf16 v[82:85], v[172:175], v[204:207], v[82:85]
	v_mfma_f32_16x16x32_bf16 v[74:77], v[180:183], v[204:207], v[74:77]
	v_mfma_f32_16x16x32_bf16 v[70:73], v[172:175], v[212:215], v[70:73]
	v_mfma_f32_16x16x32_bf16 v[66:69], v[180:183], v[212:215], v[66:69]
	v_mfma_f32_16x16x32_bf16 v[114:117], v[176:179], v[192:195], v[114:117]
	v_mfma_f32_16x16x32_bf16 v[106:109], v[184:187], v[192:195], v[106:109]
	v_mfma_f32_16x16x32_bf16 v[98:101], v[176:179], v[200:203], v[98:101]
	v_mfma_f32_16x16x32_bf16 v[90:93], v[184:187], v[200:203], v[90:93]
	v_mfma_f32_16x16x32_bf16 v[82:85], v[176:179], v[208:211], v[82:85]
	v_mfma_f32_16x16x32_bf16 v[74:77], v[184:187], v[208:211], v[74:77]
	v_mfma_f32_16x16x32_bf16 v[70:73], v[176:179], v[216:219], v[70:73]
	v_mfma_f32_16x16x32_bf16 v[66:69], v[184:187], v[216:219], v[66:69]
	s_setprio 0
	s_barrier
	v_lshl_add_u64 v[220:221], v[132:133], 0, s[20:21]
	s_add_i32 s62, s97, s71
	v_lshl_add_u64 v[222:223], v[220:221], 0, v[136:137]
	s_mov_b32 m0, s62
	ds_read_b128 v[188:191], v159 offset:49152
	ds_read_b128 v[192:195], v159 offset:50176
	ds_read_b128 v[196:199], v159 offset:51200
	ds_read_b128 v[200:203], v159 offset:52224
	ds_read_b128 v[204:207], v159 offset:53248
	ds_read_b128 v[208:211], v159 offset:54272
	ds_read_b128 v[212:215], v159 offset:55296
	ds_read_b128 v[216:219], v159 offset:56320
	global_load_lds_dwordx4 v[222:223], off
	v_lshl_add_u64 v[220:221], v[220:221], 0, v[140:141]
	s_add_i32 m0, s62, 0x2000
	v_lshl_add_u64 v[132:133], v[132:133], 0, s[22:23]
	s_add_i32 s62, vcc_lo, s71
	global_load_lds_dwordx4 v[220:221], off
	v_lshl_add_u64 v[220:221], v[132:133], 0, v[136:137]
	s_mov_b32 m0, s62
	v_lshl_add_u64 v[132:133], v[132:133], 0, v[140:141]
	global_load_lds_dwordx4 v[220:221], off
	s_add_i32 m0, s62, 0x2000
	s_nop 0
	global_load_lds_dwordx4 v[132:133], off
	v_lshl_add_u64 v[132:133], s[60:61], 0, v[134:135]
	s_mov_b32 m0, s86
	s_nop 0
	global_load_lds_dwordx4 v[132:133], off
	v_lshl_add_u64 v[132:133], s[60:61], 0, v[138:139]
	s_mov_b32 m0, s87
	s_nop 0
	global_load_lds_dwordx4 v[132:133], off
	s_waitcnt vmcnt(8)
	s_waitcnt lgkmcnt(0)
	s_barrier
	s_setprio 1
	v_mfma_f32_16x16x32_bf16 v[62:65], v[150:153], v[188:191], v[62:65]
	v_mfma_f32_16x16x32_bf16 v[58:61], v[164:167], v[188:191], v[58:61]
	v_mfma_f32_16x16x32_bf16 v[54:57], v[150:153], v[196:199], v[54:57]
	v_mfma_f32_16x16x32_bf16 v[46:49], v[164:167], v[196:199], v[46:49]
	v_mfma_f32_16x16x32_bf16 v[38:41], v[150:153], v[204:207], v[38:41]
	v_mfma_f32_16x16x32_bf16 v[30:33], v[164:167], v[204:207], v[30:33]
	v_mfma_f32_16x16x32_bf16 v[22:25], v[150:153], v[212:215], v[22:25]
	v_mfma_f32_16x16x32_bf16 v[14:17], v[164:167], v[212:215], v[14:17]
	v_mfma_f32_16x16x32_bf16 v[62:65], v[160:163], v[192:195], v[62:65]
	v_mfma_f32_16x16x32_bf16 v[58:61], v[168:171], v[192:195], v[58:61]
	v_mfma_f32_16x16x32_bf16 v[54:57], v[160:163], v[200:203], v[54:57]
	v_mfma_f32_16x16x32_bf16 v[46:49], v[168:171], v[200:203], v[46:49]
	v_mfma_f32_16x16x32_bf16 v[38:41], v[160:163], v[208:211], v[38:41]
	v_mfma_f32_16x16x32_bf16 v[30:33], v[168:171], v[208:211], v[30:33]
	v_mfma_f32_16x16x32_bf16 v[22:25], v[160:163], v[216:219], v[22:25]
	v_mfma_f32_16x16x32_bf16 v[14:17], v[168:171], v[216:219], v[14:17]
	s_setprio 0
	s_setprio 1
	v_mfma_f32_16x16x32_bf16 v[50:53], v[172:175], v[188:191], v[50:53]
	v_mfma_f32_16x16x32_bf16 v[42:45], v[180:183], v[188:191], v[42:45]
	v_mfma_f32_16x16x32_bf16 v[34:37], v[172:175], v[196:199], v[34:37]
	v_mfma_f32_16x16x32_bf16 v[26:29], v[180:183], v[196:199], v[26:29]
	v_mfma_f32_16x16x32_bf16 v[18:21], v[172:175], v[204:207], v[18:21]
	v_mfma_f32_16x16x32_bf16 v[10:13], v[180:183], v[204:207], v[10:13]
	v_mfma_f32_16x16x32_bf16 v[6:9], v[172:175], v[212:215], v[6:9]
	v_mfma_f32_16x16x32_bf16 v[2:5], v[180:183], v[212:215], v[2:5]
	v_mfma_f32_16x16x32_bf16 v[50:53], v[176:179], v[192:195], v[50:53]
	v_mfma_f32_16x16x32_bf16 v[42:45], v[184:187], v[192:195], v[42:45]
	v_mfma_f32_16x16x32_bf16 v[34:37], v[176:179], v[200:203], v[34:37]
	v_mfma_f32_16x16x32_bf16 v[26:29], v[184:187], v[200:203], v[26:29]
	v_mfma_f32_16x16x32_bf16 v[18:21], v[176:179], v[208:211], v[18:21]
	v_mfma_f32_16x16x32_bf16 v[10:13], v[184:187], v[208:211], v[10:13]
	v_mfma_f32_16x16x32_bf16 v[6:9], v[176:179], v[216:219], v[6:9]
	v_mfma_f32_16x16x32_bf16 v[2:5], v[184:187], v[216:219], v[2:5]
	s_setprio 0
	s_barrier
	s_add_u32 s58, s58, 0x10000
	s_addc_u32 s59, s59, 0
	v_lshl_add_u64 v[130:131], v[130:131], 0, s[44:45]
	s_cmp_ge_u32 s96, s28
	s_mov_b32 s60, s96
	s_cbranch_scc0 .LBB0_2999
	s_and_b64 vcc, exec, s[38:39]
	s_cbranch_vccz .LBB0_3002
	s_barrier
